# speedup vs baseline: 1.0413x; 1.0266x over previous
_Z7k_layerILi1EEvPKDF16_S1_PKfS3_S3_S3_S3_S3_S1_S1_S1_S1_S3_S3_PKhS5_PDF16_S6_PfS7_:
	s_ashr_i32 s3, s2, 1
	s_and_b32 s3, s3, -8
	s_and_b32 s16, s2, 7
	v_readfirstlane_b32 s15, v0
	s_or_b32 s12, s3, s16
	s_bfe_u32 s14, s2, 0x10003
	s_cmpk_gt_u32 s15, 0xff
	s_mov_b64 s[2:3], -1
	s_cbranch_scc0 .LBB2_17
	v_mov_b32_e32 v240, 0x64646464
	s_mov_b32 s42, 0x4010400
	s_mov_b32 s43, 0x4030402
	s_load_dwordx2 s[4:5], s[0:1], 0x80
	s_load_dwordx2 s[8:9], s[0:1], 0x0
	v_lshlrev_b32_e32 v2, 3, v0
	v_add_u32_e32 v1, 0xffffff00, v0
	v_ashrrev_i32_e32 v3, 4, v1
	v_and_b32_e32 v38, 0x78, v2
	s_lshl_b32 s17, s12, 9
	v_add_u32_e32 v2, s17, v3
	v_lshlrev_b32_e32 v4, 1, v38
	s_mov_b32 s7, 0x20000
	s_mov_b32 s6, 0x1000000
	v_lshl_or_b32 v2, v2, 8, v4
	s_waitcnt lgkmcnt(0)
	s_and_b32 s9, s9, 0xffff
	s_mov_b32 s10, s6
	s_mov_b32 s11, s7
	v_add_u32_e32 v5, 0x4000, v2
	buffer_load_dwordx4 v[10:13], v2, s[8:11], 0 offen sc1
	buffer_load_dwordx4 v[18:21], v5, s[8:11], 0 offen sc1
	v_add_u32_e32 v5, 0x1000, v2
	buffer_load_dwordx4 v[26:29], v5, s[8:11], 0 offen sc1
	v_add_u32_e32 v5, 0x2000, v2
	v_add_u32_e32 v6, 0x3000, v2
	buffer_load_dwordx4 v[30:33], v5, s[8:11], 0 offen sc1
	buffer_load_dwordx4 v[58:61], v6, s[8:11], 0 offen sc1
	v_add_u32_e32 v5, 0x5000, v2
	buffer_load_dwordx4 v[34:37], v5, s[8:11], 0 offen sc1
	v_add_u32_e32 v5, 0x6000, v2
	v_add_u32_e32 v2, 0x7000, v2
	buffer_load_dwordx4 v[62:65], v5, s[8:11], 0 offen sc1
	buffer_load_dwordx4 v[66:69], v2, s[8:11], 0 offen sc1
	s_or_b32 s2, s17, 0x80
	v_add_u32_e32 v2, s2, v3
	v_lshl_or_b32 v6, v2, 8, v4
	v_add_u32_e32 v2, 0x1000, v6
	v_add_u32_e32 v7, 0x2000, v6
	v_add_u32_e32 v8, 0x3000, v6
	buffer_load_dwordx4 v[70:73], v6, s[8:11], 0 offen sc1
	buffer_load_dwordx4 v[74:77], v2, s[8:11], 0 offen sc1
	buffer_load_dwordx4 v[14:17], v7, s[8:11], 0 offen sc1
	s_nop 0
	buffer_load_dwordx4 v[2:5], v8, s[8:11], 0 offen sc1
	v_add_u32_e32 v7, 0x4000, v6
	v_add_u32_e32 v8, 0x5000, v6
	v_add_u32_e32 v39, 0x6000, v6
	buffer_load_dwordx4 v[78:81], v7, s[8:11], 0 offen sc1
	buffer_load_dwordx4 v[82:85], v8, s[8:11], 0 offen sc1
	v_add_u32_e32 v40, 0x7000, v6
	buffer_load_dwordx4 v[22:25], v39, s[8:11], 0 offen sc1
	buffer_load_dwordx4 v[6:9], v40, s[8:11], 0 offen sc1
	v_lshlrev_b32_e32 v48, 2, v38
	v_or_b32_e32 v38, 0x1e600, v48
	s_barrier
	ds_read_b128 v[38:41], v38
	v_or_b32_e32 v42, 0x1ea00, v48
	ds_read_b128 v[42:45], v42
	v_or_b32_e32 v49, 0x1e800, v48
	v_or_b32_e32 v50, 0x1ec00, v48
	s_waitcnt lgkmcnt(1)
	v_cvt_pk_f16_f32 v46, v38, v39
	v_or_b32_e32 v38, 0x1e610, v48
	v_cvt_pk_f16_f32 v47, v40, v41
	ds_read_b128 v[38:41], v38
	v_or_b32_e32 v51, 0x1ea10, v48
	ds_read_b128 v[54:57], v49
	ds_read_b128 v[86:89], v50
	ds_read_b128 v[90:93], v51
	v_or_b32_e32 v94, 0x1e810, v48
	v_or_b32_e32 v48, 0x1ec10, v48
	s_waitcnt lgkmcnt(3)
	v_cvt_pk_f16_f32 v51, v38, v39
	s_waitcnt lgkmcnt(2)
	v_pk_fma_f32 v[38:39], v[54:55], 0, v[42:43] op_sel_hi:[1,0,1]
	v_cvt_pk_f16_f32 v52, v40, v41
	s_waitcnt lgkmcnt(1)
	v_pk_add_f32 v[38:39], v[86:87], v[38:39]
	v_pk_fma_f32 v[42:43], v[56:57], 0, v[44:45] op_sel_hi:[1,0,1]
	v_cvt_pk_f16_f32 v53, v38, v39
	ds_read_b128 v[38:41], v94
	ds_read_b128 v[94:97], v48
	v_pk_add_f32 v[42:43], v[88:89], v[42:43]
	s_movk_i32 s13, 0x110
	v_cvt_pk_f16_f32 v55, v42, v43
	s_waitcnt lgkmcnt(1)
	v_pk_fma_f32 v[38:39], v[38:39], 0, v[90:91] op_sel_hi:[1,0,1]
	s_or_b32 s20, s17, 0x100
	s_waitcnt lgkmcnt(0)
	v_pk_add_f32 v[38:39], v[94:95], v[38:39]
	s_or_b32 s18, s17, 0x180
	v_cvt_pk_f16_f32 v56, v38, v39
	v_pk_fma_f32 v[38:39], v[40:41], 0, v[92:93] op_sel_hi:[1,0,1]
	s_lshl_b32 s17, s14, 6
	v_pk_add_f32 v[38:39], v[96:97], v[38:39]
	v_mov_b32_e32 v122, 0x11000
	v_cvt_pk_f16_f32 v57, v38, v39
	v_mov_b32_e32 v38, v0
	s_and_b32 s5, s5, 0xffff
	v_add_u32_e32 v39, 0xffffff00, v38
	v_lshlrev_b32_e32 v38, 4, v38
	v_ashrrev_i32_e32 v39, 4, v39
	v_and_b32_e32 v40, 0xf0, v38
	v_mad_u64_u32 v[42:43], s[22:23], v39, s13, v[40:41]
	s_lshl_b32 s2, s2, 7
	s_or_b32 s2, s2, s17
	s_mov_b32 s3, 0
	s_lshr_b32 s19, s15, 6
	s_movk_i32 s21, 0x1000
	s_waitcnt vmcnt(15)
	v_pk_fma_f16 v12, v51, v12, v56
	v_pk_fma_f16 v10, v46, v10, v53
	v_pk_fma_f16 v13, v52, v13, v57
	v_pk_fma_f16 v11, v47, v11, v55
	s_waitcnt vmcnt(14)
	v_pk_fma_f16 v20, v51, v20, v56
	v_pk_fma_f16 v18, v46, v18, v53
	v_pk_fma_f16 v21, v52, v21, v57
	v_pk_fma_f16 v19, v47, v19, v55
	ds_write_b128 v42, v[10:13]
	ds_write_b128 v42, v[18:21] offset:17408
	v_pk_add_f16 v44, v13, v21
	v_pk_add_f16 v48, v12, v20
	v_pk_add_f16 v54, v11, v19
	v_pk_add_f16 v114, v10, v18
	s_waitcnt vmcnt(13)
	v_pk_fma_f16 v12, v51, v28, v56
	v_pk_fma_f16 v10, v46, v26, v53
	v_pk_fma_f16 v13, v52, v29, v57
	v_pk_fma_f16 v11, v47, v27, v55
	s_waitcnt vmcnt(10)
	v_pk_fma_f16 v20, v51, v36, v56
	v_pk_fma_f16 v18, v46, v34, v53
	v_pk_fma_f16 v21, v52, v37, v57
	v_pk_fma_f16 v19, v47, v35, v55
	ds_write_b128 v42, v[10:13] offset:4352
	ds_write_b128 v42, v[18:21] offset:21760
	v_pk_add_f16 v36, v13, v21
	v_pk_add_f16 v38, v12, v20
	v_pk_add_f16 v41, v11, v19
	v_pk_add_f16 v43, v10, v18
	v_pk_fma_f16 v12, v51, v32, v56
	v_pk_fma_f16 v10, v46, v30, v53
	v_pk_fma_f16 v13, v52, v33, v57
	v_pk_fma_f16 v11, v47, v31, v55
	s_waitcnt vmcnt(9)
	v_pk_fma_f16 v20, v51, v64, v56
	v_pk_fma_f16 v18, v46, v62, v53
	v_pk_fma_f16 v21, v52, v65, v57
	v_pk_fma_f16 v19, v47, v63, v55
	ds_write_b128 v42, v[10:13] offset:8704
	ds_write_b128 v42, v[18:21] offset:26112
	v_pk_add_f16 v30, v13, v21
	v_pk_add_f16 v31, v12, v20
	v_pk_add_f16 v33, v11, v19
	v_pk_add_f16 v35, v10, v18
	v_pk_fma_f16 v12, v51, v60, v56
	v_pk_fma_f16 v10, v46, v58, v53
	v_pk_fma_f16 v13, v52, v61, v57
	v_pk_fma_f16 v11, v47, v59, v55
	s_waitcnt vmcnt(8)
	v_pk_fma_f16 v18, v46, v66, v53
	v_pk_fma_f16 v20, v51, v68, v56
	v_pk_fma_f16 v21, v52, v69, v57
	v_pk_fma_f16 v19, v47, v67, v55
	ds_write_b128 v42, v[10:13] offset:13056
	ds_write_b128 v42, v[18:21] offset:30464
	v_pk_add_f16 v29, v10, v18
	v_add_u32_e32 v10, s20, v39
	v_lshl_or_b32 v18, v10, 8, v40
	v_pk_add_f16 v28, v11, v19
	v_add_u32_e32 v10, 0x1000, v18
	v_add_u32_e32 v19, 0x2000, v18
	v_pk_add_f16 v26, v13, v21
	v_pk_add_f16 v27, v12, v20
	buffer_load_dwordx4 v[60:63], v18, s[8:11], 0 offen sc1
	buffer_load_dwordx4 v[64:67], v10, s[8:11], 0 offen sc1
	v_add_u32_e32 v20, 0x3000, v18
	buffer_load_dwordx4 v[86:89], v19, s[8:11], 0 offen sc1
	buffer_load_dwordx4 v[10:13], v20, s[8:11], 0 offen sc1
	v_add_u32_e32 v19, 0x4000, v18
	v_add_u32_e32 v20, 0x5000, v18
	buffer_load_dwordx4 v[90:93], v19, s[8:11], 0 offen sc1
	buffer_load_dwordx4 v[94:97], v20, s[8:11], 0 offen sc1
	v_add_u32_e32 v32, 0x6000, v18
	v_add_u32_e32 v34, 0x7000, v18
	buffer_load_dwordx4 v[98:101], v32, s[8:11], 0 offen sc1
	buffer_load_dwordx4 v[18:21], v34, s[8:11], 0 offen sc1
	v_mov_b32_e32 v32, v0
	s_waitcnt lgkmcnt(0)
	s_barrier
	s_waitcnt vmcnt(15)
	v_pk_fma_f16 v72, v51, v72, v56
	v_add_u32_e32 v34, 0xffffff00, v32
	v_lshlrev_b32_e32 v32, 4, v32
	v_ashrrev_i32_e32 v59, 4, v34
	v_and_b32_e32 v102, 0xf0, v32
	v_pk_fma_f16 v70, v46, v70, v53
	v_pk_fma_f16 v73, v52, v73, v57
	v_pk_fma_f16 v71, v47, v71, v55
	s_waitcnt vmcnt(11)
	v_pk_fma_f16 v78, v46, v78, v53
	v_pk_fma_f16 v79, v47, v79, v55
	v_mad_u64_u32 v[104:105], s[22:23], v59, s13, v[102:103]
	v_pk_fma_f16 v80, v51, v80, v56
	v_pk_fma_f16 v81, v52, v81, v57
	ds_write_b128 v104, v[70:73] offset:34816
	ds_write_b128 v104, v[78:81] offset:52224
	v_pk_add_f16 v117, v71, v79
	v_pk_add_f16 v118, v70, v78
	v_pk_fma_f16 v70, v51, v76, v56
	v_pk_fma_f16 v68, v46, v74, v53
	v_pk_fma_f16 v71, v52, v77, v57
	v_pk_fma_f16 v69, v47, v75, v55
	v_pk_fma_f16 v16, v51, v16, v56
	v_pk_fma_f16 v14, v46, v14, v53
	v_pk_fma_f16 v17, v52, v17, v57
	v_pk_fma_f16 v15, v47, v15, v55
	v_pk_fma_f16 v4, v51, v4, v56
	v_pk_fma_f16 v2, v46, v2, v53
	v_pk_fma_f16 v5, v52, v5, v57
	v_pk_fma_f16 v3, v47, v3, v55
	s_waitcnt vmcnt(8)
	v_pk_fma_f16 v6, v46, v6, v53
	v_pk_add_f16 v115, v73, v81
	v_pk_add_f16 v116, v72, v80
	v_pk_fma_f16 v74, v51, v84, v56
	v_pk_fma_f16 v72, v46, v82, v53
	v_pk_fma_f16 v75, v52, v85, v57
	v_pk_fma_f16 v73, v47, v83, v55
	ds_write_b128 v104, v[68:71] offset:39168
	ds_write_b128 v104, v[72:75] offset:56576
	v_pk_fma_f16 v24, v51, v24, v56
	v_pk_fma_f16 v22, v46, v22, v53
	v_pk_fma_f16 v25, v52, v25, v57
	v_pk_fma_f16 v23, v47, v23, v55
	ds_write_b128 v104, v[14:17] offset:43520
	ds_write_b128 v104, v[22:25] offset:60928
	v_pk_fma_f16 v8, v51, v8, v56
	v_pk_fma_f16 v9, v52, v9, v57
	v_pk_fma_f16 v7, v47, v7, v55
	ds_write_b128 v104, v[2:5] offset:47872
	ds_write_b128 v104, v[6:9] offset:65280
	v_pk_add_f16 v39, v2, v6
	v_add_u32_e32 v2, s18, v59
	v_lshl_or_b32 v6, v2, 8, v102
	v_pk_add_f16 v34, v4, v8
	v_pk_add_f16 v37, v3, v7
	v_add_u32_e32 v2, 0x1000, v6
	v_add_u32_e32 v7, 0x2000, v6
	v_add_u32_e32 v8, 0x3000, v6
	v_pk_add_f16 v50, v71, v75
	v_pk_add_f16 v58, v70, v74
	v_pk_add_f16 v119, v69, v73
	v_pk_add_f16 v120, v68, v72
	v_pk_add_f16 v40, v17, v25
	v_pk_add_f16 v42, v16, v24
	v_pk_add_f16 v45, v15, v23
	v_pk_add_f16 v49, v14, v22
	v_pk_add_f16 v32, v5, v9
	buffer_load_dwordx4 v[68:71], v6, s[8:11], 0 offen sc1
	buffer_load_dwordx4 v[72:75], v2, s[8:11], 0 offen sc1
	buffer_load_dwordx4 v[14:17], v7, s[8:11], 0 offen sc1
	s_nop 0
	buffer_load_dwordx4 v[2:5], v8, s[8:11], 0 offen sc1
	v_add_u32_e32 v7, 0x4000, v6
	v_add_u32_e32 v8, 0x5000, v6
	v_add_u32_e32 v59, 0x6000, v6
	buffer_load_dwordx4 v[76:79], v7, s[8:11], 0 offen sc1
	buffer_load_dwordx4 v[80:83], v8, s[8:11], 0 offen sc1
	v_add_u32_e32 v84, 0x7000, v6
	buffer_load_dwordx4 v[22:25], v59, s[8:11], 0 offen sc1
	buffer_load_dwordx4 v[6:9], v84, s[8:11], 0 offen sc1
	v_mov_b32_e32 v59, v0
	s_waitcnt lgkmcnt(0)
	s_barrier
	s_lshl_b32 s8, s12, 16
	v_add_u32_e32 v85, 0xffffff00, v59
	v_lshlrev_b32_e32 v84, 3, v59
	v_lshrrev_b32_e32 v121, 4, v85
	v_and_b32_e32 v102, 56, v84
	v_lshrrev_b32_e32 v110, 3, v85
	v_ashrrev_i32_e32 v85, 3, v85
	s_movk_i32 s10, 0xffc0
	s_or_b32 s8, s8, s17
	v_lshl_or_b32 v84, v102, 1, v122
	v_bfi_b32 v85, s10, v85, v110
	s_movk_i32 s11, 0x90
	v_or_b32_e32 v106, s8, v102
	v_mad_u64_u32 v[102:103], s[8:9], v85, s11, v[84:85]
	ds_read_b128 v[102:105], v102
	v_lshlrev_b32_e32 v123, 1, v106
	v_lshrrev_b32_e32 v111, 3, v59
	v_ashrrev_i32_e32 v106, 3, v59
	v_lshl_add_u32 v85, v85, 8, v123
	v_bfi_b32 v112, s10, v106, v111
	v_mad_u64_u32 v[106:107], s[8:9], v112, s11, v[84:85]
	ds_read_b128 v[106:109], v106
	s_waitcnt lgkmcnt(1)
	buffer_store_dwordx4 v[102:105], v85, s[4:7], 0 offen sc1
	v_add_u32_e32 v85, 0x100, v59
	v_ashrrev_i32_e32 v85, 3, v85
	v_bfi_b32 v125, s10, v85, v110
	v_mad_u64_u32 v[102:103], s[8:9], v125, s11, v[84:85]
	v_add_u32_e32 v85, 0x200, v59
	v_ashrrev_i32_e32 v85, 3, v85
	v_bfi_b32 v126, s10, v85, v111
	ds_read_b128 v[102:105], v102
	v_mad_u64_u32 v[84:85], s[8:9], v126, s11, v[84:85]
	v_lshl_add_u32 v124, v112, 8, v123
	ds_read_b128 v[110:113], v84
	v_lshl_add_u32 v84, v125, 8, v123
	s_waitcnt lgkmcnt(2)
	buffer_store_dwordx4 v[106:109], v124, s[4:7], 0 offen sc1
	s_waitcnt lgkmcnt(1)
	buffer_store_dwordx4 v[102:105], v84, s[4:7], 0 offen sc1
	v_lshl_add_u32 v84, v126, 8, v123
	v_lshlrev_b32_e32 v59, 4, v59
	s_waitcnt lgkmcnt(0)
	buffer_store_dwordx4 v[110:113], v84, s[4:7], 0 offen sc1
	v_and_b32_e32 v84, 0xf0, v59
	s_waitcnt vmcnt(19)
	v_pk_fma_f16 v63, v52, v63, v57
	v_pk_fma_f16 v62, v51, v62, v56
	v_pk_fma_f16 v61, v47, v61, v55
	v_pk_fma_f16 v60, v46, v60, v53
	s_waitcnt vmcnt(15)
	v_pk_fma_f16 v93, v52, v93, v57
	v_pk_fma_f16 v92, v51, v92, v56
	v_pk_fma_f16 v91, v47, v91, v55
	v_pk_fma_f16 v90, v46, v90, v53
	v_mad_u64_u32 v[84:85], s[8:9], v121, s13, v[84:85]
	ds_write_b128 v84, v[60:63]
	ds_write_b128 v84, v[90:93] offset:17408
	v_pk_add_f16 v59, v63, v93
	v_pk_add_f16 v85, v62, v92
	v_pk_add_f16 v91, v61, v91
	v_pk_add_f16 v90, v60, v90
	v_pk_fma_f16 v63, v52, v67, v57
	v_pk_fma_f16 v62, v51, v66, v56
	v_pk_fma_f16 v61, v47, v65, v55
	v_pk_fma_f16 v60, v46, v64, v53
	s_waitcnt vmcnt(14)
	v_pk_fma_f16 v67, v52, v97, v57
	v_pk_fma_f16 v66, v51, v96, v56
	v_pk_fma_f16 v65, v47, v95, v55
	v_pk_fma_f16 v64, v46, v94, v53
	ds_write_b128 v84, v[60:63] offset:4352
	ds_write_b128 v84, v[64:67] offset:21760
	v_pk_add_f16 v92, v63, v67
	v_pk_add_f16 v93, v62, v66
	v_pk_add_f16 v94, v61, v65
	v_pk_add_f16 v95, v60, v64
	v_pk_fma_f16 v63, v52, v89, v57
	v_pk_fma_f16 v62, v51, v88, v56
	v_pk_fma_f16 v61, v47, v87, v55
	v_pk_fma_f16 v60, v46, v86, v53
	s_waitcnt vmcnt(13)
	v_pk_fma_f16 v67, v52, v101, v57
	v_pk_fma_f16 v66, v51, v100, v56
	v_pk_fma_f16 v65, v47, v99, v55
	v_pk_fma_f16 v64, v46, v98, v53
	ds_write_b128 v84, v[60:63] offset:8704
	ds_write_b128 v84, v[64:67] offset:26112
	v_pk_add_f16 v86, v63, v67
	v_pk_add_f16 v87, v62, v66
	v_pk_add_f16 v88, v61, v65
	v_pk_add_f16 v89, v60, v64
	v_pk_fma_f16 v63, v52, v13, v57
	v_pk_fma_f16 v62, v51, v12, v56
	v_pk_fma_f16 v61, v47, v11, v55
	v_pk_fma_f16 v60, v46, v10, v53
	v_mov_b32_e32 v97, v0
	s_waitcnt vmcnt(12)
	v_pk_fma_f16 v21, v52, v21, v57
	v_pk_fma_f16 v20, v51, v20, v56
	v_pk_fma_f16 v19, v47, v19, v55
	v_pk_fma_f16 v18, v46, v18, v53
	ds_write_b128 v84, v[60:63] offset:13056
	ds_write_b128 v84, v[18:21] offset:30464
	s_waitcnt lgkmcnt(0)
	s_barrier
	v_pk_add_f16 v96, v60, v18
	v_add_u32_e32 v13, 0xffffff00, v97
	v_lshlrev_b32_e32 v12, 3, v97
	v_lshrrev_b32_e32 v98, 4, v13
	v_and_b32_e32 v18, 56, v12
	v_lshrrev_b32_e32 v64, 3, v13
	v_ashrrev_i32_e32 v13, 3, v13
	v_lshl_or_b32 v12, v18, 1, v122
	v_bfi_b32 v13, s10, v13, v64
	v_pk_add_f16 v84, v61, v19
	v_or_b32_e32 v60, s2, v18
	v_mad_u64_u32 v[18:19], s[8:9], v13, s11, v[12:13]
	v_pk_add_f16 v10, v63, v21
	v_pk_add_f16 v11, v62, v20
	ds_read_b128 v[18:21], v18 offset:18432
	v_lshlrev_b32_e32 v99, 1, v60
	v_lshrrev_b32_e32 v65, 3, v97
	v_ashrrev_i32_e32 v60, 3, v97
	v_lshl_add_u32 v13, v13, 8, v99
	v_bfi_b32 v66, s10, v60, v65
	v_mad_u64_u32 v[60:61], s[8:9], v66, s11, v[12:13]
	ds_read_b128 v[60:63], v60 offset:18432
	s_waitcnt lgkmcnt(1)
	buffer_store_dwordx4 v[18:21], v13, s[4:7], 0 offen sc1
	v_add_u32_e32 v13, 0x100, v97
	v_ashrrev_i32_e32 v13, 3, v13
	v_bfi_b32 v101, s10, v13, v64
	v_mad_u64_u32 v[18:19], s[8:9], v101, s11, v[12:13]
	v_add_u32_e32 v13, 0x200, v97
	v_ashrrev_i32_e32 v13, 3, v13
	v_bfi_b32 v102, s10, v13, v65
	ds_read_b128 v[18:21], v18 offset:18432
	v_mad_u64_u32 v[12:13], s[8:9], v102, s11, v[12:13]
	v_lshl_add_u32 v100, v66, 8, v99
	ds_read_b128 v[64:67], v12 offset:18432
	v_lshl_add_u32 v12, v101, 8, v99
	s_waitcnt lgkmcnt(2)
	buffer_store_dwordx4 v[60:63], v100, s[4:7], 0 offen sc1
	s_waitcnt lgkmcnt(1)
	buffer_store_dwordx4 v[18:21], v12, s[4:7], 0 offen sc1
	v_lshl_add_u32 v12, v102, 8, v99
	s_waitcnt lgkmcnt(0)
	buffer_store_dwordx4 v[64:67], v12, s[4:7], 0 offen sc1
	v_lshlrev_b32_e32 v12, 4, v97
	v_and_b32_e32 v12, 0xf0, v12
	s_waitcnt vmcnt(15)
	v_pk_fma_f16 v21, v52, v71, v57
	v_pk_fma_f16 v20, v51, v70, v56
	v_pk_fma_f16 v19, v47, v69, v55
	v_pk_fma_f16 v18, v46, v68, v53
	s_waitcnt vmcnt(11)
	v_pk_fma_f16 v63, v52, v79, v57
	v_pk_fma_f16 v62, v51, v78, v56
	v_pk_fma_f16 v61, v47, v77, v55
	v_pk_fma_f16 v60, v46, v76, v53
	v_mad_u64_u32 v[12:13], s[8:9], v98, s13, v[12:13]
	ds_write_b128 v12, v[18:21] offset:34816
	ds_write_b128 v12, v[60:63] offset:52224
	v_pk_add_f16 v13, v21, v63
	v_pk_add_f16 v64, v20, v62
	v_pk_add_f16 v65, v19, v61
	v_pk_add_f16 v66, v18, v60
	v_pk_fma_f16 v21, v52, v75, v57
	v_pk_fma_f16 v20, v51, v74, v56
	v_pk_fma_f16 v19, v47, v73, v55
	v_pk_fma_f16 v18, v46, v72, v53
	s_waitcnt vmcnt(10)
	v_pk_fma_f16 v63, v52, v83, v57
	v_pk_fma_f16 v62, v51, v82, v56
	v_pk_fma_f16 v61, v47, v81, v55
	v_pk_fma_f16 v60, v46, v80, v53
	v_pk_fma_f16 v17, v52, v17, v57
	v_pk_fma_f16 v16, v51, v16, v56
	v_pk_fma_f16 v15, v47, v15, v55
	v_pk_fma_f16 v14, v46, v14, v53
	v_pk_fma_f16 v5, v52, v5, v57
	v_pk_fma_f16 v4, v51, v4, v56
	v_pk_fma_f16 v3, v47, v3, v55
	v_pk_fma_f16 v2, v46, v2, v53
	s_waitcnt vmcnt(8)
	v_pk_fma_f16 v7, v47, v7, v55
	v_pk_fma_f16 v6, v46, v6, v53
	ds_write_b128 v12, v[18:21] offset:39168
	ds_write_b128 v12, v[60:63] offset:56576
	v_pk_add_f16 v63, v21, v63
	v_pk_add_f16 v62, v20, v62
	v_pk_add_f16 v61, v19, v61
	v_pk_add_f16 v60, v18, v60
	v_pk_fma_f16 v21, v52, v25, v57
	v_pk_fma_f16 v20, v51, v24, v56
	v_pk_fma_f16 v19, v47, v23, v55
	v_pk_fma_f16 v18, v46, v22, v53
	ds_write_b128 v12, v[14:17] offset:43520
	ds_write_b128 v12, v[18:21] offset:60928
	v_pk_fma_f16 v9, v52, v9, v57
	v_pk_fma_f16 v8, v51, v8, v56
	ds_write_b128 v12, v[2:5] offset:47872
	ds_write_b128 v12, v[6:9] offset:65280
	v_pk_add_f16 v24, v3, v7
	v_pk_add_f16 v25, v2, v6
	v_cvt_f32_f16_e32 v2, v114
	v_cvt_f32_f16_sdwa v3, v114 dst_sel:DWORD dst_unused:UNUSED_PAD src0_sel:WORD_1
	v_pk_add_f16 v22, v5, v9
	v_pk_add_f16 v23, v4, v8
	v_cvt_f32_f16_e32 v4, v118
	v_cvt_f32_f16_sdwa v5, v118 dst_sel:DWORD dst_unused:UNUSED_PAD src0_sel:WORD_1
	v_cvt_f32_f16_e32 v6, v90
	v_cvt_f32_f16_sdwa v7, v90 dst_sel:DWORD dst_unused:UNUSED_PAD src0_sel:WORD_1
	v_cvt_f32_f16_e32 v8, v66
	v_cvt_f32_f16_sdwa v9, v66 dst_sel:DWORD dst_unused:UNUSED_PAD src0_sel:WORD_1
	v_pk_add_f32 v[2:3], v[2:3], 0 op_sel_hi:[1,0]
	v_pk_add_f16 v19, v15, v19
	v_pk_add_f32 v[2:3], v[2:3], v[4:5]
	v_cvt_f32_f16_e32 v4, v54
	v_cvt_f32_f16_sdwa v5, v54 dst_sel:DWORD dst_unused:UNUSED_PAD src0_sel:WORD_1
	v_pk_add_f32 v[2:3], v[2:3], v[6:7]
	v_cvt_f32_f16_e32 v6, v117
	v_cvt_f32_f16_sdwa v7, v117 dst_sel:DWORD dst_unused:UNUSED_PAD src0_sel:WORD_1
	v_pk_add_f32 v[2:3], v[2:3], v[8:9]
	v_cvt_f32_f16_e32 v8, v91
	v_cvt_f32_f16_sdwa v9, v91 dst_sel:DWORD dst_unused:UNUSED_PAD src0_sel:WORD_1
	v_pk_add_f16 v18, v14, v18
	v_cvt_f32_f16_e32 v14, v65
	v_cvt_f32_f16_sdwa v15, v65 dst_sel:DWORD dst_unused:UNUSED_PAD src0_sel:WORD_1
	v_pk_add_f32 v[4:5], v[4:5], 0 op_sel_hi:[1,0]
	s_mov_b32 s2, 0x3e000000
	v_pk_add_f32 v[4:5], v[4:5], v[6:7]
	v_pk_mul_f32 v[2:3], v[2:3], s[2:3] op_sel_hi:[1,0]
	v_pk_add_f32 v[4:5], v[4:5], v[8:9]
	v_cvt_pk_f16_f32 v2, v2, v3
	v_pk_add_f32 v[4:5], v[4:5], v[14:15]
	v_cvt_f32_f16_e32 v6, v116
	v_pk_mul_f32 v[4:5], v[4:5], s[2:3] op_sel_hi:[1,0]
	v_cvt_f32_f16_sdwa v7, v116 dst_sel:DWORD dst_unused:UNUSED_PAD src0_sel:WORD_1
	v_cvt_pk_f16_f32 v3, v4, v5
	v_cvt_f32_f16_e32 v4, v48
	v_cvt_f32_f16_sdwa v5, v48 dst_sel:DWORD dst_unused:UNUSED_PAD src0_sel:WORD_1
	v_cvt_f32_f16_e32 v8, v85
	v_cvt_f32_f16_sdwa v9, v85 dst_sel:DWORD dst_unused:UNUSED_PAD src0_sel:WORD_1
	v_cvt_f32_f16_e32 v14, v64
	v_cvt_f32_f16_sdwa v15, v64 dst_sel:DWORD dst_unused:UNUSED_PAD src0_sel:WORD_1
	v_pk_add_f32 v[4:5], v[4:5], 0 op_sel_hi:[1,0]
	v_pk_add_f16 v21, v17, v21
	v_pk_add_f32 v[4:5], v[4:5], v[6:7]
	v_cvt_f32_f16_e32 v6, v44
	v_cvt_f32_f16_sdwa v7, v44 dst_sel:DWORD dst_unused:UNUSED_PAD src0_sel:WORD_1
	v_pk_add_f32 v[4:5], v[4:5], v[8:9]
	v_cvt_f32_f16_e32 v8, v115
	v_cvt_f32_f16_sdwa v9, v115 dst_sel:DWORD dst_unused:UNUSED_PAD src0_sel:WORD_1
	v_pk_add_f32 v[4:5], v[4:5], v[14:15]
	v_cvt_f32_f16_e32 v14, v59
	v_cvt_f32_f16_sdwa v15, v59 dst_sel:DWORD dst_unused:UNUSED_PAD src0_sel:WORD_1
	v_pk_add_f16 v20, v16, v20
	v_cvt_f32_f16_e32 v16, v13
	v_cvt_f32_f16_sdwa v17, v13 dst_sel:DWORD dst_unused:UNUSED_PAD src0_sel:WORD_1
	v_pk_add_f32 v[6:7], v[6:7], 0 op_sel_hi:[1,0]
	v_pk_mul_f32 v[4:5], v[4:5], s[2:3] op_sel_hi:[1,0]
	v_pk_add_f32 v[6:7], v[6:7], v[8:9]
	v_cvt_pk_f16_f32 v4, v4, v5
	v_pk_add_f32 v[6:7], v[6:7], v[14:15]
	v_cvt_f32_f16_e32 v8, v60
	v_pk_add_f32 v[6:7], v[6:7], v[16:17]
	v_add_u32_e32 v16, 0x1a000, v12
	v_pk_mul_f32 v[6:7], v[6:7], s[2:3] op_sel_hi:[1,0]
	v_cvt_f32_f16_sdwa v9, v60 dst_sel:DWORD dst_unused:UNUSED_PAD src0_sel:WORD_1
	v_cvt_pk_f16_f32 v5, v6, v7
	ds_write_b128 v16, v[2:5]
	v_cvt_f32_f16_e32 v2, v43
	v_cvt_f32_f16_sdwa v3, v43 dst_sel:DWORD dst_unused:UNUSED_PAD src0_sel:WORD_1
	v_cvt_f32_f16_e32 v4, v120
	v_cvt_f32_f16_sdwa v5, v120 dst_sel:DWORD dst_unused:UNUSED_PAD src0_sel:WORD_1
	v_cvt_f32_f16_e32 v6, v95
	v_cvt_f32_f16_sdwa v7, v95 dst_sel:DWORD dst_unused:UNUSED_PAD src0_sel:WORD_1
	v_pk_add_f32 v[2:3], v[2:3], 0 op_sel_hi:[1,0]
	v_cvt_f32_f16_e32 v12, v61
	v_pk_add_f32 v[2:3], v[2:3], v[4:5]
	v_cvt_f32_f16_e32 v4, v41
	v_cvt_f32_f16_sdwa v5, v41 dst_sel:DWORD dst_unused:UNUSED_PAD src0_sel:WORD_1
	v_pk_add_f32 v[2:3], v[2:3], v[6:7]
	v_cvt_f32_f16_e32 v6, v119
	v_cvt_f32_f16_sdwa v7, v119 dst_sel:DWORD dst_unused:UNUSED_PAD src0_sel:WORD_1
	v_pk_add_f32 v[2:3], v[2:3], v[8:9]
	v_cvt_f32_f16_e32 v8, v94
	v_cvt_f32_f16_sdwa v9, v94 dst_sel:DWORD dst_unused:UNUSED_PAD src0_sel:WORD_1
	v_cvt_f32_f16_sdwa v13, v61 dst_sel:DWORD dst_unused:UNUSED_PAD src0_sel:WORD_1
	v_pk_add_f32 v[4:5], v[4:5], 0 op_sel_hi:[1,0]
	v_pk_mul_f32 v[2:3], v[2:3], s[2:3] op_sel_hi:[1,0]
	v_pk_add_f32 v[4:5], v[4:5], v[6:7]
	v_cvt_pk_f16_f32 v2, v2, v3
	v_pk_add_f32 v[4:5], v[4:5], v[8:9]
	v_cvt_f32_f16_e32 v6, v58
	v_pk_add_f32 v[4:5], v[4:5], v[12:13]
	v_cvt_f32_f16_sdwa v7, v58 dst_sel:DWORD dst_unused:UNUSED_PAD src0_sel:WORD_1
	v_pk_mul_f32 v[4:5], v[4:5], s[2:3] op_sel_hi:[1,0]
	v_cvt_f32_f16_e32 v8, v93
	v_cvt_pk_f16_f32 v3, v4, v5
	v_cvt_f32_f16_e32 v4, v38
	v_cvt_f32_f16_sdwa v5, v38 dst_sel:DWORD dst_unused:UNUSED_PAD src0_sel:WORD_1
	v_cvt_f32_f16_sdwa v9, v93 dst_sel:DWORD dst_unused:UNUSED_PAD src0_sel:WORD_1
	v_cvt_f32_f16_e32 v12, v62
	v_cvt_f32_f16_sdwa v13, v62 dst_sel:DWORD dst_unused:UNUSED_PAD src0_sel:WORD_1
	v_pk_add_f32 v[4:5], v[4:5], 0 op_sel_hi:[1,0]
	v_cvt_f32_f16_e32 v14, v63
	v_pk_add_f32 v[4:5], v[4:5], v[6:7]
	v_cvt_f32_f16_e32 v6, v36
	v_cvt_f32_f16_sdwa v7, v36 dst_sel:DWORD dst_unused:UNUSED_PAD src0_sel:WORD_1
	v_pk_add_f32 v[4:5], v[4:5], v[8:9]
	v_cvt_f32_f16_e32 v8, v50
	v_cvt_f32_f16_sdwa v9, v50 dst_sel:DWORD dst_unused:UNUSED_PAD src0_sel:WORD_1
	v_pk_add_f32 v[4:5], v[4:5], v[12:13]
	v_cvt_f32_f16_e32 v12, v92
	v_cvt_f32_f16_sdwa v13, v92 dst_sel:DWORD dst_unused:UNUSED_PAD src0_sel:WORD_1
	v_cvt_f32_f16_sdwa v15, v63 dst_sel:DWORD dst_unused:UNUSED_PAD src0_sel:WORD_1
	v_pk_add_f32 v[6:7], v[6:7], 0 op_sel_hi:[1,0]
	v_pk_mul_f32 v[4:5], v[4:5], s[2:3] op_sel_hi:[1,0]
	v_pk_add_f32 v[6:7], v[6:7], v[8:9]
	v_cvt_pk_f16_f32 v4, v4, v5
	v_pk_add_f32 v[6:7], v[6:7], v[12:13]
	v_cvt_f32_f16_e32 v8, v18
	v_pk_add_f32 v[6:7], v[6:7], v[14:15]
	v_cvt_f32_f16_sdwa v9, v18 dst_sel:DWORD dst_unused:UNUSED_PAD src0_sel:WORD_1
	v_pk_mul_f32 v[6:7], v[6:7], s[2:3] op_sel_hi:[1,0]
	v_cvt_f32_f16_e32 v12, v19
	v_cvt_pk_f16_f32 v5, v6, v7
	ds_write_b128 v16, v[2:5] offset:4352
	v_cvt_f32_f16_e32 v2, v35
	v_cvt_f32_f16_sdwa v3, v35 dst_sel:DWORD dst_unused:UNUSED_PAD src0_sel:WORD_1
	v_cvt_f32_f16_e32 v4, v49
	v_cvt_f32_f16_sdwa v5, v49 dst_sel:DWORD dst_unused:UNUSED_PAD src0_sel:WORD_1
	v_cvt_f32_f16_e32 v6, v89
	v_cvt_f32_f16_sdwa v7, v89 dst_sel:DWORD dst_unused:UNUSED_PAD src0_sel:WORD_1
	v_pk_add_f32 v[2:3], v[2:3], 0 op_sel_hi:[1,0]
	v_cvt_f32_f16_sdwa v13, v19 dst_sel:DWORD dst_unused:UNUSED_PAD src0_sel:WORD_1
	v_pk_add_f32 v[2:3], v[2:3], v[4:5]
	v_cvt_f32_f16_e32 v4, v33
	v_cvt_f32_f16_sdwa v5, v33 dst_sel:DWORD dst_unused:UNUSED_PAD src0_sel:WORD_1
	v_pk_add_f32 v[2:3], v[2:3], v[6:7]
	v_cvt_f32_f16_e32 v6, v45
	v_cvt_f32_f16_sdwa v7, v45 dst_sel:DWORD dst_unused:UNUSED_PAD src0_sel:WORD_1
	v_pk_add_f32 v[2:3], v[2:3], v[8:9]
	v_cvt_f32_f16_e32 v8, v88
	v_cvt_f32_f16_sdwa v9, v88 dst_sel:DWORD dst_unused:UNUSED_PAD src0_sel:WORD_1
	v_pk_add_f32 v[4:5], v[4:5], 0 op_sel_hi:[1,0]
	v_pk_mul_f32 v[2:3], v[2:3], s[2:3] op_sel_hi:[1,0]
	v_pk_add_f32 v[4:5], v[4:5], v[6:7]
	v_cvt_pk_f16_f32 v2, v2, v3
	v_pk_add_f32 v[4:5], v[4:5], v[8:9]
	v_cvt_f32_f16_e32 v6, v42
	v_pk_add_f32 v[4:5], v[4:5], v[12:13]
	v_cvt_f32_f16_sdwa v7, v42 dst_sel:DWORD dst_unused:UNUSED_PAD src0_sel:WORD_1
	v_pk_mul_f32 v[4:5], v[4:5], s[2:3] op_sel_hi:[1,0]
	v_cvt_f32_f16_e32 v8, v87
	v_cvt_pk_f16_f32 v3, v4, v5
	v_cvt_f32_f16_e32 v4, v31
	v_cvt_f32_f16_sdwa v5, v31 dst_sel:DWORD dst_unused:UNUSED_PAD src0_sel:WORD_1
	v_cvt_f32_f16_sdwa v9, v87 dst_sel:DWORD dst_unused:UNUSED_PAD src0_sel:WORD_1
	v_cvt_f32_f16_e32 v12, v20
	v_cvt_f32_f16_sdwa v13, v20 dst_sel:DWORD dst_unused:UNUSED_PAD src0_sel:WORD_1
	v_pk_add_f32 v[4:5], v[4:5], 0 op_sel_hi:[1,0]
	v_cvt_f32_f16_e32 v14, v21
	v_pk_add_f32 v[4:5], v[4:5], v[6:7]
	v_cvt_f32_f16_e32 v6, v30
	v_cvt_f32_f16_sdwa v7, v30 dst_sel:DWORD dst_unused:UNUSED_PAD src0_sel:WORD_1
	v_pk_add_f32 v[4:5], v[4:5], v[8:9]
	v_cvt_f32_f16_e32 v8, v40
	v_cvt_f32_f16_sdwa v9, v40 dst_sel:DWORD dst_unused:UNUSED_PAD src0_sel:WORD_1
	v_pk_add_f32 v[4:5], v[4:5], v[12:13]
	v_cvt_f32_f16_e32 v12, v86
	v_cvt_f32_f16_sdwa v13, v86 dst_sel:DWORD dst_unused:UNUSED_PAD src0_sel:WORD_1
	v_cvt_f32_f16_sdwa v15, v21 dst_sel:DWORD dst_unused:UNUSED_PAD src0_sel:WORD_1
	v_pk_add_f32 v[6:7], v[6:7], 0 op_sel_hi:[1,0]
	v_pk_mul_f32 v[4:5], v[4:5], s[2:3] op_sel_hi:[1,0]
	v_pk_add_f32 v[6:7], v[6:7], v[8:9]
	v_cvt_pk_f16_f32 v4, v4, v5
	v_pk_add_f32 v[6:7], v[6:7], v[12:13]
	v_cvt_f32_f16_e32 v8, v25
	v_pk_add_f32 v[6:7], v[6:7], v[14:15]
	v_cvt_f32_f16_sdwa v9, v25 dst_sel:DWORD dst_unused:UNUSED_PAD src0_sel:WORD_1
	v_pk_mul_f32 v[6:7], v[6:7], s[2:3] op_sel_hi:[1,0]
	v_cvt_f32_f16_e32 v12, v24
	v_cvt_pk_f16_f32 v5, v6, v7
	ds_write_b128 v16, v[2:5] offset:8704
	v_cvt_f32_f16_e32 v2, v29
	v_cvt_f32_f16_sdwa v3, v29 dst_sel:DWORD dst_unused:UNUSED_PAD src0_sel:WORD_1
	v_cvt_f32_f16_e32 v4, v39
	v_cvt_f32_f16_sdwa v5, v39 dst_sel:DWORD dst_unused:UNUSED_PAD src0_sel:WORD_1
	v_cvt_f32_f16_e32 v6, v96
	v_cvt_f32_f16_sdwa v7, v96 dst_sel:DWORD dst_unused:UNUSED_PAD src0_sel:WORD_1
	v_pk_add_f32 v[2:3], v[2:3], 0 op_sel_hi:[1,0]
	v_cvt_f32_f16_sdwa v13, v24 dst_sel:DWORD dst_unused:UNUSED_PAD src0_sel:WORD_1
	v_pk_add_f32 v[2:3], v[2:3], v[4:5]
	v_cvt_f32_f16_e32 v4, v28
	v_cvt_f32_f16_sdwa v5, v28 dst_sel:DWORD dst_unused:UNUSED_PAD src0_sel:WORD_1
	v_pk_add_f32 v[2:3], v[2:3], v[6:7]
	v_cvt_f32_f16_e32 v6, v37
	v_cvt_f32_f16_sdwa v7, v37 dst_sel:DWORD dst_unused:UNUSED_PAD src0_sel:WORD_1
	v_pk_add_f32 v[2:3], v[2:3], v[8:9]
	v_cvt_f32_f16_e32 v8, v84
	v_cvt_f32_f16_sdwa v9, v84 dst_sel:DWORD dst_unused:UNUSED_PAD src0_sel:WORD_1
	v_pk_add_f32 v[4:5], v[4:5], 0 op_sel_hi:[1,0]
	v_pk_mul_f32 v[2:3], v[2:3], s[2:3] op_sel_hi:[1,0]
	v_pk_add_f32 v[4:5], v[4:5], v[6:7]
	v_cvt_pk_f16_f32 v2, v2, v3
	v_pk_add_f32 v[4:5], v[4:5], v[8:9]
	v_cvt_f32_f16_e32 v6, v34
	v_pk_add_f32 v[4:5], v[4:5], v[12:13]
	v_cvt_f32_f16_sdwa v7, v34 dst_sel:DWORD dst_unused:UNUSED_PAD src0_sel:WORD_1
	v_pk_mul_f32 v[4:5], v[4:5], s[2:3] op_sel_hi:[1,0]
	v_cvt_f32_f16_e32 v8, v11
	v_cvt_pk_f16_f32 v3, v4, v5
	v_cvt_f32_f16_e32 v4, v27
	v_cvt_f32_f16_sdwa v5, v27 dst_sel:DWORD dst_unused:UNUSED_PAD src0_sel:WORD_1
	v_cvt_f32_f16_sdwa v9, v11 dst_sel:DWORD dst_unused:UNUSED_PAD src0_sel:WORD_1
	v_cvt_f32_f16_e32 v12, v23
	v_cvt_f32_f16_sdwa v13, v23 dst_sel:DWORD dst_unused:UNUSED_PAD src0_sel:WORD_1
	v_pk_add_f32 v[4:5], v[4:5], 0 op_sel_hi:[1,0]
	v_cvt_f32_f16_sdwa v11, v22 dst_sel:DWORD dst_unused:UNUSED_PAD src0_sel:WORD_1
	v_pk_add_f32 v[4:5], v[4:5], v[6:7]
	v_cvt_f32_f16_e32 v6, v26
	v_cvt_f32_f16_sdwa v7, v26 dst_sel:DWORD dst_unused:UNUSED_PAD src0_sel:WORD_1
	v_pk_add_f32 v[4:5], v[4:5], v[8:9]
	v_cvt_f32_f16_e32 v8, v32
	v_cvt_f32_f16_sdwa v9, v32 dst_sel:DWORD dst_unused:UNUSED_PAD src0_sel:WORD_1
	v_pk_add_f32 v[4:5], v[4:5], v[12:13]
	v_cvt_f32_f16_e32 v12, v10
	v_cvt_f32_f16_sdwa v13, v10 dst_sel:DWORD dst_unused:UNUSED_PAD src0_sel:WORD_1
	v_cvt_f32_f16_e32 v10, v22
	v_pk_add_f32 v[6:7], v[6:7], 0 op_sel_hi:[1,0]
	v_pk_mul_f32 v[4:5], v[4:5], s[2:3] op_sel_hi:[1,0]
	v_pk_add_f32 v[6:7], v[6:7], v[8:9]
	s_cmpk_lt_u32 s15, 0x180
	v_pk_add_f32 v[6:7], v[6:7], v[12:13]
	v_cvt_pk_f16_f32 v4, v4, v5
	v_pk_add_f32 v[6:7], v[6:7], v[10:11]
	s_cselect_b64 s[8:9], -1, 0
	v_pk_mul_f32 v[6:7], v[6:7], s[2:3] op_sel_hi:[1,0]
	s_cmpk_gt_u32 s15, 0x17f
	v_cvt_pk_f16_f32 v5, v6, v7
	ds_write_b128 v16, v[2:5] offset:13056
	s_cbranch_scc1 .LBB2_3
	s_load_dwordx2 s[10:11], s[0:1], 0x78
	s_load_dwordx4 s[24:27], s[0:1], 0x50
	v_mov_b32_e32 v2, v0
	s_ashr_i32 s13, s12, 31
	s_lshl_b64 s[22:23], s[12:13], 12
	s_waitcnt lgkmcnt(0)
	s_add_u32 s10, s10, s22
	v_lshlrev_b32_e32 v2, 3, v2
	s_addc_u32 s11, s11, s23
	v_and_b32_e32 v2, 0x1f8, v2
	global_load_dwordx2 v[136:137], v2, s[10:11]
	global_load_dwordx2 v[132:133], v2, s[10:11] offset:512
	global_load_dwordx2 v[128:129], v2, s[10:11] offset:1024
	global_load_dwordx2 v[124:125], v2, s[10:11] offset:1536
	global_load_dwordx2 v[134:135], v2, s[10:11] offset:2048
	global_load_dwordx2 v[130:131], v2, s[10:11] offset:2560
	global_load_dwordx2 v[126:127], v2, s[10:11] offset:3072
	global_load_dwordx2 v[122:123], v2, s[10:11] offset:3584
	s_lshl_b32 s2, s14, 4
	s_lshl_b32 s10, s19, 3
	s_add_i32 s10, s10, s2
	s_sub_i32 s2, s10, 32
	s_lshl_b64 s[2:3], s[2:3], 10
	v_lshl_or_b32 v2, v2, 1, s2
	v_mov_b32_e32 v3, s3
	v_lshl_add_u64 v[4:5], s[24:25], 0, v[2:3]
	global_load_dwordx4 v[18:21], v[4:5], off
	global_load_dwordx4 v[102:105], v[4:5], off offset:1024
	global_load_dwordx4 v[94:97], v[4:5], off offset:2048
	global_load_dwordx4 v[86:89], v[4:5], off offset:3072
	v_add_co_u32_e32 v4, vcc, s21, v4
	v_lshl_add_u64 v[6:7], s[26:27], 0, v[2:3]
	s_nop 0
	v_addc_co_u32_e32 v5, vcc, 0, v5, vcc
	global_load_dwordx4 v[78:81], v[4:5], off
	global_load_dwordx4 v[74:77], v[4:5], off offset:1024
	global_load_dwordx4 v[70:73], v[4:5], off offset:2048
	global_load_dwordx4 v[66:69], v[4:5], off offset:3072
	s_nop 0
	global_load_dwordx4 v[2:5], v[6:7], off
	global_load_dwordx4 v[118:121], v[6:7], off offset:1024
	global_load_dwordx4 v[114:117], v[6:7], off offset:2048
	global_load_dwordx4 v[110:113], v[6:7], off offset:3072
	v_add_co_u32_e32 v6, vcc, s21, v6
	s_nop 1
	v_addc_co_u32_e32 v7, vcc, 0, v7, vcc
	global_load_dwordx4 v[106:109], v[6:7], off
	global_load_dwordx4 v[98:101], v[6:7], off offset:1024
	global_load_dwordx4 v[90:93], v[6:7], off offset:2048
	global_load_dwordx4 v[82:85], v[6:7], off offset:3072
	s_branch .LBB2_4

.LBB2_6:
	s_load_dwordx2 s[2:3], s[0:1], 0x90
	s_andn2_b64 vcc, exec, s[8:9]
	s_cbranch_vccnz .LBB2_10
	v_mov_b32_e32 v154, v0
	s_mov_b32 s8, 0x1a000
	v_and_b32_e32 v155, 31, v154
	v_bfe_u32 v156, v154, 5, 1
	v_mul_u32_u24_e32 v6, 0x110, v155
	v_lshlrev_b32_e32 v7, 4, v156
	v_add3_u32 v157, v6, v7, s8
	ds_read_b128 v[6:9], v157
	ds_read_b128 v[22:25], v157 offset:8704
	ds_read_b128 v[138:141], v157 offset:32
	ds_read_b128 v[142:145], v157 offset:8736
	s_mov_b32 s13, 0xc060c00
	s_waitcnt vmcnt(7) lgkmcnt(0)
	v_mfma_f32_32x32x16_f16 v[50:65], v[6:9], v[2:5], 0
	s_load_dwordx2 s[10:11], s[0:1], 0x68
	s_mov_b32 s20, 0xe400
	s_lshl_b32 s19, s19, 5
	s_add_i32 s19, s19, s17
	s_addk_i32 s19, 0xff80
	s_load_dwordx2 s[8:9], s[0:1], 0x88
	s_waitcnt lgkmcnt(0)
	s_and_b32 s9, s9, 0xffff
	v_mfma_f32_32x32x16_f16 v[34:49], v[22:25], v[2:5], 0
	v_mfma_f32_32x32x16_f16 v[2:17], v[6:9], v[18:21], 0
	v_mfma_f32_32x32x16_f16 v[18:33], v[22:25], v[18:21], 0
	ds_read_b128 v[146:149], v157 offset:64
	ds_read_b128 v[150:153], v157 offset:8768
	s_waitcnt vmcnt(6)
	v_mfma_f32_32x32x16_f16 v[50:65], v[138:141], v[118:121], v[50:65]
	v_mfma_f32_32x32x16_f16 v[34:49], v[142:145], v[118:121], v[34:49]
	v_mfma_f32_32x32x16_f16 v[2:17], v[138:141], v[102:105], v[2:17]
	v_mfma_f32_32x32x16_f16 v[18:33], v[142:145], v[102:105], v[18:33]
	ds_read_b128 v[102:105], v157 offset:96
	ds_read_b128 v[118:121], v157 offset:8800
	s_waitcnt vmcnt(5) lgkmcnt(3)
	v_mfma_f32_32x32x16_f16 v[50:65], v[146:149], v[114:117], v[50:65]
	s_waitcnt lgkmcnt(2)
	v_mfma_f32_32x32x16_f16 v[34:49], v[150:153], v[114:117], v[34:49]
	v_mfma_f32_32x32x16_f16 v[2:17], v[146:149], v[94:97], v[2:17]
	v_mfma_f32_32x32x16_f16 v[18:33], v[150:153], v[94:97], v[18:33]
	ds_read_b128 v[94:97], v157 offset:128
	ds_read_b128 v[114:117], v157 offset:8832
	s_waitcnt vmcnt(4) lgkmcnt(3)
	v_mfma_f32_32x32x16_f16 v[50:65], v[102:105], v[110:113], v[50:65]
	s_waitcnt lgkmcnt(2)
	v_mfma_f32_32x32x16_f16 v[34:49], v[118:121], v[110:113], v[34:49]
	v_mfma_f32_32x32x16_f16 v[2:17], v[102:105], v[86:89], v[2:17]
	v_mfma_f32_32x32x16_f16 v[18:33], v[118:121], v[86:89], v[18:33]
	ds_read_b128 v[86:89], v157 offset:160
	ds_read_b128 v[102:105], v157 offset:8864
	s_waitcnt vmcnt(3) lgkmcnt(3)
	v_mfma_f32_32x32x16_f16 v[50:65], v[94:97], v[106:109], v[50:65]
	s_waitcnt lgkmcnt(2)
	v_mfma_f32_32x32x16_f16 v[34:49], v[114:117], v[106:109], v[34:49]
	v_mfma_f32_32x32x16_f16 v[2:17], v[94:97], v[78:81], v[2:17]
	v_mfma_f32_32x32x16_f16 v[18:33], v[114:117], v[78:81], v[18:33]
	ds_read_b128 v[78:81], v157 offset:192
	ds_read_b128 v[94:97], v157 offset:8896
	s_waitcnt vmcnt(2) lgkmcnt(3)
	v_mfma_f32_32x32x16_f16 v[50:65], v[86:89], v[98:101], v[50:65]
	s_waitcnt lgkmcnt(2)
	v_mfma_f32_32x32x16_f16 v[34:49], v[102:105], v[98:101], v[34:49]
	v_mfma_f32_32x32x16_f16 v[2:17], v[86:89], v[74:77], v[2:17]
	v_mfma_f32_32x32x16_f16 v[18:33], v[102:105], v[74:77], v[18:33]
	ds_read_b128 v[74:77], v157 offset:224
	ds_read_b128 v[86:89], v157 offset:8928
	s_waitcnt vmcnt(1) lgkmcnt(3)
	v_mfma_f32_32x32x16_f16 v[50:65], v[78:81], v[90:93], v[50:65]
	s_waitcnt lgkmcnt(2)
	v_mfma_f32_32x32x16_f16 v[34:49], v[94:97], v[90:93], v[34:49]
	v_mfma_f32_32x32x16_f16 v[2:17], v[78:81], v[70:73], v[2:17]
	v_lshrrev_b32_e32 v81, 16, v127
	v_mfma_f32_32x32x16_f16 v[18:33], v[94:97], v[70:73], v[18:33]
	v_perm_b32 v73, v240, v130, s43
	s_waitcnt vmcnt(0) lgkmcnt(1)
	v_mfma_f32_32x32x16_f16 v[50:65], v[74:77], v[82:85], v[50:65]
	v_pk_add_f16 v73, v73, s20 op_sel_hi:[1,0]
	v_and_b32_e32 v70, 63, v154
	v_cmp_gt_u32_e32 vcc, 32, v70
	s_waitcnt lgkmcnt(0)
	v_mfma_f32_32x32x16_f16 v[34:49], v[86:89], v[82:85], v[34:49]
	s_nop 6
	v_cvt_pk_f16_f32 v65, v64, v65
	v_cvt_pk_f16_f32 v64, v62, v63
	v_cvt_pk_f16_f32 v63, v60, v61
	v_cvt_pk_f16_f32 v57, v56, v57
	v_cvt_pk_f16_f32 v56, v54, v55
	v_cvt_pk_f16_f32 v55, v52, v53
	v_mfma_f32_32x32x16_f16 v[2:17], v[74:77], v[66:69], v[2:17]
	v_perm_b32 v74, v240, v131, s42
	v_cvt_pk_f16_f32 v41, v40, v41
	v_cvt_pk_f16_f32 v40, v38, v39
	v_cvt_pk_f16_f32 v38, v34, v35
	v_mfma_f32_32x32x16_f16 v[18:33], v[86:89], v[66:69], v[18:33]
	v_perm_b32 v71, v240, v130, s42
	v_perm_b32 v75, v240, v131, s43
	v_pk_add_f16 v72, v71, s20 op_sel_hi:[1,0]
	v_perm_b32 v71, v240, v128, s42
	v_perm_b32 v77, v240, v128, s43
	v_or_b32_e32 v34, s19, v155
	v_mov_b32_e32 v35, 0
	v_cvt_pk_f16_f32 v39, v36, v37
	v_lshl_add_u64 v[36:37], v[34:35], 2, s[10:11]
	global_load_dword v80, v[36:37], off
	v_cvt_pk_f16_f32 v54, v50, v51
	v_perm_b32 v50, v240, v136, s42
	v_perm_b32 v51, v240, v136, s43
	v_perm_b32 v52, v240, v137, s42
	v_perm_b32 v53, v240, v137, s43
	v_perm_b32 v66, v240, v134, s42
	v_perm_b32 v67, v240, v134, s43
	v_perm_b32 v68, v240, v135, s42
	v_perm_b32 v69, v240, v135, s43
	v_pk_add_f16 v50, v50, s20 op_sel_hi:[1,0]
	v_pk_add_f16 v51, v51, s20 op_sel_hi:[1,0]
	v_pk_add_f16 v52, v52, s20 op_sel_hi:[1,0]
	v_pk_add_f16 v53, v53, s20 op_sel_hi:[1,0]
	v_pk_add_f16 v66, v66, s20 op_sel_hi:[1,0]
	v_pk_add_f16 v67, v67, s20 op_sel_hi:[1,0]
	v_pk_add_f16 v68, v68, s20 op_sel_hi:[1,0]
	v_pk_add_f16 v69, v69, s20 op_sel_hi:[1,0]
	v_cvt_pk_f16_f32 v62, v58, v59
	v_mfma_f32_32x32x16_f16 v[2:17], v[50:53], v[54:57], v[2:17]
	v_perm_b32 v58, v240, v132, s42
	v_perm_b32 v59, v240, v132, s43
	v_perm_b32 v60, v240, v133, s42
	v_perm_b32 v61, v240, v133, s43
	v_pk_add_f16 v58, v58, s20 op_sel_hi:[1,0]
	v_mfma_f32_32x32x16_f16 v[18:33], v[66:69], v[54:57], v[18:33]
	v_pk_add_f16 v59, v59, s20 op_sel_hi:[1,0]
	v_pk_add_f16 v60, v60, s20 op_sel_hi:[1,0]
	v_pk_add_f16 v61, v61, s20 op_sel_hi:[1,0]
	v_pk_add_f16 v74, v74, s20 op_sel_hi:[1,0]
	v_pk_add_f16 v75, v75, s20 op_sel_hi:[1,0]
	v_perm_b32 v36, v240, v129, s42
	v_perm_b32 v37, v240, v129, s43
	v_pk_add_f16 v76, v71, s20 op_sel_hi:[1,0]
	v_pk_add_f16 v79, v37, s20 op_sel_hi:[1,0]
	v_pk_add_f16 v78, v36, s20 op_sel_hi:[1,0]
	v_lshrrev_b32_e32 v82, 8, v127
	v_mfma_f32_32x32x16_f16 v[2:17], v[58:61], v[62:65], v[2:17]
	v_perm_b32 v81, v82, v81, s13
	v_perm_b32 v36, v240, v126, s42
	v_perm_b32 v37, v240, v126, s43
	v_perm_b32 v71, v240, v127, s42
	v_or_b32_e32 v81, 0x64006400, v81
	v_mfma_f32_32x32x16_f16 v[18:33], v[72:75], v[62:65], v[18:33]
	v_pk_add_f16 v77, v77, s20 op_sel_hi:[1,0]
	v_pk_add_f16 v50, v36, s20 op_sel_hi:[1,0]
	v_pk_add_f16 v51, v37, s20 op_sel_hi:[1,0]
	v_pk_add_f16 v52, v71, s20 op_sel_hi:[1,0]
	v_pk_add_f16 v53, v81, s20 op_sel_hi:[1,0]
	v_cvt_pk_f16_f32 v49, v48, v49
	v_cvt_pk_f16_f32 v48, v46, v47
	v_cvt_pk_f16_f32 v46, v42, v43
	v_cvt_pk_f16_f32 v47, v44, v45
	v_perm_b32 v37, v240, v124, s43
	v_perm_b32 v44, v240, v125, s42
	v_perm_b32 v36, v240, v124, s42
	v_pk_add_f16 v43, v37, s20 op_sel_hi:[1,0]
	v_lshrrev_b32_e32 v37, 16, v122
	v_lshrrev_b32_e32 v54, 8, v122
	v_perm_b32 v45, v240, v125, s43
	v_pk_add_f16 v42, v36, s20 op_sel_hi:[1,0]
	v_mfma_f32_32x32x16_f16 v[2:17], v[76:79], v[38:41], v[2:17]
	v_perm_b32 v37, v54, v37, s13
	v_lshlrev_b32_e32 v54, 8, v123
	v_perm_b32 v54, v54, v123, s13
	v_perm_b32 v36, v240, v122, s42
	v_or_b32_e32 v37, 0x64006400, v37
	v_pk_add_f16 v36, v36, s20 op_sel_hi:[1,0]
	v_mfma_f32_32x32x16_f16 v[18:33], v[50:53], v[38:41], v[18:33]
	v_or_b32_e32 v38, 0x64006400, v54
	v_perm_b32 v39, v240, v123, s43
	v_pk_add_f16 v37, v37, s20 op_sel_hi:[1,0]
	v_pk_add_f16 v38, v38, s20 op_sel_hi:[1,0]
	v_pk_add_f16 v39, v39, s20 op_sel_hi:[1,0]
	v_pk_add_f16 v44, v44, s20 op_sel_hi:[1,0]
	v_pk_add_f16 v45, v45, s20 op_sel_hi:[1,0]
	v_mfma_f32_32x32x16_f16 v[18:33], v[36:39], v[46:49], v[18:33]
	s_lshl_b32 s13, s12, 14
	v_lshlrev_b32_e32 v40, 1, v34
	v_lshl_or_b32 v38, v156, 10, s13
	s_mov_b32 s11, 0x20000
	s_mov_b32 s10, 0x200000
	v_add_u32_e32 v39, v38, v40
	s_waitcnt vmcnt(0)
	s_nop 4
	v_add_f32_e32 v18, v80, v18
	v_mfma_f32_32x32x16_f16 v[2:17], v[42:45], v[46:49], v[2:17]
	v_mul_f32_e32 v37, v18, v18
	s_nop 10
	v_add_f32_e32 v2, v80, v2
	v_add_f32_e32 v36, v2, v18
	v_fmac_f32_e32 v37, v2, v2
	v_cvt_f16_f32_e32 v2, v2
	v_cvt_f16_f32_e32 v18, v18
	v_add_f32_e32 v36, 0, v36
	buffer_store_short v2, v39, s[8:11], 0 offen sc1
	v_add_u32_e32 v39, 0x2000, v40
	v_add_u32_e32 v2, v38, v39
	buffer_store_short v18, v2, s[8:11], 0 offen sc1
	v_add_f32_e32 v2, v80, v3
	v_add_f32_e32 v3, v80, v19
	v_mul_f32_e32 v19, v3, v3
	v_add_f32_e32 v18, v2, v3
	v_fmac_f32_e32 v19, v2, v2
	v_cvt_f16_f32_e32 v2, v2
	v_cvt_f16_f32_e32 v3, v3
	v_add_f32_e32 v18, v36, v18
	v_or_b32_e32 v36, 0x100, v38
	v_add_f32_e32 v19, v37, v19
	v_add_u32_e32 v37, v36, v40
	buffer_store_short v2, v37, s[8:11], 0 offen sc1
	v_add_u32_e32 v2, v36, v39
	buffer_store_short v3, v2, s[8:11], 0 offen sc1
	v_add_f32_e32 v2, v80, v4
	v_add_f32_e32 v3, v80, v20
	v_add_f32_e32 v4, v2, v3
	v_add_f32_e32 v4, v18, v4
	v_mul_f32_e32 v18, v3, v3
	v_fmac_f32_e32 v18, v2, v2
	v_cvt_f16_f32_e32 v2, v2
	v_cvt_f16_f32_e32 v3, v3
	v_add_f32_e32 v18, v19, v18
	v_or_b32_e32 v19, 0x200, v38
	v_add_u32_e32 v20, v19, v40
	buffer_store_short v2, v20, s[8:11], 0 offen sc1
	v_add_u32_e32 v2, v19, v39
	buffer_store_short v3, v2, s[8:11], 0 offen sc1
	v_add_f32_e32 v2, v80, v5
	v_add_f32_e32 v3, v80, v21
	v_add_f32_e32 v5, v2, v3
	v_add_f32_e32 v4, v4, v5
	v_mul_f32_e32 v5, v3, v3
	v_fmac_f32_e32 v5, v2, v2
	v_cvt_f16_f32_e32 v2, v2
	v_cvt_f16_f32_e32 v3, v3
	v_add_f32_e32 v5, v18, v5
	v_or_b32_e32 v18, 0x300, v38
	v_add_u32_e32 v19, v18, v40
	buffer_store_short v2, v19, s[8:11], 0 offen sc1
	v_add_u32_e32 v2, v18, v39
	buffer_store_short v3, v2, s[8:11], 0 offen sc1
	v_add_f32_e32 v2, v80, v6
	v_add_f32_e32 v3, v80, v22
	v_add_f32_e32 v6, v2, v3
	v_add_f32_e32 v4, v4, v6
	v_mul_f32_e32 v6, v3, v3
	v_fmac_f32_e32 v6, v2, v2
	v_cvt_f16_f32_e32 v2, v2
	v_cvt_f16_f32_e32 v3, v3
	v_add_f32_e32 v5, v5, v6
	v_or_b32_e32 v6, 0x800, v38
	v_add_u32_e32 v18, v6, v40
	buffer_store_short v2, v18, s[8:11], 0 offen sc1
	v_add_u32_e32 v2, v6, v39
	buffer_store_short v3, v2, s[8:11], 0 offen sc1
	v_add_f32_e32 v2, v80, v7
	v_add_f32_e32 v3, v80, v23
	v_add_f32_e32 v6, v2, v3
	v_add_f32_e32 v4, v4, v6
	v_mul_f32_e32 v6, v3, v3
	v_fmac_f32_e32 v6, v2, v2
	v_cvt_f16_f32_e32 v2, v2
	v_cvt_f16_f32_e32 v3, v3
	v_add_f32_e32 v5, v5, v6
	v_or_b32_e32 v6, 0x900, v38
	v_add_u32_e32 v7, v6, v40
	buffer_store_short v2, v7, s[8:11], 0 offen sc1
	v_add_u32_e32 v2, v6, v39
	buffer_store_short v3, v2, s[8:11], 0 offen sc1
	v_add_f32_e32 v2, v80, v8
	v_add_f32_e32 v3, v80, v24
	v_add_f32_e32 v6, v2, v3
	v_add_f32_e32 v4, v4, v6
	v_mul_f32_e32 v6, v3, v3
	v_fmac_f32_e32 v6, v2, v2
	v_cvt_f16_f32_e32 v2, v2
	v_cvt_f16_f32_e32 v3, v3
	v_add_f32_e32 v5, v5, v6
	v_or_b32_e32 v6, 0xa00, v38
	v_add_u32_e32 v7, v6, v40
	buffer_store_short v2, v7, s[8:11], 0 offen sc1
	v_add_u32_e32 v2, v6, v39
	buffer_store_short v3, v2, s[8:11], 0 offen sc1
	v_add_f32_e32 v2, v80, v9
	v_add_f32_e32 v3, v80, v25
	v_add_f32_e32 v6, v2, v3
	v_add_f32_e32 v4, v4, v6
	v_mul_f32_e32 v6, v3, v3
	v_fmac_f32_e32 v6, v2, v2
	v_cvt_f16_f32_e32 v2, v2
	v_cvt_f16_f32_e32 v3, v3
	v_add_f32_e32 v5, v5, v6
	v_or_b32_e32 v6, 0xb00, v38
	v_add_u32_e32 v7, v6, v40
	buffer_store_short v2, v7, s[8:11], 0 offen sc1
	v_add_u32_e32 v2, v6, v39
	buffer_store_short v3, v2, s[8:11], 0 offen sc1
	v_add_f32_e32 v2, v80, v10
	v_add_f32_e32 v3, v80, v26
	v_add_f32_e32 v6, v2, v3
	v_add_f32_e32 v4, v4, v6
	v_mul_f32_e32 v6, v3, v3
	v_fmac_f32_e32 v6, v2, v2
	v_cvt_f16_f32_e32 v2, v2
	v_cvt_f16_f32_e32 v3, v3
	v_add_f32_e32 v5, v5, v6
	v_or_b32_e32 v6, 0x1000, v38
	v_add_u32_e32 v7, v6, v40
	buffer_store_short v2, v7, s[8:11], 0 offen sc1
	v_add_u32_e32 v2, v6, v39
	buffer_store_short v3, v2, s[8:11], 0 offen sc1
	v_add_f32_e32 v2, v80, v11
	v_add_f32_e32 v3, v80, v27
	v_add_f32_e32 v6, v2, v3
	v_add_f32_e32 v4, v4, v6
	v_mul_f32_e32 v6, v3, v3
	v_fmac_f32_e32 v6, v2, v2
	v_cvt_f16_f32_e32 v2, v2
	v_cvt_f16_f32_e32 v3, v3
	v_add_f32_e32 v5, v5, v6
	v_or_b32_e32 v6, 0x1100, v38
	v_add_u32_e32 v7, v6, v40
	buffer_store_short v2, v7, s[8:11], 0 offen sc1
	v_add_u32_e32 v2, v6, v39
	buffer_store_short v3, v2, s[8:11], 0 offen sc1
	v_add_f32_e32 v2, v80, v12
	v_add_f32_e32 v3, v80, v28
	v_add_f32_e32 v6, v2, v3
	v_add_f32_e32 v4, v4, v6
	v_mul_f32_e32 v6, v3, v3
	v_fmac_f32_e32 v6, v2, v2
	v_cvt_f16_f32_e32 v2, v2
	v_cvt_f16_f32_e32 v3, v3
	v_add_f32_e32 v5, v5, v6
	v_or_b32_e32 v6, 0x1200, v38
	v_add_u32_e32 v7, v6, v40
	buffer_store_short v2, v7, s[8:11], 0 offen sc1
	v_add_u32_e32 v2, v6, v39
	buffer_store_short v3, v2, s[8:11], 0 offen sc1
	v_add_f32_e32 v2, v80, v13
	v_add_f32_e32 v3, v80, v29
	v_add_f32_e32 v6, v2, v3
	v_add_f32_e32 v4, v4, v6
	v_mul_f32_e32 v6, v3, v3
	v_fmac_f32_e32 v6, v2, v2
	v_cvt_f16_f32_e32 v2, v2
	v_cvt_f16_f32_e32 v3, v3
	v_add_f32_e32 v5, v5, v6
	v_or_b32_e32 v6, 0x1300, v38
	v_add_u32_e32 v7, v6, v40
	buffer_store_short v2, v7, s[8:11], 0 offen sc1
	v_add_u32_e32 v2, v6, v39
	buffer_store_short v3, v2, s[8:11], 0 offen sc1
	v_add_f32_e32 v2, v80, v14
	v_add_f32_e32 v3, v80, v30
	v_add_f32_e32 v6, v2, v3
	v_add_f32_e32 v4, v4, v6
	v_mul_f32_e32 v6, v3, v3
	v_fmac_f32_e32 v6, v2, v2
	v_cvt_f16_f32_e32 v2, v2
	v_cvt_f16_f32_e32 v3, v3
	v_add_f32_e32 v5, v5, v6
	v_or_b32_e32 v6, 0x1800, v38
	v_add_u32_e32 v7, v6, v40
	buffer_store_short v2, v7, s[8:11], 0 offen sc1
	v_add_u32_e32 v2, v6, v39
	buffer_store_short v3, v2, s[8:11], 0 offen sc1
	v_add_f32_e32 v2, v80, v15
	v_add_f32_e32 v3, v80, v31
	v_add_f32_e32 v6, v2, v3
	v_add_f32_e32 v4, v4, v6
	v_mul_f32_e32 v6, v3, v3
	v_fmac_f32_e32 v6, v2, v2
	v_cvt_f16_f32_e32 v2, v2
	v_cvt_f16_f32_e32 v3, v3
	v_add_f32_e32 v5, v5, v6
	v_or_b32_e32 v6, 0x1900, v38
	v_add_u32_e32 v7, v6, v40
	buffer_store_short v2, v7, s[8:11], 0 offen sc1
	v_add_u32_e32 v2, v6, v39
	buffer_store_short v3, v2, s[8:11], 0 offen sc1
	v_add_f32_e32 v2, v80, v16
	v_add_f32_e32 v3, v80, v32
	v_add_f32_e32 v6, v2, v3
	v_add_f32_e32 v4, v4, v6
	v_mul_f32_e32 v6, v3, v3
	v_fmac_f32_e32 v6, v2, v2
	v_cvt_f16_f32_e32 v2, v2
	v_cvt_f16_f32_e32 v3, v3
	v_add_f32_e32 v5, v5, v6
	v_or_b32_e32 v6, 0x1a00, v38
	v_add_u32_e32 v7, v6, v40
	buffer_store_short v2, v7, s[8:11], 0 offen sc1
	v_add_u32_e32 v2, v6, v39
	v_add_f32_e32 v6, v80, v17
	v_add_f32_e32 v7, v80, v33
	buffer_store_short v3, v2, s[8:11], 0 offen sc1
	v_add_f32_e32 v2, v6, v7
	v_mul_f32_e32 v3, v7, v7
	v_add_f32_e32 v2, v4, v2
	v_fmac_f32_e32 v3, v6, v6
	v_lshlrev_b32_e32 v4, 2, v70
	v_add_f32_e32 v3, v5, v3
	v_xor_b32_e32 v5, 0x80, v4
	v_cvt_f16_f32_e32 v6, v6
	ds_bpermute_b32 v4, v5, v2
	ds_bpermute_b32 v5, v5, v3
	v_cvt_f16_f32_e32 v7, v7
	v_or_b32_e32 v8, 0x1b00, v38
	v_add_u32_e32 v9, v8, v40
	buffer_store_short v6, v9, s[8:11], 0 offen sc1
	v_add_u32_e32 v6, v8, v39
	buffer_store_short v7, v6, s[8:11], 0 offen sc1
	s_and_saveexec_b64 s[8:9], vcc
	s_cbranch_execz .LBB2_9
	s_load_dwordx2 s[10:11], s[0:1], 0x98
	v_lshl_add_u32 v34, s16, 8, v34
	s_waitcnt lgkmcnt(0)
	v_add_f32_e32 v5, v3, v5
	v_add_f32_e32 v4, v2, v4
	v_lshl_add_u64 v[2:3], v[34:35], 2, s[10:11]
	global_atomic_add_f32 v[2:3], v4, off
	global_atomic_add_f32 v[2:3], v5, off offset:512

.LBB2_17:
	s_and_b64 vcc, exec, s[2:3]
	s_cbranch_vccz .LBB2_27
	v_mov_b32_e32 v240, 0x64646464
	s_mov_b32 s42, 0x4010400
	s_mov_b32 s43, 0x4030402
	s_load_dwordx2 s[2:3], s[0:1], 0x70
	s_load_dwordx4 s[4:7], s[0:1], 0x40
	s_lshr_b32 s11, s15, 7
	s_lshl_b32 s8, s12, 3
	s_or_b32 s8, s11, s8
	s_ashr_i32 s9, s8, 31
	s_bfe_u32 s10, s15, 0x10006
	s_lshl_b64 s[12:13], s[8:9], 12
	v_and_b32_e32 v156, 63, v0
	s_waitcnt lgkmcnt(0)
	s_add_u32 s12, s2, s12
	s_addc_u32 s13, s3, s13
	v_lshlrev_b32_e32 v1, 3, v156
	global_load_dwordx2 v[154:155], v1, s[12:13]
	global_load_dwordx2 v[150:151], v1, s[12:13] offset:512
	global_load_dwordx2 v[146:147], v1, s[12:13] offset:1024
	global_load_dwordx2 v[142:143], v1, s[12:13] offset:1536
	global_load_dwordx2 v[152:153], v1, s[12:13] offset:2048
	global_load_dwordx2 v[148:149], v1, s[12:13] offset:2560
	global_load_dwordx2 v[144:145], v1, s[12:13] offset:3072
	global_load_dwordx2 v[140:141], v1, s[12:13] offset:3584
	s_lshl_b32 s9, s14, 10
	s_lshl_b32 s12, s10, 9
	s_or_b32 s9, s12, s9
	v_or_b32_e32 v1, s9, v156
	v_lshlrev_b32_e32 v2, 4, v1
	v_mov_b32_e32 v3, 0
	v_lshl_add_u64 v[4:5], s[4:5], 0, v[2:3]
	s_movk_i32 s9, 0x1000
	v_add_co_u32_e32 v4, vcc, s9, v4
	v_lshlrev_b32_e32 v1, 2, v0
	s_nop 0
	v_addc_co_u32_e32 v5, vcc, 0, v5, vcc
	global_load_dwordx4 v[86:89], v[4:5], off
	global_load_dwordx4 v[78:81], v[4:5], off offset:1024
	global_load_dwordx4 v[70:73], v[4:5], off offset:2048
	global_load_dwordx4 v[66:69], v[4:5], off offset:3072
	global_load_dwordx4 v[122:125], v2, s[4:5]
	global_load_dwordx4 v[126:129], v2, s[6:7]
	global_load_dwordx4 v[114:117], v2, s[4:5] offset:1024
	global_load_dwordx4 v[118:121], v2, s[6:7] offset:1024
	global_load_dwordx4 v[106:109], v2, s[4:5] offset:2048
	global_load_dwordx4 v[110:113], v2, s[6:7] offset:2048
	global_load_dwordx4 v[98:101], v2, s[4:5] offset:3072
	global_load_dwordx4 v[102:105], v2, s[6:7] offset:3072
	v_lshl_add_u64 v[4:5], s[6:7], 0, v[2:3]
	v_add_co_u32_e32 v2, vcc, 0x1000, v4
	s_nop 1
	v_addc_co_u32_e32 v3, vcc, 0, v5, vcc
	global_load_dwordx4 v[94:97], v[2:3], off
	global_load_dwordx4 v[90:93], v[2:3], off offset:1024
	global_load_dwordx4 v[82:85], v[2:3], off offset:2048
	global_load_dwordx4 v[74:77], v[2:3], off offset:3072
	v_cmp_gt_u32_e32 vcc, 64, v0
	s_and_saveexec_b64 s[4:5], vcc
	s_cbranch_execz .LBB2_20
	s_load_dwordx2 s[0:1], s[0:1], 0x60
	v_lshl_or_b32 v2, s14, 8, v1
	v_add_u32_e32 v3, 0x1ee00, v1
	s_waitcnt lgkmcnt(0)
	global_load_dword v2, v2, s[0:1]
	s_waitcnt vmcnt(0)
	ds_write_b32 v3, v2

.LBB2_24:
	s_or_b64 exec, exec, s[0:1]
	v_and_b32_e32 v1, 31, v0
	v_lshlrev_b32_e32 v2, 2, v1
	v_lshl_or_b32 v2, s10, 7, v2
	v_or_b32_e32 v2, 0x1ee00, v2
	v_lshrrev_b32_e32 v158, 5, v156
	s_waitcnt lgkmcnt(0)
	s_barrier
	s_barrier
	ds_read_b32 v157, v2
	v_mul_u32_u24_e32 v2, 0x88, v1
	s_mul_i32 s0, s11, 0x4400
	v_lshlrev_b32_e32 v2, 1, v2
	v_lshlrev_b32_e32 v3, 4, v158
	v_mov_b32_e32 v138, v0
	v_add3_u32 v159, s0, v2, v3
	ds_read_b128 v[2:5], v159
	ds_read_b128 v[18:21], v159 offset:8704
	ds_read_b128 v[130:133], v159 offset:32
	s_waitcnt vmcnt(10) lgkmcnt(2)
	v_mfma_f32_32x32x16_f16 v[50:65], v[2:5], v[126:129], 0
	s_mov_b32 s4, 0xc060c00
	s_mov_b32 s5, 0xe400
	s_mulk_i32 s11, 0x2400
	s_lshl_b32 s0, s10, 6
	s_or_b32 s0, s11, s0
	s_add_i32 s0, s0, 0x11000
	v_lshl_or_b32 v1, v1, 1, s0
	s_waitcnt lgkmcnt(1)
	v_mfma_f32_32x32x16_f16 v[34:49], v[18:21], v[126:129], 0
	s_or_b32 s0, s8, 2
	s_ashr_i32 s1, s0, 31
	s_lshl_b64 s[0:1], s[0:1], 12
	s_add_u32 s0, s2, s0
	s_addc_u32 s1, s3, s1
	v_cmp_gt_u32_e32 vcc, 32, v156
	v_mfma_f32_32x32x16_f16 v[2:17], v[2:5], v[122:125], 0
	v_mfma_f32_32x32x16_f16 v[18:33], v[18:21], v[122:125], 0
	ds_read_b128 v[134:137], v159 offset:8736
	ds_read_b128 v[160:163], v159 offset:64
	s_waitcnt vmcnt(8) lgkmcnt(2)
	v_mfma_f32_32x32x16_f16 v[50:65], v[130:133], v[118:121], v[50:65]
	s_waitcnt lgkmcnt(1)
	v_mfma_f32_32x32x16_f16 v[34:49], v[134:137], v[118:121], v[34:49]
	v_mfma_f32_32x32x16_f16 v[2:17], v[130:133], v[114:117], v[2:17]
	v_mfma_f32_32x32x16_f16 v[18:33], v[134:137], v[114:117], v[18:33]
	ds_read_b128 v[130:133], v159 offset:8768
	ds_read_b128 v[134:137], v159 offset:96
	s_waitcnt vmcnt(6) lgkmcnt(2)
	v_mfma_f32_32x32x16_f16 v[50:65], v[160:163], v[110:113], v[50:65]
	s_waitcnt lgkmcnt(1)
	v_mfma_f32_32x32x16_f16 v[34:49], v[130:133], v[110:113], v[34:49]
	v_mfma_f32_32x32x16_f16 v[2:17], v[160:163], v[106:109], v[2:17]
	v_mfma_f32_32x32x16_f16 v[18:33], v[130:133], v[106:109], v[18:33]
	ds_read_b128 v[130:133], v159 offset:8800
	ds_read_b128 v[160:163], v159 offset:128
	s_waitcnt vmcnt(4) lgkmcnt(2)
	v_mfma_f32_32x32x16_f16 v[50:65], v[134:137], v[102:105], v[50:65]
	s_waitcnt lgkmcnt(1)
	v_mfma_f32_32x32x16_f16 v[34:49], v[130:133], v[102:105], v[34:49]
	v_mfma_f32_32x32x16_f16 v[2:17], v[134:137], v[98:101], v[2:17]
	v_mfma_f32_32x32x16_f16 v[18:33], v[130:133], v[98:101], v[18:33]
	ds_read_b128 v[130:133], v159 offset:8832
	ds_read_b128 v[134:137], v159 offset:160
	s_waitcnt vmcnt(3) lgkmcnt(2)
	v_mfma_f32_32x32x16_f16 v[50:65], v[160:163], v[94:97], v[50:65]
	s_waitcnt lgkmcnt(1)
	v_mfma_f32_32x32x16_f16 v[34:49], v[130:133], v[94:97], v[34:49]
	v_mfma_f32_32x32x16_f16 v[2:17], v[160:163], v[86:89], v[2:17]
	v_mfma_f32_32x32x16_f16 v[18:33], v[130:133], v[86:89], v[18:33]
	ds_read_b128 v[130:133], v159 offset:8864
	ds_read_b128 v[160:163], v159 offset:192
	s_waitcnt vmcnt(2) lgkmcnt(2)
	v_mfma_f32_32x32x16_f16 v[50:65], v[134:137], v[90:93], v[50:65]
	s_waitcnt lgkmcnt(1)
	v_mfma_f32_32x32x16_f16 v[34:49], v[130:133], v[90:93], v[34:49]
	v_mfma_f32_32x32x16_f16 v[2:17], v[134:137], v[78:81], v[2:17]
	v_mfma_f32_32x32x16_f16 v[18:33], v[130:133], v[78:81], v[18:33]
	ds_read_b128 v[130:133], v159 offset:8896
	ds_read_b128 v[164:167], v159 offset:224
	s_waitcnt vmcnt(1) lgkmcnt(2)
	v_mfma_f32_32x32x16_f16 v[50:65], v[160:163], v[82:85], v[50:65]
	s_waitcnt lgkmcnt(1)
	v_mfma_f32_32x32x16_f16 v[34:49], v[130:133], v[82:85], v[34:49]
	v_mfma_f32_32x32x16_f16 v[2:17], v[160:163], v[70:73], v[2:17]
	v_mfma_f32_32x32x16_f16 v[18:33], v[130:133], v[70:73], v[18:33]
	v_lshlrev_b32_e32 v130, 3, v138
	v_and_b32_e32 v168, 0x1f8, v130
	global_load_dwordx2 v[138:139], v168, s[0:1]
	global_load_dwordx2 v[134:135], v168, s[0:1] offset:512
	global_load_dwordx2 v[132:133], v168, s[0:1] offset:1024
	global_load_dwordx2 v[130:131], v168, s[0:1] offset:1536
	global_load_dwordx2 v[136:137], v168, s[0:1] offset:2048
	s_waitcnt vmcnt(5) lgkmcnt(0)
	v_mfma_f32_32x32x16_f16 v[50:65], v[164:167], v[74:77], v[50:65]
	v_mfma_f32_32x32x16_f16 v[2:17], v[164:167], v[66:69], v[2:17]
	s_nop 10
	v_cvt_pk_f16_f32 v57, v56, v57
	v_cvt_pk_f16_f32 v56, v54, v55
	v_cvt_pk_f16_f32 v55, v52, v53
	v_cvt_pk_f16_f32 v54, v50, v51
	v_perm_b32 v50, v240, v154, s42
	v_perm_b32 v51, v240, v154, s43
	v_perm_b32 v52, v240, v155, s42
	v_perm_b32 v53, v240, v155, s43
	v_pk_add_f16 v50, v50, s5 op_sel_hi:[1,0]
	v_pk_add_f16 v51, v51, s5 op_sel_hi:[1,0]
	v_pk_add_f16 v52, v52, s5 op_sel_hi:[1,0]
	v_pk_add_f16 v53, v53, s5 op_sel_hi:[1,0]
	v_cvt_pk_f16_f32 v65, v64, v65
	v_cvt_pk_f16_f32 v64, v62, v63
	v_cvt_pk_f16_f32 v63, v60, v61
	v_cvt_pk_f16_f32 v62, v58, v59
	v_mfma_f32_32x32x16_f16 v[2:17], v[50:53], v[54:57], v[2:17]
	v_perm_b32 v58, v240, v150, s42
	v_perm_b32 v59, v240, v150, s43
	v_perm_b32 v60, v240, v151, s42
	v_perm_b32 v61, v240, v151, s43
	v_pk_add_f16 v58, v58, s5 op_sel_hi:[1,0]
	v_pk_add_f16 v59, v59, s5 op_sel_hi:[1,0]
	v_pk_add_f16 v60, v60, s5 op_sel_hi:[1,0]
	v_pk_add_f16 v61, v61, s5 op_sel_hi:[1,0]
	s_nop 1
	v_mfma_f32_32x32x16_f16 v[2:17], v[58:61], v[62:65], v[2:17]
	ds_read_b128 v[160:163], v159 offset:8928
	v_perm_b32 v155, v240, v152, s43
	v_perm_b32 v164, v240, v153, s42
	s_waitcnt lgkmcnt(0)
	v_mfma_f32_32x32x16_f16 v[18:33], v[160:163], v[66:69], v[18:33]
	v_perm_b32 v154, v240, v152, s42
	v_perm_b32 v165, v240, v153, s43
	v_pk_add_f16 v152, v154, s5 op_sel_hi:[1,0]
	v_pk_add_f16 v153, v155, s5 op_sel_hi:[1,0]
	v_pk_add_f16 v154, v164, s5 op_sel_hi:[1,0]
	v_pk_add_f16 v155, v165, s5 op_sel_hi:[1,0]
	v_mfma_f32_32x32x16_f16 v[34:49], v[160:163], v[74:77], v[34:49]
	v_perm_b32 v151, v240, v148, s43
	v_perm_b32 v164, v240, v149, s42
	v_mfma_f32_32x32x16_f16 v[18:33], v[152:155], v[54:57], v[18:33]
	v_perm_b32 v150, v240, v148, s42
	v_perm_b32 v165, v240, v149, s43
	v_pk_add_f16 v148, v150, s5 op_sel_hi:[1,0]
	v_pk_add_f16 v149, v151, s5 op_sel_hi:[1,0]
	v_pk_add_f16 v150, v164, s5 op_sel_hi:[1,0]
	v_pk_add_f16 v151, v165, s5 op_sel_hi:[1,0]
	s_nop 2
	v_cvt_pk_f16_f32 v41, v40, v41
	v_cvt_pk_f16_f32 v40, v38, v39
	v_cvt_pk_f16_f32 v38, v34, v35
	v_cvt_pk_f16_f32 v39, v36, v37
	v_mfma_f32_32x32x16_f16 v[18:33], v[148:151], v[62:65], v[18:33]
	v_perm_b32 v34, v240, v146, s42
	v_perm_b32 v35, v240, v146, s43
	v_perm_b32 v36, v240, v147, s42
	v_perm_b32 v37, v240, v147, s43
	v_pk_add_f16 v34, v34, s5 op_sel_hi:[1,0]
	v_pk_add_f16 v35, v35, s5 op_sel_hi:[1,0]
	v_pk_add_f16 v36, v36, s5 op_sel_hi:[1,0]
	v_pk_add_f16 v37, v37, s5 op_sel_hi:[1,0]
	v_perm_b32 v146, v240, v144, s42
	v_perm_b32 v144, v240, v144, s43
	v_perm_b32 v147, v240, v145, s42
	v_perm_b32 v53, v240, v145, s43
	v_pk_add_f16 v50, v146, s5 op_sel_hi:[1,0]
	v_pk_add_f16 v51, v144, s5 op_sel_hi:[1,0]
	v_pk_add_f16 v52, v147, s5 op_sel_hi:[1,0]
	v_pk_add_f16 v53, v53, s5 op_sel_hi:[1,0]
	v_cvt_pk_f16_f32 v49, v48, v49
	v_cvt_pk_f16_f32 v48, v46, v47
	v_cvt_pk_f16_f32 v47, v44, v45
	v_mfma_f32_32x32x16_f16 v[2:17], v[34:37], v[38:41], v[2:17]
	v_cvt_pk_f16_f32 v46, v42, v43
	v_lshlrev_b32_e32 v54, 8, v140
	v_mfma_f32_32x32x16_f16 v[18:33], v[50:53], v[38:41], v[18:33]
	v_lshrrev_b32_e32 v37, 16, v141
	v_lshrrev_b32_e32 v38, 8, v141
	v_perm_b32 v34, v54, v140, s4
	v_perm_b32 v37, v38, v37, s4
	v_or_b32_e32 v34, 0x64006400, v34
	v_perm_b32 v35, v240, v140, s43
	v_perm_b32 v36, v240, v141, s42
	v_or_b32_e32 v37, 0x64006400, v37
	v_perm_b32 v42, v240, v142, s42
	v_perm_b32 v43, v240, v142, s43
	v_perm_b32 v44, v240, v143, s42
	v_perm_b32 v45, v240, v143, s43
	v_pk_add_f16 v34, v34, s5 op_sel_hi:[1,0]
	v_pk_add_f16 v35, v35, s5 op_sel_hi:[1,0]
	v_pk_add_f16 v36, v36, s5 op_sel_hi:[1,0]
	v_pk_add_f16 v37, v37, s5 op_sel_hi:[1,0]
	v_pk_add_f16 v42, v42, s5 op_sel_hi:[1,0]
	v_pk_add_f16 v43, v43, s5 op_sel_hi:[1,0]
	v_pk_add_f16 v44, v44, s5 op_sel_hi:[1,0]
	v_pk_add_f16 v45, v45, s5 op_sel_hi:[1,0]
	v_mfma_f32_32x32x16_f16 v[18:33], v[34:37], v[46:49], v[18:33]
	global_load_dwordx2 v[154:155], v168, s[0:1] offset:2560
	global_load_dwordx2 v[152:153], v168, s[0:1] offset:3072
	global_load_dwordx2 v[150:151], v168, s[0:1] offset:3584
	v_mov_b32_e32 v148, v0
	s_or_b32 s0, s8, 4
	s_ashr_i32 s1, s0, 31
	s_lshl_b64 s[0:1], s[0:1], 12
	v_mfma_f32_32x32x16_f16 v[2:17], v[42:45], v[46:49], v[2:17]
	s_nop 3
	v_add_f32_e32 v196, v157, v18
	v_mul_u32_u24_e32 v18, 0x120, v158
	v_lshl_add_u32 v158, v18, 1, v1
	v_cvt_f16_f32_e32 v1, v196
	v_add_f32_e32 v204, v157, v20
	v_add_f32_e32 v160, v157, v21
	v_add_f32_e32 v162, v157, v22
	s_nop 0
	v_add_f32_e32 v193, v157, v2
	v_add_f32_e32 v198, v157, v3
	v_cvt_f16_f32_e32 v2, v193
	v_cvt_f16_f32_e32 v3, v198
	ds_write_b16 v158, v1 offset:4608
	v_add_f32_e32 v203, v157, v4
	v_add_f32_e32 v1, v157, v5
	ds_write_b16 v158, v2
	ds_write_b16 v158, v3 offset:144
	v_cvt_f16_f32_e32 v2, v203
	v_cvt_f16_f32_e32 v3, v204
	v_cvt_f16_f32_e32 v4, v1
	v_cvt_f16_f32_e32 v5, v160
	v_add_f32_e32 v161, v157, v6
	v_add_f32_e32 v163, v157, v7
	v_add_f32_e32 v164, v157, v23
	ds_write_b16 v158, v2 offset:288
	ds_write_b16 v158, v3 offset:4896
	ds_write_b16 v158, v4 offset:432
	ds_write_b16 v158, v5 offset:5040
	v_cvt_f16_f32_e32 v2, v161
	v_cvt_f16_f32_e32 v3, v162
	v_cvt_f16_f32_e32 v4, v163
	v_cvt_f16_f32_e32 v5, v164
	v_add_f32_e32 v165, v157, v8
	v_add_f32_e32 v166, v157, v24
	v_add_f32_e32 v167, v157, v9
	v_add_f32_e32 v168, v157, v25
	ds_write_b16 v158, v2 offset:1152
	ds_write_b16 v158, v3 offset:5760
	ds_write_b16 v158, v4 offset:1296
	ds_write_b16 v158, v5 offset:5904
	v_cvt_f16_f32_e32 v2, v165
	v_cvt_f16_f32_e32 v3, v166
	v_cvt_f16_f32_e32 v4, v167
	v_cvt_f16_f32_e32 v5, v168
	v_add_f32_e32 v169, v157, v10
	v_add_f32_e32 v170, v157, v26
	v_add_f32_e32 v171, v157, v11
	v_add_f32_e32 v172, v157, v27
	ds_write_b16 v158, v2 offset:1440
	ds_write_b16 v158, v3 offset:6048
	ds_write_b16 v158, v4 offset:1584
	ds_write_b16 v158, v5 offset:6192
	v_cvt_f16_f32_e32 v2, v169
	v_cvt_f16_f32_e32 v3, v170
	v_cvt_f16_f32_e32 v4, v171
	v_cvt_f16_f32_e32 v5, v172
	v_add_f32_e32 v173, v157, v12
	v_add_f32_e32 v174, v157, v28
	v_add_f32_e32 v175, v157, v13
	v_add_f32_e32 v176, v157, v29
	ds_write_b16 v158, v2 offset:2304
	ds_write_b16 v158, v3 offset:6912
	ds_write_b16 v158, v4 offset:2448
	ds_write_b16 v158, v5 offset:7056
	v_cvt_f16_f32_e32 v2, v173
	v_cvt_f16_f32_e32 v3, v174
	v_cvt_f16_f32_e32 v4, v175
	v_cvt_f16_f32_e32 v5, v176
	v_add_f32_e32 v177, v157, v14
	v_add_f32_e32 v178, v157, v30
	v_add_f32_e32 v179, v157, v15
	v_add_f32_e32 v180, v157, v31
	ds_write_b16 v158, v2 offset:2592
	ds_write_b16 v158, v3 offset:7200
	ds_write_b16 v158, v4 offset:2736
	ds_write_b16 v158, v5 offset:7344
	v_cvt_f16_f32_e32 v2, v177
	v_cvt_f16_f32_e32 v3, v178
	v_cvt_f16_f32_e32 v4, v179
	v_cvt_f16_f32_e32 v5, v180
	v_add_f32_e32 v200, v157, v19
	v_add_f32_e32 v181, v157, v16
	v_add_f32_e32 v183, v157, v32
	v_add_f32_e32 v182, v157, v17
	v_add_f32_e32 v184, v157, v33
	v_cvt_f16_f32_e32 v18, v200
	ds_write_b16 v158, v2 offset:3456
	ds_write_b16 v158, v3 offset:8064
	ds_write_b16 v158, v4 offset:3600
	ds_write_b16 v158, v5 offset:8208
	v_cvt_f16_f32_e32 v2, v181
	v_cvt_f16_f32_e32 v3, v183
	v_cvt_f16_f32_e32 v4, v182
	v_cvt_f16_f32_e32 v5, v184
	ds_write_b16 v158, v18 offset:4752
	ds_write_b16 v158, v2 offset:3744
	ds_write_b16 v158, v3 offset:8352
	ds_write_b16 v158, v4 offset:3888
	ds_write_b16 v158, v5 offset:8496
	s_waitcnt lgkmcnt(0)
	s_barrier
	ds_read_b128 v[2:5], v159 offset:34816
	ds_read_b128 v[18:21], v159 offset:43520
	s_waitcnt lgkmcnt(1)
	v_mfma_f32_32x32x16_f16 v[50:65], v[2:5], v[126:129], 0
	s_add_u32 s0, s2, s0
	s_addc_u32 s1, s3, s1
	s_waitcnt lgkmcnt(0)
	v_mfma_f32_32x32x16_f16 v[34:49], v[18:21], v[126:129], 0
	v_mfma_f32_32x32x16_f16 v[2:17], v[2:5], v[122:125], 0
	v_mfma_f32_32x32x16_f16 v[18:33], v[18:21], v[122:125], 0
	ds_read_b128 v[140:143], v159 offset:34848
	ds_read_b128 v[144:147], v159 offset:43552
	s_waitcnt lgkmcnt(1)
	v_mfma_f32_32x32x16_f16 v[50:65], v[140:143], v[118:121], v[50:65]
	s_waitcnt lgkmcnt(0)
	v_mfma_f32_32x32x16_f16 v[34:49], v[144:147], v[118:121], v[34:49]
	v_mfma_f32_32x32x16_f16 v[2:17], v[140:143], v[114:117], v[2:17]
	v_mfma_f32_32x32x16_f16 v[18:33], v[144:147], v[114:117], v[18:33]
	ds_read_b128 v[140:143], v159 offset:34880
	ds_read_b128 v[144:147], v159 offset:43584
	s_waitcnt lgkmcnt(1)
	v_mfma_f32_32x32x16_f16 v[50:65], v[140:143], v[110:113], v[50:65]
	s_waitcnt lgkmcnt(0)
	v_mfma_f32_32x32x16_f16 v[34:49], v[144:147], v[110:113], v[34:49]
	v_mfma_f32_32x32x16_f16 v[2:17], v[140:143], v[106:109], v[2:17]
	v_mfma_f32_32x32x16_f16 v[18:33], v[144:147], v[106:109], v[18:33]
	ds_read_b128 v[140:143], v159 offset:34912
	ds_read_b128 v[144:147], v159 offset:43616
	s_waitcnt lgkmcnt(1)
	v_mfma_f32_32x32x16_f16 v[50:65], v[140:143], v[102:105], v[50:65]
	s_waitcnt lgkmcnt(0)
	v_mfma_f32_32x32x16_f16 v[34:49], v[144:147], v[102:105], v[34:49]
	v_mfma_f32_32x32x16_f16 v[2:17], v[140:143], v[98:101], v[2:17]
	v_mfma_f32_32x32x16_f16 v[18:33], v[144:147], v[98:101], v[18:33]
	ds_read_b128 v[140:143], v159 offset:34944
	ds_read_b128 v[144:147], v159 offset:43648
	s_waitcnt lgkmcnt(1)
	v_mfma_f32_32x32x16_f16 v[50:65], v[140:143], v[94:97], v[50:65]
	s_waitcnt lgkmcnt(0)
	v_mfma_f32_32x32x16_f16 v[34:49], v[144:147], v[94:97], v[34:49]
	v_mfma_f32_32x32x16_f16 v[2:17], v[140:143], v[86:89], v[2:17]
	v_mfma_f32_32x32x16_f16 v[18:33], v[144:147], v[86:89], v[18:33]
	ds_read_b128 v[186:189], v159 offset:34976
	ds_read_b128 v[206:209], v159 offset:43680
	ds_read_b128 v[140:143], v159 offset:35008
	ds_read_b128 v[144:147], v159 offset:43712
	s_waitcnt lgkmcnt(3)
	v_mfma_f32_32x32x16_f16 v[50:65], v[186:189], v[90:93], v[50:65]
	s_waitcnt lgkmcnt(2)
	v_mfma_f32_32x32x16_f16 v[34:49], v[206:209], v[90:93], v[34:49]
	v_mfma_f32_32x32x16_f16 v[2:17], v[186:189], v[78:81], v[2:17]
	v_mfma_f32_32x32x16_f16 v[18:33], v[206:209], v[78:81], v[18:33]
	ds_read_b128 v[186:189], v159 offset:35040
	ds_read_b128 v[206:209], v159 offset:43744
	s_waitcnt lgkmcnt(3)
	v_mfma_f32_32x32x16_f16 v[50:65], v[140:143], v[82:85], v[50:65]
	s_waitcnt lgkmcnt(2)
	v_mfma_f32_32x32x16_f16 v[34:49], v[144:147], v[82:85], v[34:49]
	v_mfma_f32_32x32x16_f16 v[2:17], v[140:143], v[70:73], v[2:17]
	v_lshlrev_b32_e32 v140, 3, v148
	v_and_b32_e32 v185, 0x1f8, v140
	global_load_dwordx2 v[148:149], v185, s[0:1]
	global_load_dwordx2 v[142:143], v185, s[0:1] offset:1024
	global_load_dwordx2 v[140:141], v185, s[0:1] offset:1536
	v_mfma_f32_32x32x16_f16 v[18:33], v[144:147], v[70:73], v[18:33]
	global_load_dwordx2 v[144:145], v185, s[0:1] offset:512
	global_load_dwordx2 v[146:147], v185, s[0:1] offset:2048
	s_waitcnt lgkmcnt(1)
	v_mfma_f32_32x32x16_f16 v[50:65], v[186:189], v[74:77], v[50:65]
	v_mfma_f32_32x32x16_f16 v[2:17], v[186:189], v[66:69], v[2:17]
	s_nop 10
	v_cvt_pk_f16_f32 v57, v56, v57
	v_cvt_pk_f16_f32 v56, v54, v55
	v_cvt_pk_f16_f32 v54, v50, v51
	s_waitcnt vmcnt(12)
	v_cvt_pk_f16_f32 v55, v52, v53
	s_waitcnt vmcnt(8)
	v_perm_b32 v50, v240, v138, s42
	v_perm_b32 v51, v240, v138, s43
	v_perm_b32 v52, v240, v139, s42
	v_perm_b32 v53, v240, v139, s43
	v_perm_b32 v139, v240, v136, s43
	v_pk_add_f16 v50, v50, s5 op_sel_hi:[1,0]
	v_pk_add_f16 v51, v51, s5 op_sel_hi:[1,0]
	v_pk_add_f16 v52, v52, s5 op_sel_hi:[1,0]
	v_pk_add_f16 v53, v53, s5 op_sel_hi:[1,0]
	v_perm_b32 v190, v240, v137, s42
	s_waitcnt lgkmcnt(0)
	v_mfma_f32_32x32x16_f16 v[18:33], v[206:209], v[66:69], v[18:33]
	v_perm_b32 v138, v240, v136, s42
	v_perm_b32 v191, v240, v137, s43
	v_pk_add_f16 v136, v138, s5 op_sel_hi:[1,0]
	v_pk_add_f16 v137, v139, s5 op_sel_hi:[1,0]
	v_pk_add_f16 v138, v190, s5 op_sel_hi:[1,0]
	v_pk_add_f16 v139, v191, s5 op_sel_hi:[1,0]
	v_cvt_pk_f16_f32 v65, v64, v65
	v_cvt_pk_f16_f32 v64, v62, v63
	v_cvt_pk_f16_f32 v63, v60, v61
	v_cvt_pk_f16_f32 v62, v58, v59
	v_mfma_f32_32x32x16_f16 v[34:49], v[206:209], v[74:77], v[34:49]
	v_mfma_f32_32x32x16_f16 v[2:17], v[50:53], v[54:57], v[2:17]
	s_waitcnt vmcnt(7)
	v_perm_b32 v58, v240, v134, s42
	v_perm_b32 v59, v240, v134, s43
	v_perm_b32 v60, v240, v135, s42
	v_perm_b32 v61, v240, v135, s43
	v_pk_add_f16 v58, v58, s5 op_sel_hi:[1,0]
	v_pk_add_f16 v59, v59, s5 op_sel_hi:[1,0]
	v_pk_add_f16 v60, v60, s5 op_sel_hi:[1,0]
	v_pk_add_f16 v61, v61, s5 op_sel_hi:[1,0]
	v_mfma_f32_32x32x16_f16 v[18:33], v[136:139], v[54:57], v[18:33]
	v_perm_b32 v134, v240, v154, s42
	v_perm_b32 v135, v240, v154, s43
	v_perm_b32 v154, v240, v155, s42
	v_perm_b32 v155, v240, v155, s43
	v_pk_add_f16 v210, v134, s5 op_sel_hi:[1,0]
	v_pk_add_f16 v211, v135, s5 op_sel_hi:[1,0]
	v_pk_add_f16 v212, v154, s5 op_sel_hi:[1,0]
	v_pk_add_f16 v213, v155, s5 op_sel_hi:[1,0]
	v_cvt_pk_f16_f32 v41, v40, v41
	v_cvt_pk_f16_f32 v40, v38, v39
	v_cvt_pk_f16_f32 v39, v36, v37
	v_cvt_pk_f16_f32 v38, v34, v35
	v_mfma_f32_32x32x16_f16 v[2:17], v[58:61], v[62:65], v[2:17]
	v_perm_b32 v34, v240, v132, s42
	v_perm_b32 v35, v240, v132, s43
	v_perm_b32 v36, v240, v133, s42
	v_perm_b32 v37, v240, v133, s43
	v_pk_add_f16 v34, v34, s5 op_sel_hi:[1,0]
	v_pk_add_f16 v35, v35, s5 op_sel_hi:[1,0]
	v_pk_add_f16 v36, v36, s5 op_sel_hi:[1,0]
	v_pk_add_f16 v37, v37, s5 op_sel_hi:[1,0]
	s_waitcnt vmcnt(6)
	v_mfma_f32_32x32x16_f16 v[18:33], v[210:213], v[62:65], v[18:33]
	v_perm_b32 v132, v240, v152, s42
	v_perm_b32 v133, v240, v152, s43
	v_perm_b32 v134, v240, v153, s42
	v_perm_b32 v53, v240, v153, s43
	v_pk_add_f16 v50, v132, s5 op_sel_hi:[1,0]
	v_pk_add_f16 v51, v133, s5 op_sel_hi:[1,0]
	v_pk_add_f16 v52, v134, s5 op_sel_hi:[1,0]
	v_pk_add_f16 v53, v53, s5 op_sel_hi:[1,0]
	v_cvt_pk_f16_f32 v49, v48, v49
	v_cvt_pk_f16_f32 v48, v46, v47
	v_cvt_pk_f16_f32 v47, v44, v45
	v_cvt_pk_f16_f32 v46, v42, v43
	v_mfma_f32_32x32x16_f16 v[2:17], v[34:37], v[38:41], v[2:17]
	v_perm_b32 v42, v240, v130, s42
	v_perm_b32 v43, v240, v130, s43
	v_perm_b32 v44, v240, v131, s42
	v_perm_b32 v45, v240, v131, s43
	v_pk_add_f16 v42, v42, s5 op_sel_hi:[1,0]
	v_pk_add_f16 v43, v43, s5 op_sel_hi:[1,0]
	v_pk_add_f16 v44, v44, s5 op_sel_hi:[1,0]
	v_pk_add_f16 v45, v45, s5 op_sel_hi:[1,0]
	s_waitcnt vmcnt(5)
	v_lshlrev_b32_e32 v54, 8, v150
	v_mfma_f32_32x32x16_f16 v[18:33], v[50:53], v[38:41], v[18:33]
	v_lshrrev_b32_e32 v37, 16, v151
	v_lshrrev_b32_e32 v38, 8, v151
	v_perm_b32 v34, v54, v150, s4
	v_perm_b32 v37, v38, v37, s4
	v_or_b32_e32 v34, 0x64006400, v34
	v_perm_b32 v35, v240, v150, s43
	v_perm_b32 v36, v240, v151, s42
	v_or_b32_e32 v37, 0x64006400, v37
	v_pk_add_f16 v34, v34, s5 op_sel_hi:[1,0]
	v_pk_add_f16 v35, v35, s5 op_sel_hi:[1,0]
	v_pk_add_f16 v36, v36, s5 op_sel_hi:[1,0]
	v_pk_add_f16 v37, v37, s5 op_sel_hi:[1,0]
	v_mfma_f32_32x32x16_f16 v[2:17], v[42:45], v[46:49], v[2:17]
	global_load_dwordx2 v[154:155], v185, s[0:1] offset:2560
	global_load_dwordx2 v[152:153], v185, s[0:1] offset:3072
	global_load_dwordx2 v[150:151], v185, s[0:1] offset:3584
	s_or_b32 s0, s8, 6
	s_ashr_i32 s1, s0, 31
	s_lshl_b64 s[0:1], s[0:1], 12
	s_add_u32 s0, s2, s0
	v_mfma_f32_32x32x16_f16 v[18:33], v[34:37], v[46:49], v[18:33]
	s_nop 3
	v_add_f32_e32 v185, v157, v2
	v_add_f32_e32 v187, v157, v3
	v_cvt_f16_f32_e32 v2, v185
	v_cvt_f16_f32_e32 v3, v187
	v_add_f32_e32 v189, v157, v4
	v_add_f32_e32 v191, v157, v5
	ds_write_b16 v158, v2 offset:18432
	s_nop 0
	v_add_f32_e32 v190, v157, v20
	v_add_f32_e32 v192, v157, v21
	ds_write_b16 v158, v3 offset:18576
	v_cvt_f16_f32_e32 v2, v189
	v_cvt_f16_f32_e32 v3, v190
	v_cvt_f16_f32_e32 v4, v191
	v_cvt_f16_f32_e32 v5, v192
	v_add_f32_e32 v194, v157, v6
	v_add_f32_e32 v195, v157, v22
	v_add_f32_e32 v197, v157, v7
	v_add_f32_e32 v199, v157, v23
	ds_write_b16 v158, v2 offset:18720
	ds_write_b16 v158, v3 offset:23328
	ds_write_b16 v158, v4 offset:18864
	ds_write_b16 v158, v5 offset:23472
	v_cvt_f16_f32_e32 v2, v194
	v_cvt_f16_f32_e32 v3, v195
	v_cvt_f16_f32_e32 v4, v197
	v_cvt_f16_f32_e32 v5, v199
	v_add_f32_e32 v201, v157, v8
	v_add_f32_e32 v202, v157, v24
	v_add_f32_e32 v205, v157, v9
	v_add_f32_e32 v206, v157, v25
	ds_write_b16 v158, v2 offset:19584
	ds_write_b16 v158, v3 offset:24192
	ds_write_b16 v158, v4 offset:19728
	ds_write_b16 v158, v5 offset:24336
	v_cvt_f16_f32_e32 v2, v201
	v_cvt_f16_f32_e32 v3, v202
	v_cvt_f16_f32_e32 v4, v205
	v_cvt_f16_f32_e32 v5, v206
	v_add_f32_e32 v207, v157, v10
	v_add_f32_e32 v209, v157, v26
	v_add_f32_e32 v208, v157, v11
	v_add_f32_e32 v210, v157, v27
	ds_write_b16 v158, v2 offset:19872
	ds_write_b16 v158, v3 offset:24480
	ds_write_b16 v158, v4 offset:20016
	ds_write_b16 v158, v5 offset:24624
	v_cvt_f16_f32_e32 v2, v207
	v_cvt_f16_f32_e32 v3, v209
	v_cvt_f16_f32_e32 v4, v208
	v_cvt_f16_f32_e32 v5, v210
	v_add_f32_e32 v211, v157, v12
	v_add_f32_e32 v212, v157, v28
	v_add_f32_e32 v213, v157, v13
	v_add_f32_e32 v214, v157, v29
	ds_write_b16 v158, v2 offset:20736
	ds_write_b16 v158, v3 offset:25344
	ds_write_b16 v158, v4 offset:20880
	ds_write_b16 v158, v5 offset:25488
	v_cvt_f16_f32_e32 v2, v211
	v_cvt_f16_f32_e32 v3, v212
	v_cvt_f16_f32_e32 v4, v213
	v_cvt_f16_f32_e32 v5, v214
	v_add_f32_e32 v215, v157, v14
	v_add_f32_e32 v216, v157, v30
	v_add_f32_e32 v217, v157, v15
	v_add_f32_e32 v218, v157, v31
	ds_write_b16 v158, v2 offset:21024
	ds_write_b16 v158, v3 offset:25632
	ds_write_b16 v158, v4 offset:21168
	ds_write_b16 v158, v5 offset:25776
	v_cvt_f16_f32_e32 v2, v215
	v_cvt_f16_f32_e32 v3, v216
	v_cvt_f16_f32_e32 v4, v217
	v_cvt_f16_f32_e32 v5, v218
	v_add_f32_e32 v186, v157, v18
	v_add_f32_e32 v188, v157, v19
	v_add_f32_e32 v219, v157, v16
	v_add_f32_e32 v221, v157, v32
	v_add_f32_e32 v220, v157, v17
	v_add_f32_e32 v222, v157, v33
	v_cvt_f16_f32_e32 v18, v186
	v_cvt_f16_f32_e32 v19, v188
	ds_write_b16 v158, v2 offset:21888
	ds_write_b16 v158, v3 offset:26496
	ds_write_b16 v158, v4 offset:22032
	ds_write_b16 v158, v5 offset:26640
	v_cvt_f16_f32_e32 v2, v219
	v_cvt_f16_f32_e32 v3, v221
	v_cvt_f16_f32_e32 v4, v220
	v_cvt_f16_f32_e32 v5, v222
	ds_write_b16 v158, v18 offset:23040
	ds_write_b16 v158, v19 offset:23184
	ds_write_b16 v158, v2 offset:22176
	ds_write_b16 v158, v3 offset:26784
	ds_write_b16 v158, v4 offset:22320
	ds_write_b16 v158, v5 offset:26928
	s_waitcnt lgkmcnt(0)
	s_barrier
	ds_read_b128 v[2:5], v159
	ds_read_b128 v[18:21], v159 offset:8704
	s_waitcnt lgkmcnt(1)
	v_mfma_f32_32x32x16_f16 v[50:65], v[2:5], v[126:129], 0
	v_lshlrev_b32_e32 v0, 3, v0
	s_addc_u32 s1, s3, s1
	v_and_b32_e32 v0, 0x1f8, v0
	global_load_dwordx2 v[138:139], v0, s[0:1]
	s_waitcnt lgkmcnt(0)
	v_mfma_f32_32x32x16_f16 v[34:49], v[18:21], v[126:129], 0
	v_mfma_f32_32x32x16_f16 v[2:17], v[2:5], v[122:125], 0
	v_mfma_f32_32x32x16_f16 v[18:33], v[18:21], v[122:125], 0
	ds_read_b128 v[130:133], v159 offset:32
	ds_read_b128 v[134:137], v159 offset:8736
	s_waitcnt lgkmcnt(1)
	v_mfma_f32_32x32x16_f16 v[50:65], v[130:133], v[118:121], v[50:65]
	s_waitcnt lgkmcnt(0)
	v_mfma_f32_32x32x16_f16 v[34:49], v[134:137], v[118:121], v[34:49]
	v_mfma_f32_32x32x16_f16 v[2:17], v[130:133], v[114:117], v[2:17]
	v_mfma_f32_32x32x16_f16 v[18:33], v[134:137], v[114:117], v[18:33]
	ds_read_b128 v[224:227], v159 offset:64
	ds_read_b128 v[228:231], v159 offset:8768
	ds_read_b128 v[130:133], v159 offset:96
	ds_read_b128 v[134:137], v159 offset:8800
	s_waitcnt lgkmcnt(3)
	v_mfma_f32_32x32x16_f16 v[50:65], v[224:227], v[110:113], v[50:65]
	s_waitcnt lgkmcnt(2)
	v_mfma_f32_32x32x16_f16 v[34:49], v[228:231], v[110:113], v[34:49]
	v_mfma_f32_32x32x16_f16 v[2:17], v[224:227], v[106:109], v[2:17]
	v_mfma_f32_32x32x16_f16 v[18:33], v[228:231], v[106:109], v[18:33]
	ds_read_b128 v[224:227], v159 offset:128
	ds_read_b128 v[228:231], v159 offset:8832
	s_waitcnt lgkmcnt(3)
	v_mfma_f32_32x32x16_f16 v[50:65], v[130:133], v[102:105], v[50:65]
	s_waitcnt lgkmcnt(2)
	v_mfma_f32_32x32x16_f16 v[34:49], v[134:137], v[102:105], v[34:49]
	v_mfma_f32_32x32x16_f16 v[2:17], v[130:133], v[98:101], v[2:17]
	v_mfma_f32_32x32x16_f16 v[18:33], v[134:137], v[98:101], v[18:33]
	ds_read_b128 v[130:133], v159 offset:160
	ds_read_b128 v[134:137], v159 offset:8864
	s_waitcnt lgkmcnt(3)
	v_mfma_f32_32x32x16_f16 v[50:65], v[224:227], v[94:97], v[50:65]
	s_waitcnt lgkmcnt(2)
	v_mfma_f32_32x32x16_f16 v[34:49], v[228:231], v[94:97], v[34:49]
	v_mfma_f32_32x32x16_f16 v[2:17], v[224:227], v[86:89], v[2:17]
	v_mfma_f32_32x32x16_f16 v[18:33], v[228:231], v[86:89], v[18:33]
	ds_read_b128 v[224:227], v159 offset:192
	ds_read_b128 v[228:231], v159 offset:8896
	s_waitcnt lgkmcnt(3)
	v_mfma_f32_32x32x16_f16 v[50:65], v[130:133], v[90:93], v[50:65]
	s_waitcnt lgkmcnt(2)
	v_mfma_f32_32x32x16_f16 v[34:49], v[134:137], v[90:93], v[34:49]
	v_mfma_f32_32x32x16_f16 v[2:17], v[130:133], v[78:81], v[2:17]
	v_add_f32_e32 v130, v193, v196
	v_add_f32_e32 v130, 0, v130
	v_add_f32_e32 v132, v198, v200
	v_add_f32_e32 v130, v132, v130
	v_mul_f32_e32 v132, v200, v200
	v_fmac_f32_e32 v132, v198, v198
	v_mul_f32_e32 v131, v196, v196
	v_mfma_f32_32x32x16_f16 v[18:33], v[134:137], v[78:81], v[18:33]
	ds_read_b128 v[232:235], v159 offset:224
	ds_read_b128 v[236:239], v159 offset:8928
	v_fmac_f32_e32 v131, v193, v193
	v_add_f32_e32 v131, v131, v132
	v_add_f32_e32 v132, v203, v204
	v_add_f32_e32 v130, v132, v130
	v_mul_f32_e32 v132, v204, v204
	s_waitcnt lgkmcnt(3)
	v_mfma_f32_32x32x16_f16 v[50:65], v[224:227], v[82:85], v[50:65]
	v_fmac_f32_e32 v132, v203, v203
	v_add_f32_e32 v193, v132, v131
	v_add_f32_e32 v131, v1, v160
	v_add_f32_e32 v196, v131, v130
	global_load_dwordx2 v[134:135], v0, s[0:1] offset:512
	global_load_dwordx2 v[132:133], v0, s[0:1] offset:1024
	global_load_dwordx2 v[130:131], v0, s[0:1] offset:1536
	s_waitcnt lgkmcnt(2)
	v_mfma_f32_32x32x16_f16 v[34:49], v[228:231], v[82:85], v[34:49]
	global_load_dwordx2 v[136:137], v0, s[0:1] offset:2048
	v_mfma_f32_32x32x16_f16 v[2:17], v[224:227], v[70:73], v[2:17]
	v_mfma_f32_32x32x16_f16 v[18:33], v[228:231], v[70:73], v[18:33]
	s_waitcnt lgkmcnt(1)
	v_mfma_f32_32x32x16_f16 v[50:65], v[232:235], v[74:77], v[50:65]
	v_mfma_f32_32x32x16_f16 v[2:17], v[232:235], v[66:69], v[2:17]
	s_nop 10
	v_cvt_pk_f16_f32 v57, v56, v57
	v_cvt_pk_f16_f32 v56, v54, v55
	v_cvt_pk_f16_f32 v54, v50, v51
	s_waitcnt vmcnt(12)
	v_lshlrev_b32_e32 v50, 8, v148
	v_cvt_pk_f16_f32 v55, v52, v53
	v_perm_b32 v50, v50, v148, s4
	v_lshrrev_b32_e32 v51, 16, v148
	v_lshrrev_b32_e32 v52, 8, v148
	v_lshrrev_b32_e32 v53, 16, v149
	v_lshrrev_b32_e32 v148, 8, v149
	v_perm_b32 v51, v52, v51, s4
	v_lshlrev_b32_e32 v52, 8, v149
	v_perm_b32 v53, v148, v53, s4
	s_waitcnt vmcnt(8)
	v_perm_b32 v52, v52, v149, s4
	v_perm_b32 v149, v240, v146, s43
	v_perm_b32 v198, v240, v147, s42
	s_waitcnt lgkmcnt(0)
	v_mfma_f32_32x32x16_f16 v[18:33], v[236:239], v[66:69], v[18:33]
	v_or_b32_e32 v50, 0x64006400, v50
	v_or_b32_e32 v51, 0x64006400, v51
	v_or_b32_e32 v52, 0x64006400, v52
	v_or_b32_e32 v53, 0x64006400, v53
	v_pk_add_f16 v50, v50, s5 op_sel_hi:[1,0]
	v_pk_add_f16 v51, v51, s5 op_sel_hi:[1,0]
	v_pk_add_f16 v52, v52, s5 op_sel_hi:[1,0]
	v_pk_add_f16 v53, v53, s5 op_sel_hi:[1,0]
	v_perm_b32 v148, v240, v146, s42
	v_perm_b32 v200, v240, v147, s43
	v_pk_add_f16 v146, v148, s5 op_sel_hi:[1,0]
	v_pk_add_f16 v147, v149, s5 op_sel_hi:[1,0]
	v_pk_add_f16 v148, v198, s5 op_sel_hi:[1,0]
	v_pk_add_f16 v149, v200, s5 op_sel_hi:[1,0]
	v_cvt_pk_f16_f32 v65, v64, v65
	v_cvt_pk_f16_f32 v64, v62, v63
	v_cvt_pk_f16_f32 v62, v58, v59
	v_cvt_pk_f16_f32 v63, v60, v61
	s_waitcnt vmcnt(7)
	v_mfma_f32_32x32x16_f16 v[34:49], v[236:239], v[74:77], v[34:49]
	v_mfma_f32_32x32x16_f16 v[2:17], v[50:53], v[54:57], v[2:17]
	v_perm_b32 v58, v240, v144, s42
	v_perm_b32 v59, v240, v144, s43
	v_perm_b32 v60, v240, v145, s42
	v_perm_b32 v61, v240, v145, s43
	v_mfma_f32_32x32x16_f16 v[18:33], v[146:149], v[54:57], v[18:33]
	v_pk_add_f16 v58, v58, s5 op_sel_hi:[1,0]
	v_pk_add_f16 v59, v59, s5 op_sel_hi:[1,0]
	v_pk_add_f16 v60, v60, s5 op_sel_hi:[1,0]
	v_pk_add_f16 v61, v61, s5 op_sel_hi:[1,0]
	v_perm_b32 v144, v240, v154, s42
	v_perm_b32 v145, v240, v154, s43
	v_perm_b32 v154, v240, v155, s42
	v_perm_b32 v155, v240, v155, s43
	v_pk_add_f16 v224, v144, s5 op_sel_hi:[1,0]
	v_pk_add_f16 v225, v145, s5 op_sel_hi:[1,0]
	v_pk_add_f16 v226, v154, s5 op_sel_hi:[1,0]
	v_pk_add_f16 v227, v155, s5 op_sel_hi:[1,0]
	v_cvt_pk_f16_f32 v41, v40, v41
	v_cvt_pk_f16_f32 v40, v38, v39
	v_cvt_pk_f16_f32 v39, v36, v37
	v_cvt_pk_f16_f32 v38, v34, v35
	s_waitcnt vmcnt(6)
	v_mfma_f32_32x32x16_f16 v[2:17], v[58:61], v[62:65], v[2:17]
	v_perm_b32 v34, v240, v142, s42
	v_perm_b32 v35, v240, v142, s43
	v_mfma_f32_32x32x16_f16 v[18:33], v[224:227], v[62:65], v[18:33]
	v_perm_b32 v36, v240, v143, s42
	v_perm_b32 v37, v240, v143, s43
	v_pk_add_f16 v34, v34, s5 op_sel_hi:[1,0]
	v_pk_add_f16 v35, v35, s5 op_sel_hi:[1,0]
	v_pk_add_f16 v36, v36, s5 op_sel_hi:[1,0]
	v_pk_add_f16 v37, v37, s5 op_sel_hi:[1,0]
	v_perm_b32 v142, v240, v152, s42
	v_perm_b32 v143, v240, v152, s43
	v_perm_b32 v144, v240, v153, s42
	v_perm_b32 v53, v240, v153, s43
	v_pk_add_f16 v50, v142, s5 op_sel_hi:[1,0]
	v_pk_add_f16 v51, v143, s5 op_sel_hi:[1,0]
	v_pk_add_f16 v52, v144, s5 op_sel_hi:[1,0]
	v_pk_add_f16 v53, v53, s5 op_sel_hi:[1,0]
	v_cvt_pk_f16_f32 v49, v48, v49
	v_cvt_pk_f16_f32 v48, v46, v47
	v_cvt_pk_f16_f32 v47, v44, v45
	v_cvt_pk_f16_f32 v46, v42, v43
	v_mfma_f32_32x32x16_f16 v[2:17], v[34:37], v[38:41], v[2:17]
	s_waitcnt vmcnt(5)
	v_lshlrev_b32_e32 v54, 8, v150
	v_mfma_f32_32x32x16_f16 v[18:33], v[50:53], v[38:41], v[18:33]
	v_lshrrev_b32_e32 v37, 16, v151
	v_lshrrev_b32_e32 v38, 8, v151
	v_perm_b32 v34, v54, v150, s4
	v_perm_b32 v37, v38, v37, s4
	v_perm_b32 v42, v240, v140, s42
	v_perm_b32 v43, v240, v140, s43
	v_perm_b32 v44, v240, v141, s42
	v_perm_b32 v45, v240, v141, s43
	v_or_b32_e32 v34, 0x64006400, v34
	v_perm_b32 v35, v240, v150, s43
	v_perm_b32 v36, v240, v151, s42
	v_or_b32_e32 v37, 0x64006400, v37
	v_pk_add_f16 v42, v42, s5 op_sel_hi:[1,0]
	v_pk_add_f16 v43, v43, s5 op_sel_hi:[1,0]
	v_pk_add_f16 v44, v44, s5 op_sel_hi:[1,0]
	v_pk_add_f16 v45, v45, s5 op_sel_hi:[1,0]
	v_pk_add_f16 v34, v34, s5 op_sel_hi:[1,0]
	v_pk_add_f16 v35, v35, s5 op_sel_hi:[1,0]
	v_pk_add_f16 v36, v36, s5 op_sel_hi:[1,0]
	v_pk_add_f16 v37, v37, s5 op_sel_hi:[1,0]
	v_mfma_f32_32x32x16_f16 v[2:17], v[42:45], v[46:49], v[2:17]
	global_load_dwordx2 v[142:143], v0, s[0:1] offset:2560
	global_load_dwordx2 v[140:141], v0, s[0:1] offset:3072
	global_load_dwordx2 v[64:65], v0, s[0:1] offset:3584
	v_mfma_f32_32x32x16_f16 v[18:33], v[34:37], v[46:49], v[18:33]
	s_nop 7
	v_add_f32_e32 v146, v157, v2
	v_add_f32_e32 v148, v157, v3
	v_cvt_f16_f32_e32 v0, v146
	v_cvt_f16_f32_e32 v3, v148
	v_add_f32_e32 v150, v157, v4
	v_add_f32_e32 v152, v157, v5
	ds_write_b16 v158, v0
	v_add_f32_e32 v147, v157, v18
	v_cvt_f16_f32_e32 v2, v147
	v_add_f32_e32 v151, v157, v20
	v_add_f32_e32 v153, v157, v21
	ds_write_b16 v158, v3 offset:144
	ds_write_b16 v158, v2 offset:4608
	v_cvt_f16_f32_e32 v0, v150
	v_cvt_f16_f32_e32 v2, v151
	v_cvt_f16_f32_e32 v3, v152
	v_cvt_f16_f32_e32 v4, v153
	v_add_f32_e32 v154, v157, v6
	v_add_f32_e32 v155, v157, v22
	v_add_f32_e32 v198, v157, v7
	v_add_f32_e32 v200, v157, v23
	ds_write_b16 v158, v0 offset:288
	ds_write_b16 v158, v2 offset:4896
	ds_write_b16 v158, v3 offset:432
	ds_write_b16 v158, v4 offset:5040
	v_cvt_f16_f32_e32 v0, v154
	v_cvt_f16_f32_e32 v2, v155
	v_cvt_f16_f32_e32 v3, v198
	v_cvt_f16_f32_e32 v4, v200
	v_add_f32_e32 v203, v157, v8
	v_add_f32_e32 v204, v157, v24
	v_add_f32_e32 v223, v157, v9
	v_add_f32_e32 v224, v157, v25
	ds_write_b16 v158, v0 offset:1152
	ds_write_b16 v158, v2 offset:5760
	ds_write_b16 v158, v3 offset:1296
	ds_write_b16 v158, v4 offset:5904
	v_cvt_f16_f32_e32 v0, v203
	v_cvt_f16_f32_e32 v2, v204
	v_cvt_f16_f32_e32 v3, v223
	v_cvt_f16_f32_e32 v4, v224
	v_add_f32_e32 v225, v157, v10
	v_add_f32_e32 v226, v157, v26
	v_add_f32_e32 v227, v157, v11
	v_add_f32_e32 v228, v157, v27
	ds_write_b16 v158, v0 offset:1440
	ds_write_b16 v158, v2 offset:6048
	ds_write_b16 v158, v3 offset:1584
	ds_write_b16 v158, v4 offset:6192
	v_cvt_f16_f32_e32 v0, v225
	v_cvt_f16_f32_e32 v2, v226
	v_cvt_f16_f32_e32 v3, v227
	v_cvt_f16_f32_e32 v4, v228
	v_add_f32_e32 v229, v157, v12
	v_add_f32_e32 v230, v157, v28
	v_add_f32_e32 v231, v157, v13
	v_add_f32_e32 v232, v157, v29
	ds_write_b16 v158, v0 offset:2304
	ds_write_b16 v158, v2 offset:6912
	ds_write_b16 v158, v3 offset:2448
	ds_write_b16 v158, v4 offset:7056
	v_cvt_f16_f32_e32 v0, v229
	v_cvt_f16_f32_e32 v2, v230
	v_cvt_f16_f32_e32 v3, v231
	v_cvt_f16_f32_e32 v4, v232
	v_add_f32_e32 v233, v157, v14
	v_add_f32_e32 v234, v157, v30
	v_add_f32_e32 v235, v157, v15
	v_add_f32_e32 v236, v157, v31
	ds_write_b16 v158, v0 offset:2592
	ds_write_b16 v158, v2 offset:7200
	ds_write_b16 v158, v3 offset:2736
	ds_write_b16 v158, v4 offset:7344
	v_cvt_f16_f32_e32 v0, v233
	v_cvt_f16_f32_e32 v2, v234
	v_cvt_f16_f32_e32 v3, v235
	v_cvt_f16_f32_e32 v4, v236
	v_add_f32_e32 v149, v157, v19
	v_add_f32_e32 v237, v157, v16
	v_add_f32_e32 v238, v157, v32
	v_add_f32_e32 v144, v157, v17
	v_add_f32_e32 v145, v157, v33
	v_cvt_f16_f32_e32 v18, v149
	ds_write_b16 v158, v0 offset:3456
	ds_write_b16 v158, v2 offset:8064
	ds_write_b16 v158, v3 offset:3600
	ds_write_b16 v158, v4 offset:8208
	v_cvt_f16_f32_e32 v0, v237
	v_cvt_f16_f32_e32 v2, v238
	v_cvt_f16_f32_e32 v3, v144
	v_cvt_f16_f32_e32 v4, v145
	ds_write_b16 v158, v18 offset:4752
	ds_write_b16 v158, v0 offset:3744
	ds_write_b16 v158, v2 offset:8352
	ds_write_b16 v158, v3 offset:3888
	ds_write_b16 v158, v4 offset:8496
	s_waitcnt lgkmcnt(0)
	s_barrier
	ds_read_b128 v[16:19], v159 offset:43520
	s_waitcnt lgkmcnt(0)
	v_mfma_f32_32x32x16_f16 v[32:47], v[16:19], v[126:129], 0
	ds_read_b128 v[2:5], v159 offset:34816
	v_mul_f32_e32 v0, v160, v160
	v_fmac_f32_e32 v0, v1, v1
	v_mul_f32_e32 v6, v162, v162
	v_add_f32_e32 v0, v0, v193
	v_add_f32_e32 v1, v161, v162
	v_fmac_f32_e32 v6, v161, v161
	s_waitcnt lgkmcnt(0)
	v_mfma_f32_32x32x16_f16 v[48:63], v[2:5], v[126:129], 0
	ds_read_b128 v[126:129], v159 offset:34848
	v_add_f32_e32 v1, v1, v196
	v_add_f32_e32 v0, v6, v0
	v_add_f32_e32 v6, v163, v164
	v_add_f32_e32 v1, v6, v1
	v_mul_f32_e32 v6, v164, v164
	v_fmac_f32_e32 v6, v163, v163
	v_add_f32_e32 v0, v6, v0
	v_add_f32_e32 v6, v165, v166
	v_add_f32_e32 v1, v6, v1
	v_mul_f32_e32 v6, v166, v166
	v_fmac_f32_e32 v6, v165, v165
	v_add_f32_e32 v20, v6, v0
	v_add_f32_e32 v0, v167, v168
	v_add_f32_e32 v21, v0, v1
	s_waitcnt lgkmcnt(0)
	v_mfma_f32_32x32x16_f16 v[48:63], v[126:129], v[118:121], v[48:63]
	v_mul_f32_e32 v22, v168, v168
	v_fmac_f32_e32 v22, v167, v167
	v_add_f32_e32 v160, v22, v20
	v_add_f32_e32 v20, v169, v170
	v_mul_f32_e32 v162, v170, v170
	v_add_f32_e32 v161, v20, v21
	v_fmac_f32_e32 v162, v169, v169
	v_mfma_f32_32x32x16_f16 v[0:15], v[2:5], v[122:125], 0
	v_mfma_f32_32x32x16_f16 v[0:15], v[126:129], v[114:117], v[0:15]
	v_mfma_f32_32x32x16_f16 v[16:31], v[16:19], v[122:125], 0
	v_add_f32_e32 v123, v171, v172
	v_add_f32_e32 v122, v162, v160
	v_add_f32_e32 v160, v123, v161
	v_mul_f32_e32 v123, v172, v172
	v_fmac_f32_e32 v123, v171, v171
	v_add_f32_e32 v161, v123, v122
	ds_read_b128 v[122:125], v159 offset:43552
	v_add_f32_e32 v162, v173, v174
	v_add_f32_e32 v160, v162, v160
	v_mul_f32_e32 v162, v174, v174
	v_fmac_f32_e32 v162, v173, v173
	s_waitcnt lgkmcnt(0)
	v_mfma_f32_32x32x16_f16 v[32:47], v[122:125], v[118:121], v[32:47]
	v_mul_f32_e32 v118, v176, v176
	v_add_f32_e32 v161, v162, v161
	v_add_f32_e32 v162, v175, v176
	v_fmac_f32_e32 v118, v175, v175
	v_mul_f32_e32 v120, v178, v178
	v_add_f32_e32 v160, v162, v160
	v_add_f32_e32 v118, v118, v161
	v_add_f32_e32 v119, v177, v178
	v_fmac_f32_e32 v120, v177, v177
	v_add_f32_e32 v119, v119, v160
	v_add_f32_e32 v118, v120, v118
	v_add_f32_e32 v120, v179, v180
	v_add_f32_e32 v126, v120, v119
	v_mul_f32_e32 v119, v180, v180
	v_mfma_f32_32x32x16_f16 v[16:31], v[122:125], v[114:117], v[16:31]
	v_add_f32_e32 v114, v181, v183
	v_fmac_f32_e32 v119, v179, v179
	v_add_f32_e32 v122, v114, v126
	v_mul_f32_e32 v114, v183, v183
	v_add_f32_e32 v127, v119, v118
	v_fmac_f32_e32 v114, v181, v181
	ds_read_b128 v[118:121], v159 offset:34880
	v_add_f32_e32 v123, v114, v127
	ds_read_b128 v[114:117], v159 offset:43584
	v_add_f32_e32 v124, v182, v184
	v_add_f32_e32 v122, v124, v122
	v_mul_f32_e32 v124, v184, v184
	v_fmac_f32_e32 v124, v182, v182
	s_waitcnt lgkmcnt(1)
	v_mfma_f32_32x32x16_f16 v[48:63], v[118:121], v[110:113], v[48:63]
	v_add_f32_e32 v123, v124, v123
	v_add_f32_e32 v124, v185, v186
	v_add_f32_e32 v124, 0, v124
	v_add_f32_e32 v122, 0, v122
	s_waitcnt lgkmcnt(0)
	v_mfma_f32_32x32x16_f16 v[32:47], v[114:117], v[110:113], v[32:47]
	v_mul_f32_e32 v110, v186, v186
	v_mul_f32_e32 v112, v188, v188
	v_fmac_f32_e32 v110, v185, v185
	v_add_f32_e32 v111, v187, v188
	v_fmac_f32_e32 v112, v187, v187
	v_add_f32_e32 v111, v111, v124
	v_add_f32_e32 v110, v110, v112
	v_add_f32_e32 v112, v189, v190
	v_mfma_f32_32x32x16_f16 v[0:15], v[118:121], v[106:109], v[0:15]
	v_add_f32_e32 v118, v112, v111
	v_mul_f32_e32 v111, v190, v190
	v_fmac_f32_e32 v111, v189, v189
	v_add_f32_e32 v119, v111, v110
	v_add_f32_e32 v120, v191, v192
	ds_read_b128 v[110:113], v159 offset:34912
	v_mfma_f32_32x32x16_f16 v[16:31], v[114:117], v[106:109], v[16:31]
	v_mul_f32_e32 v107, v192, v192
	v_fmac_f32_e32 v107, v191, v191
	v_add_f32_e32 v106, v120, v118
	v_add_f32_e32 v114, v107, v119
	v_add_f32_e32 v107, v194, v195
	v_add_f32_e32 v115, v107, v106
	ds_read_b128 v[106:109], v159 offset:43616
	v_mul_f32_e32 v116, v195, v195
	v_fmac_f32_e32 v116, v194, v194
	v_add_f32_e32 v114, v116, v114
	v_add_f32_e32 v116, v197, v199
	v_add_f32_e32 v115, v116, v115
	v_mul_f32_e32 v116, v199, v199
	s_waitcnt lgkmcnt(1)
	v_mfma_f32_32x32x16_f16 v[48:63], v[110:113], v[102:105], v[48:63]
	v_fmac_f32_e32 v116, v197, v197
	s_waitcnt lgkmcnt(0)
	v_mfma_f32_32x32x16_f16 v[32:47], v[106:109], v[102:105], v[32:47]
	v_mul_f32_e32 v104, v202, v202
	v_add_f32_e32 v102, v116, v114
	v_add_f32_e32 v103, v201, v202
	v_fmac_f32_e32 v104, v201, v201
	v_add_f32_e32 v103, v103, v115
	v_add_f32_e32 v102, v104, v102
	v_add_f32_e32 v104, v205, v206
	v_add_f32_e32 v103, v104, v103
	v_mul_f32_e32 v104, v206, v206
	v_mfma_f32_32x32x16_f16 v[0:15], v[110:113], v[98:101], v[0:15]
	v_fmac_f32_e32 v104, v205, v205
	v_add_f32_e32 v110, v104, v102
	v_add_f32_e32 v102, v207, v209
	v_add_f32_e32 v111, v102, v103
	ds_read_b128 v[102:105], v159 offset:34944
	v_mfma_f32_32x32x16_f16 v[16:31], v[106:109], v[98:101], v[16:31]
	v_mul_f32_e32 v98, v209, v209
	v_fmac_f32_e32 v98, v207, v207
	v_add_f32_e32 v106, v98, v110
	v_add_f32_e32 v98, v208, v210
	v_add_f32_e32 v107, v98, v111
	ds_read_b128 v[98:101], v159 offset:43648
	v_mul_f32_e32 v108, v210, v210
	v_fmac_f32_e32 v108, v208, v208
	v_add_f32_e32 v106, v108, v106
	v_add_f32_e32 v108, v211, v212
	s_waitcnt lgkmcnt(1)
	v_mfma_f32_32x32x16_f16 v[48:63], v[102:105], v[94:97], v[48:63]
	v_add_f32_e32 v107, v108, v107
	v_mul_f32_e32 v108, v212, v212
	v_fmac_f32_e32 v108, v211, v211
	v_add_f32_e32 v106, v108, v106
	s_waitcnt lgkmcnt(0)
	v_mfma_f32_32x32x16_f16 v[32:47], v[98:101], v[94:97], v[32:47]
	v_add_f32_e32 v94, v213, v214
	v_add_f32_e32 v94, v94, v107
	v_mul_f32_e32 v95, v214, v214
	v_add_f32_e32 v96, v215, v216
	v_fmac_f32_e32 v95, v213, v213
	v_add_f32_e32 v94, v96, v94
	v_mul_f32_e32 v96, v216, v216
	v_add_f32_e32 v95, v95, v106
	v_fmac_f32_e32 v96, v215, v215
	v_mfma_f32_32x32x16_f16 v[0:15], v[102:105], v[86:89], v[0:15]
	v_add_f32_e32 v102, v96, v95
	v_add_f32_e32 v95, v217, v218
	v_add_f32_e32 v103, v95, v94
	ds_read_b128 v[94:97], v159 offset:34976
	v_mul_f32_e32 v104, v218, v218
	v_fmac_f32_e32 v104, v217, v217
	v_mfma_f32_32x32x16_f16 v[16:31], v[98:101], v[86:89], v[16:31]
	v_add_f32_e32 v86, v219, v221
	v_add_f32_e32 v99, v86, v103
	ds_read_b128 v[86:89], v159 offset:43680
	v_mul_f32_e32 v100, v221, v221
	v_add_f32_e32 v98, v104, v102
	v_fmac_f32_e32 v100, v219, v219
	v_add_f32_e32 v98, v100, v98
	s_waitcnt lgkmcnt(1)
	v_mfma_f32_32x32x16_f16 v[48:63], v[94:97], v[90:93], v[48:63]
	v_add_f32_e32 v100, v220, v222
	v_add_f32_e32 v99, v100, v99
	v_mul_f32_e32 v100, v222, v222
	v_fmac_f32_e32 v100, v220, v220
	v_add_f32_e32 v98, v100, v98
	v_add_f32_e32 v98, v123, v98
	v_add_f32_e32 v99, v122, v99
	s_waitcnt lgkmcnt(0)
	v_mfma_f32_32x32x16_f16 v[32:47], v[86:89], v[90:93], v[32:47]
	v_add_f32_e32 v90, v146, v147
	v_add_f32_e32 v90, 0, v90
	v_add_f32_e32 v92, v148, v149
	v_mul_f32_e32 v91, v147, v147
	v_add_f32_e32 v90, v92, v90
	v_mul_f32_e32 v92, v149, v149
	v_fmac_f32_e32 v91, v146, v146
	v_fmac_f32_e32 v92, v148, v148
	v_mfma_f32_32x32x16_f16 v[0:15], v[94:97], v[78:81], v[0:15]
	v_add_f32_e32 v94, v91, v92
	v_add_f32_e32 v91, v150, v151
	v_add_f32_e32 v95, v91, v90
	ds_read_b128 v[90:93], v159 offset:35008
	v_mul_f32_e32 v96, v151, v151
	v_fmac_f32_e32 v96, v150, v150
	v_mfma_f32_32x32x16_f16 v[16:31], v[86:89], v[78:81], v[16:31]
	v_add_f32_e32 v78, v152, v153
	v_add_f32_e32 v87, v78, v95
	ds_read_b128 v[78:81], v159 offset:43712
	v_mul_f32_e32 v88, v153, v153
	v_add_f32_e32 v86, v96, v94
	v_fmac_f32_e32 v88, v152, v152
	v_add_f32_e32 v86, v88, v86
	v_add_f32_e32 v88, v154, v155
	v_add_f32_e32 v87, v88, v87
	v_mul_f32_e32 v88, v155, v155
	v_fmac_f32_e32 v88, v154, v154
	v_add_f32_e32 v86, v88, v86
	v_add_f32_e32 v88, v198, v200
	s_waitcnt lgkmcnt(1)
	v_mfma_f32_32x32x16_f16 v[48:63], v[90:93], v[82:85], v[48:63]
	s_waitcnt lgkmcnt(0)
	v_mfma_f32_32x32x16_f16 v[32:47], v[78:81], v[82:85], v[32:47]
	v_add_f32_e32 v82, v88, v87
	v_mul_f32_e32 v83, v200, v200
	v_add_f32_e32 v84, v203, v204
	v_fmac_f32_e32 v83, v198, v198
	v_add_f32_e32 v82, v84, v82
	v_mul_f32_e32 v84, v204, v204
	v_add_f32_e32 v83, v83, v86
	v_fmac_f32_e32 v84, v203, v203
	v_add_f32_e32 v86, v84, v83
	v_add_f32_e32 v83, v223, v224
	v_mfma_f32_32x32x16_f16 v[0:15], v[90:93], v[70:73], v[0:15]
	v_add_f32_e32 v87, v83, v82
	v_mul_f32_e32 v88, v224, v224
	v_fmac_f32_e32 v88, v223, v223
	ds_read_b128 v[82:85], v159 offset:35040
	v_mfma_f32_32x32x16_f16 v[16:31], v[78:81], v[70:73], v[16:31]
	v_add_f32_e32 v71, v225, v226
	v_add_f32_e32 v78, v71, v87
	v_mul_f32_e32 v71, v226, v226
	v_add_f32_e32 v70, v88, v86
	v_fmac_f32_e32 v71, v225, v225
	v_add_f32_e32 v79, v71, v70
	ds_read_b128 v[70:73], v159 offset:43744
	s_waitcnt lgkmcnt(1)
	v_mfma_f32_32x32x16_f16 v[48:63], v[82:85], v[74:77], v[48:63]
	v_add_f32_e32 v80, v227, v228
	v_add_f32_e32 v78, v80, v78
	v_mul_f32_e32 v80, v228, v228
	v_fmac_f32_e32 v80, v227, v227
	v_add_f32_e32 v79, v80, v79
	v_add_f32_e32 v80, v229, v230
	v_add_f32_e32 v78, v80, v78
	v_mfma_f32_32x32x16_f16 v[0:15], v[82:85], v[66:69], v[0:15]
	s_nop 3
	v_cvt_pk_f16_f32 v55, v54, v55
	v_cvt_pk_f16_f32 v54, v52, v53
	v_cvt_pk_f16_f32 v53, v50, v51
	v_cvt_pk_f16_f32 v52, v48, v49
	s_waitcnt vmcnt(3)
	s_waitcnt lgkmcnt(0)
	v_mfma_f32_32x32x16_f16 v[16:31], v[70:73], v[66:69], v[16:31]
	v_lshrrev_b32_e32 v69, 16, v139
	v_mfma_f32_32x32x16_f16 v[32:47], v[70:73], v[74:77], v[32:47]
	v_lshrrev_b32_e32 v70, 8, v139
	v_perm_b32 v69, v70, v69, s4
	v_perm_b32 v66, v240, v138, s42
	v_perm_b32 v67, v240, v138, s43
	v_perm_b32 v68, v240, v139, s42
	v_or_b32_e32 v69, 0x64006400, v69
	v_pk_add_f16 v66, v66, s5 op_sel_hi:[1,0]
	v_pk_add_f16 v67, v67, s5 op_sel_hi:[1,0]
	v_pk_add_f16 v68, v68, s5 op_sel_hi:[1,0]
	v_pk_add_f16 v69, v69, s5 op_sel_hi:[1,0]
	s_nop 1
	v_mfma_f32_32x32x16_f16 v[0:15], v[66:69], v[52:55], v[0:15]
	v_perm_b32 v48, v240, v136, s42
	v_perm_b32 v49, v240, v136, s43
	v_perm_b32 v50, v240, v137, s42
	v_perm_b32 v51, v240, v137, s43
	v_pk_add_f16 v48, v48, s5 op_sel_hi:[1,0]
	v_pk_add_f16 v49, v49, s5 op_sel_hi:[1,0]
	v_pk_add_f16 v50, v50, s5 op_sel_hi:[1,0]
	v_pk_add_f16 v51, v51, s5 op_sel_hi:[1,0]
	v_cvt_pk_f16_f32 v39, v38, v39
	v_cvt_pk_f16_f32 v38, v36, v37
	v_mfma_f32_32x32x16_f16 v[16:31], v[48:51], v[52:55], v[16:31]
	v_perm_b32 v48, v240, v134, s42
	v_perm_b32 v49, v240, v134, s43
	v_perm_b32 v50, v240, v135, s42
	v_perm_b32 v51, v240, v135, s43
	v_pk_add_f16 v48, v48, s5 op_sel_hi:[1,0]
	v_pk_add_f16 v49, v49, s5 op_sel_hi:[1,0]
	v_pk_add_f16 v50, v50, s5 op_sel_hi:[1,0]
	v_pk_add_f16 v51, v51, s5 op_sel_hi:[1,0]
	v_cvt_pk_f16_f32 v55, v62, v63
	v_cvt_pk_f16_f32 v54, v60, v61
	v_cvt_pk_f16_f32 v53, v58, v59
	v_cvt_pk_f16_f32 v52, v56, v57
	s_waitcnt vmcnt(2)
	v_cvt_pk_f16_f32 v37, v34, v35
	v_mfma_f32_32x32x16_f16 v[0:15], v[48:51], v[52:55], v[0:15]
	v_perm_b32 v48, v240, v142, s42
	v_perm_b32 v49, v240, v142, s43
	v_perm_b32 v50, v240, v143, s42
	v_perm_b32 v51, v240, v143, s43
	v_pk_add_f16 v48, v48, s5 op_sel_hi:[1,0]
	v_pk_add_f16 v49, v49, s5 op_sel_hi:[1,0]
	v_pk_add_f16 v50, v50, s5 op_sel_hi:[1,0]
	v_pk_add_f16 v51, v51, s5 op_sel_hi:[1,0]
	v_cvt_pk_f16_f32 v36, v32, v33
	s_waitcnt vmcnt(1)
	v_mfma_f32_32x32x16_f16 v[16:31], v[48:51], v[52:55], v[16:31]
	v_lshrrev_b32_e32 v51, 16, v133
	v_lshrrev_b32_e32 v52, 8, v133
	v_perm_b32 v51, v52, v51, s4
	v_perm_b32 v48, v240, v132, s42
	v_perm_b32 v49, v240, v132, s43
	v_perm_b32 v50, v240, v133, s42
	v_or_b32_e32 v51, 0x64006400, v51
	v_pk_add_f16 v48, v48, s5 op_sel_hi:[1,0]
	v_pk_add_f16 v49, v49, s5 op_sel_hi:[1,0]
	v_pk_add_f16 v50, v50, s5 op_sel_hi:[1,0]
	v_pk_add_f16 v51, v51, s5 op_sel_hi:[1,0]
	s_nop 1
	v_mfma_f32_32x32x16_f16 v[0:15], v[48:51], v[36:39], v[0:15]
	v_perm_b32 v32, v240, v140, s42
	v_perm_b32 v33, v240, v140, s43
	v_perm_b32 v34, v240, v141, s42
	v_perm_b32 v35, v240, v141, s43
	v_pk_add_f16 v32, v32, s5 op_sel_hi:[1,0]
	v_pk_add_f16 v33, v33, s5 op_sel_hi:[1,0]
	v_pk_add_f16 v34, v34, s5 op_sel_hi:[1,0]
	v_pk_add_f16 v35, v35, s5 op_sel_hi:[1,0]
	v_mul_f32_e32 v74, v230, v230
	v_fmac_f32_e32 v74, v229, v229
	v_mfma_f32_32x32x16_f16 v[16:31], v[32:35], v[36:39], v[16:31]
	v_perm_b32 v32, v240, v130, s42
	v_perm_b32 v33, v240, v130, s43
	v_perm_b32 v34, v240, v131, s42
	v_perm_b32 v35, v240, v131, s43
	v_pk_add_f16 v32, v32, s5 op_sel_hi:[1,0]
	v_pk_add_f16 v33, v33, s5 op_sel_hi:[1,0]
	v_pk_add_f16 v34, v34, s5 op_sel_hi:[1,0]
	v_pk_add_f16 v35, v35, s5 op_sel_hi:[1,0]
	v_cvt_pk_f16_f32 v39, v46, v47
	v_cvt_pk_f16_f32 v38, v44, v45
	v_cvt_pk_f16_f32 v37, v42, v43
	v_cvt_pk_f16_f32 v36, v40, v41
	s_waitcnt vmcnt(0)
	v_mul_f32_e32 v76, v232, v232
	v_mfma_f32_32x32x16_f16 v[0:15], v[32:35], v[36:39], v[0:15]
	v_perm_b32 v32, v240, v64, s42
	v_perm_b32 v33, v240, v64, s43
	v_perm_b32 v34, v240, v65, s42
	v_perm_b32 v35, v240, v65, s43
	v_pk_add_f16 v32, v32, s5 op_sel_hi:[1,0]
	v_pk_add_f16 v33, v33, s5 op_sel_hi:[1,0]
	v_pk_add_f16 v34, v34, s5 op_sel_hi:[1,0]
	v_pk_add_f16 v35, v35, s5 op_sel_hi:[1,0]
	s_nop 3
	v_add_f32_e32 v0, v157, v0
	v_add_f32_e32 v74, v74, v79
	v_mfma_f32_32x32x16_f16 v[16:31], v[32:35], v[36:39], v[16:31]
	v_cvt_f16_f32_e32 v33, v0
	v_add_f32_e32 v75, v231, v232
	v_fmac_f32_e32 v76, v231, v231
	v_add_f32_e32 v75, v75, v78
	ds_write_b16 v158, v33 offset:18432
	v_add_f32_e32 v74, v76, v74
	v_add_f32_e32 v76, v233, v234
	s_nop 4
	v_add_f32_e32 v16, v157, v16
	v_add_f32_e32 v32, v0, v16
	v_cvt_f16_f32_e32 v34, v16
	v_mul_f32_e32 v16, v16, v16
	v_fmac_f32_e32 v16, v0, v0
	v_add_f32_e32 v0, v157, v1
	v_add_f32_e32 v1, v157, v17
	v_add_f32_e32 v32, 0, v32
	v_add_f32_e32 v17, v0, v1
	v_add_f32_e32 v17, v17, v32
	v_mul_f32_e32 v32, v1, v1
	v_cvt_f16_f32_e32 v1, v1
	v_fmac_f32_e32 v32, v0, v0
	v_cvt_f16_f32_e32 v33, v0
	v_add_f32_e32 v0, v16, v32
	ds_write_b16 v158, v1 offset:23184
	v_add_f32_e32 v1, v157, v2
	v_add_f32_e32 v2, v157, v18
	v_add_f32_e32 v16, v1, v2
	v_add_f32_e32 v16, v16, v17
	v_mul_f32_e32 v17, v2, v2
	v_cvt_f16_f32_e32 v2, v2
	v_cvt_f16_f32_e32 v18, v1
	v_fmac_f32_e32 v17, v1, v1
	v_add_f32_e32 v1, v157, v3
	ds_write_b16 v158, v2 offset:23328
	v_add_f32_e32 v2, v157, v19
	v_add_f32_e32 v3, v1, v2
	v_add_f32_e32 v3, v3, v16
	v_mul_f32_e32 v16, v2, v2
	v_cvt_f16_f32_e32 v2, v2
	v_add_f32_e32 v0, v17, v0
	v_cvt_f16_f32_e32 v17, v1
	v_fmac_f32_e32 v16, v1, v1
	ds_write_b16 v158, v2 offset:23472
	v_add_f32_e32 v1, v157, v4
	v_add_f32_e32 v2, v157, v20
	v_add_f32_e32 v4, v1, v2
	v_add_f32_e32 v3, v4, v3
	v_mul_f32_e32 v4, v2, v2
	v_cvt_f16_f32_e32 v2, v2
	v_add_f32_e32 v0, v16, v0
	v_cvt_f16_f32_e32 v16, v1
	v_fmac_f32_e32 v4, v1, v1
	ds_write_b16 v158, v2 offset:24192
	v_add_f32_e32 v1, v157, v5
	v_add_f32_e32 v2, v157, v21
	v_add_f32_e32 v0, v4, v0
	v_add_f32_e32 v4, v1, v2
	v_add_f32_e32 v3, v4, v3
	v_mul_f32_e32 v4, v2, v2
	v_cvt_f16_f32_e32 v2, v2
	v_cvt_f16_f32_e32 v5, v1
	v_fmac_f32_e32 v4, v1, v1
	v_add_f32_e32 v1, v157, v6
	ds_write_b16 v158, v2 offset:24336
	v_add_f32_e32 v2, v157, v22
	v_add_f32_e32 v0, v4, v0
	v_add_f32_e32 v4, v1, v2
	v_add_f32_e32 v3, v4, v3
	v_mul_f32_e32 v4, v2, v2
	v_cvt_f16_f32_e32 v2, v2
	ds_write_b16 v158, v5 offset:19728
	v_cvt_f16_f32_e32 v5, v1
	v_fmac_f32_e32 v4, v1, v1
	ds_write_b16 v158, v2 offset:24480
	v_add_f32_e32 v1, v157, v7
	v_add_f32_e32 v2, v157, v23
	v_add_f32_e32 v0, v4, v0
	v_add_f32_e32 v4, v1, v2
	v_add_f32_e32 v3, v4, v3
	v_mul_f32_e32 v4, v2, v2
	v_cvt_f16_f32_e32 v2, v2
	ds_write_b16 v158, v5 offset:19872
	v_cvt_f16_f32_e32 v5, v1
	v_fmac_f32_e32 v4, v1, v1
	ds_write_b16 v158, v2 offset:24624
	v_add_f32_e32 v1, v157, v8
	v_add_f32_e32 v2, v157, v24
	v_add_f32_e32 v0, v4, v0
	v_add_f32_e32 v4, v1, v2
	v_add_f32_e32 v3, v4, v3
	v_mul_f32_e32 v4, v2, v2
	v_cvt_f16_f32_e32 v2, v2
	ds_write_b16 v158, v5 offset:20016
	v_cvt_f16_f32_e32 v5, v1
	v_fmac_f32_e32 v4, v1, v1
	ds_write_b16 v158, v2 offset:25344
	v_add_f32_e32 v1, v157, v9
	v_add_f32_e32 v2, v157, v25
	v_add_f32_e32 v0, v4, v0
	v_add_f32_e32 v4, v1, v2
	v_add_f32_e32 v3, v4, v3
	v_mul_f32_e32 v4, v2, v2
	v_cvt_f16_f32_e32 v2, v2
	ds_write_b16 v158, v5 offset:20736
	v_cvt_f16_f32_e32 v5, v1
	v_fmac_f32_e32 v4, v1, v1
	ds_write_b16 v158, v2 offset:25488
	v_add_f32_e32 v1, v157, v10
	v_add_f32_e32 v2, v157, v26
	v_add_f32_e32 v0, v4, v0
	v_add_f32_e32 v4, v1, v2
	v_add_f32_e32 v3, v4, v3
	v_mul_f32_e32 v4, v2, v2
	v_cvt_f16_f32_e32 v2, v2
	ds_write_b16 v158, v5 offset:20880
	v_cvt_f16_f32_e32 v5, v1
	v_fmac_f32_e32 v4, v1, v1
	ds_write_b16 v158, v2 offset:25632
	v_add_f32_e32 v1, v157, v11
	v_add_f32_e32 v2, v157, v27
	v_add_f32_e32 v0, v4, v0
	v_add_f32_e32 v4, v1, v2
	v_add_f32_e32 v3, v4, v3
	v_mul_f32_e32 v4, v2, v2
	v_cvt_f16_f32_e32 v2, v2
	ds_write_b16 v158, v5 offset:21024
	v_cvt_f16_f32_e32 v5, v1
	v_fmac_f32_e32 v4, v1, v1
	ds_write_b16 v158, v2 offset:25776
	v_add_f32_e32 v1, v157, v12
	v_add_f32_e32 v2, v157, v28
	v_add_f32_e32 v0, v4, v0
	v_add_f32_e32 v4, v1, v2
	v_add_f32_e32 v3, v4, v3
	v_mul_f32_e32 v4, v2, v2
	v_cvt_f16_f32_e32 v2, v2
	ds_write_b16 v158, v5 offset:21168
	v_cvt_f16_f32_e32 v5, v1
	v_fmac_f32_e32 v4, v1, v1
	ds_write_b16 v158, v2 offset:26496
	v_add_f32_e32 v1, v157, v13
	v_add_f32_e32 v2, v157, v29
	v_add_f32_e32 v0, v4, v0
	v_add_f32_e32 v4, v1, v2
	v_add_f32_e32 v3, v4, v3
	v_mul_f32_e32 v4, v2, v2
	v_cvt_f16_f32_e32 v2, v2
	ds_write_b16 v158, v5 offset:21888
	v_cvt_f16_f32_e32 v5, v1
	v_fmac_f32_e32 v4, v1, v1
	ds_write_b16 v158, v2 offset:26640
	v_add_f32_e32 v1, v157, v14
	v_add_f32_e32 v2, v157, v30
	v_add_f32_e32 v0, v4, v0
	v_add_f32_e32 v4, v1, v2
	v_add_f32_e32 v3, v4, v3
	v_cvt_f16_f32_e32 v4, v1
	v_add_f32_e32 v75, v76, v75
	v_mul_f32_e32 v76, v234, v234
	ds_write_b16 v158, v5 offset:22032
	v_mul_f32_e32 v5, v2, v2
	v_fmac_f32_e32 v76, v233, v233
	v_mul_f32_e32 v67, v236, v236
	v_fmac_f32_e32 v5, v1, v1
	v_add_f32_e32 v74, v76, v74
	v_fmac_f32_e32 v67, v235, v235
	v_mul_f32_e32 v57, v238, v238
	v_add_f32_e32 v0, v5, v0
	v_cvt_f16_f32_e32 v5, v2
	v_add_f32_e32 v1, v157, v15
	v_add_f32_e32 v2, v157, v31
	v_add_f32_e32 v76, v235, v236
	v_add_f32_e32 v67, v67, v74
	v_fmac_f32_e32 v57, v237, v237
	v_mul_f32_e32 v50, v145, v145
	ds_write_b16 v158, v4 offset:22176
	v_add_f32_e32 v4, v1, v2
	v_add_f32_e32 v66, v76, v75
	v_add_f32_e32 v56, v237, v238
	v_add_f32_e32 v48, v57, v67
	v_fmac_f32_e32 v50, v144, v144
	v_add_f32_e32 v3, v4, v3
	v_mul_f32_e32 v4, v2, v2
	v_add_f32_e32 v56, v56, v66
	v_add_f32_e32 v49, v144, v145
	v_add_f32_e32 v40, v50, v48
	v_fmac_f32_e32 v4, v1, v1
	v_add_f32_e32 v49, v49, v56
	v_add_f32_e32 v40, v98, v40
	v_add_f32_e32 v4, v4, v0
	v_add_f32_e32 v41, v99, v49
	v_cvt_f16_f32_e32 v6, v1
	v_add_f32_e32 v1, v40, v4
	v_lshlrev_b32_e32 v4, 2, v156
	v_add_f32_e32 v0, v41, v3
	v_xor_b32_e32 v3, 0x80, v4
	v_cvt_f16_f32_e32 v7, v2
	ds_bpermute_b32 v2, v3, v0
	ds_bpermute_b32 v3, v3, v1
	ds_write_b16 v158, v34 offset:23040
	ds_write_b16 v158, v33 offset:18576
	ds_write_b16 v158, v18 offset:18720
	ds_write_b16 v158, v17 offset:18864
	ds_write_b16 v158, v16 offset:19584
	ds_write_b16 v158, v5 offset:26784
	ds_write_b16 v158, v6 offset:22320
	ds_write_b16 v158, v7 offset:26928
	s_and_saveexec_b64 s[0:1], vcc
	s_cbranch_execz .LBB2_26
	s_lshl_b32 s2, s10, 5
	v_lshl_add_u32 v4, s2, 2, v4
	v_or_b32_e32 v5, 0x1e400, v4
	s_waitcnt lgkmcnt(9)
	v_add_f32_e32 v0, v0, v2
	v_add_u32_e32 v4, 0x1e500, v4
	s_waitcnt lgkmcnt(8)
	v_add_f32_e32 v1, v1, v3
	ds_add_f32 v5, v0
	ds_add_f32 v4, v1

	.amdhsa_kernel _Z7k_layerILi1EEvPKDF16_S1_PKfS3_S3_S3_S3_S3_S1_S1_S1_S1_S3_S3_PKhS5_PDF16_S6_PfS7_
		.amdhsa_group_segment_fixed_size 126720
		.amdhsa_private_segment_fixed_size 0
		.amdhsa_kernarg_size 160
		.amdhsa_user_sgpr_count 2
		.amdhsa_user_sgpr_dispatch_ptr 0
		.amdhsa_user_sgpr_queue_ptr 0
		.amdhsa_user_sgpr_kernarg_segment_ptr 1
		.amdhsa_user_sgpr_dispatch_id 0
		.amdhsa_user_sgpr_kernarg_preload_length 0
		.amdhsa_user_sgpr_kernarg_preload_offset 0
		.amdhsa_user_sgpr_private_segment_size 0
		.amdhsa_uses_dynamic_stack 0
		.amdhsa_enable_private_segment 0
		.amdhsa_system_sgpr_workgroup_id_x 1
		.amdhsa_system_sgpr_workgroup_id_y 0
		.amdhsa_system_sgpr_workgroup_id_z 0
		.amdhsa_system_sgpr_workgroup_info 0
		.amdhsa_system_vgpr_workitem_id 0
		.amdhsa_next_free_vgpr 248
		.amdhsa_next_free_sgpr 96
		.amdhsa_accum_offset 248
		.amdhsa_reserve_vcc 1
		.amdhsa_float_round_mode_32 0
		.amdhsa_float_round_mode_16_64 0
		.amdhsa_float_denorm_mode_32 3
		.amdhsa_float_denorm_mode_16_64 3
		.amdhsa_dx10_clamp 1
		.amdhsa_ieee_mode 1
		.amdhsa_fp16_overflow 0
		.amdhsa_tg_split 0
		.amdhsa_exception_fp_ieee_invalid_op 0
		.amdhsa_exception_fp_denorm_src 0
		.amdhsa_exception_fp_ieee_div_zero 0
		.amdhsa_exception_fp_ieee_overflow 0
		.amdhsa_exception_fp_ieee_underflow 0
		.amdhsa_exception_fp_ieee_inexact 0
		.amdhsa_exception_int_div_zero 0
	.end_amdhsa_kernel

_Z7k_layerILi0EEvPKDF16_S1_PKfS3_S3_S3_S3_S3_S1_S1_S1_S1_S3_S3_PKhS5_PDF16_S6_PfS7_:
	s_ashr_i32 s3, s2, 1
	s_and_b32 s3, s3, -8
	s_and_b32 s16, s2, 7
	v_readfirstlane_b32 s15, v0
	s_or_b32 s12, s3, s16
	s_bfe_u32 s14, s2, 0x10003
	s_cmpk_gt_u32 s15, 0xff
	s_mov_b64 s[2:3], -1
	s_cbranch_scc0 .LBB3_17
	v_mov_b32_e32 v240, 0x64646464
	s_mov_b32 s42, 0x4010400
	s_mov_b32 s43, 0x4030402
	s_load_dwordx4 s[8:11], s[0:1], 0x0
	s_load_dwordx2 s[4:5], s[0:1], 0x80
	v_add_u32_e32 v1, 0xffffff00, v0
	s_ashr_i32 s13, s12, 31
	s_lshr_b32 s17, s15, 6
	v_ashrrev_i32_e32 v2, 4, v1
	v_lshlrev_b32_e32 v3, 3, v0
	s_lshl_b64 s[2:3], s[12:13], 14
	v_and_b32_e32 v82, 0x78, v3
	v_ashrrev_i32_e32 v3, 31, v2
	s_waitcnt lgkmcnt(0)
	s_add_u32 s2, s10, s2
	s_addc_u32 s3, s11, s3
	v_lshlrev_b64 v[4:5], 8, v[2:3]
	v_lshl_add_u64 v[4:5], s[2:3], 0, v[4:5]
	v_lshlrev_b32_e32 v6, 1, v82
	v_mov_b32_e32 v7, 0
	v_lshl_add_u64 v[4:5], v[4:5], 0, v[6:7]
	s_movk_i32 s2, 0x2000
	v_add_co_u32_e32 v8, vcc, s2, v4
	global_load_dwordx4 v[74:77], v[4:5], off
	s_nop 0
	v_addc_co_u32_e32 v9, vcc, 0, v5, vcc
	global_load_dwordx4 v[78:81], v[8:9], off offset:-4096
	global_load_dwordx4 v[66:69], v[8:9], off
	s_movk_i32 s2, 0x3000
	v_add_co_u32_e32 v4, vcc, s2, v4
	s_lshl_b32 s18, s12, 9
	s_nop 0
	v_addc_co_u32_e32 v5, vcc, 0, v5, vcc
	global_load_dwordx4 v[62:65], v[4:5], off
	v_add_u32_e32 v3, s18, v2
	s_mov_b32 s7, 0x20000
	s_mov_b32 s6, 0x1000000
	v_lshl_or_b32 v3, v3, 8, v6
	s_and_b32 s9, s9, 0xffff
	s_mov_b32 s10, s6
	s_mov_b32 s11, s7
	v_add_u32_e32 v4, 0x1000, v3
	buffer_load_dwordx4 v[58:61], v3, s[8:11], 0 offen sc1
	buffer_load_dwordx4 v[50:53], v4, s[8:11], 0 offen sc1
	v_add_u32_e32 v4, 0x2000, v3
	v_add_u32_e32 v5, 0x3000, v3
	buffer_load_dwordx4 v[42:45], v4, s[8:11], 0 offen sc1
	buffer_load_dwordx4 v[34:37], v5, s[8:11], 0 offen sc1
	v_add_u32_e32 v4, 0x4000, v3
	v_add_u32_e32 v5, 0x5000, v3
	buffer_load_dwordx4 v[70:73], v4, s[8:11], 0 offen sc1
	buffer_load_dwordx4 v[54:57], v5, s[8:11], 0 offen sc1
	v_add_u32_e32 v4, 0x6000, v3
	v_add_u32_e32 v3, 0x7000, v3
	buffer_load_dwordx4 v[46:49], v4, s[8:11], 0 offen sc1
	buffer_load_dwordx4 v[38:41], v3, s[8:11], 0 offen sc1
	s_or_b32 s2, s18, 0x80
	v_add_u32_e32 v2, s2, v2
	v_lshl_or_b32 v6, v2, 8, v6
	v_add_u32_e32 v2, 0x1000, v6
	v_add_u32_e32 v7, 0x2000, v6
	v_add_u32_e32 v8, 0x3000, v6
	buffer_load_dwordx4 v[26:29], v6, s[8:11], 0 offen sc1
	buffer_load_dwordx4 v[18:21], v2, s[8:11], 0 offen sc1
	buffer_load_dwordx4 v[10:13], v7, s[8:11], 0 offen sc1
	s_nop 0
	buffer_load_dwordx4 v[2:5], v8, s[8:11], 0 offen sc1
	v_add_u32_e32 v7, 0x4000, v6
	v_add_u32_e32 v8, 0x5000, v6
	v_add_u32_e32 v83, 0x6000, v6
	buffer_load_dwordx4 v[30:33], v7, s[8:11], 0 offen sc1
	buffer_load_dwordx4 v[22:25], v8, s[8:11], 0 offen sc1
	v_add_u32_e32 v84, 0x7000, v6
	buffer_load_dwordx4 v[14:17], v83, s[8:11], 0 offen sc1
	buffer_load_dwordx4 v[6:9], v84, s[8:11], 0 offen sc1
	v_lshlrev_b32_e32 v92, 2, v82
	v_or_b32_e32 v82, 0x1e600, v92
	s_barrier
	ds_read_b128 v[82:85], v82
	v_or_b32_e32 v86, 0x1ea00, v92
	ds_read_b128 v[88:91], v86
	v_or_b32_e32 v93, 0x1e800, v92
	v_or_b32_e32 v102, 0x1ec00, v92
	s_waitcnt lgkmcnt(1)
	v_cvt_pk_f16_f32 v82, v82, v83
	v_cvt_pk_f16_f32 v83, v84, v85
	v_or_b32_e32 v84, 0x1e610, v92
	ds_read_b128 v[84:87], v84
	v_or_b32_e32 v94, 0x1ea10, v92
	v_or_b32_e32 v108, 0x1e810, v92
	v_or_b32_e32 v109, 0x1ec10, v92
	ds_read_b128 v[94:97], v94
	ds_read_b128 v[98:101], v93
	ds_read_b128 v[102:105], v102
	s_waitcnt lgkmcnt(3)
	v_cvt_pk_f16_f32 v84, v84, v85
	s_movk_i32 s22, 0x110
	s_or_b32 s21, s18, 0x100
	s_or_b32 s19, s18, 0x180
	v_mov_b32_e32 v130, v0
	s_lshl_b32 s18, s14, 6
	v_mov_b32_e32 v132, 0x11000
	s_and_b32 s5, s5, 0xffff
	s_lshl_b32 s2, s2, 7
	s_or_b32 s2, s2, s18
	s_mov_b32 s3, 0
	s_movk_i32 s20, 0x1000
	s_waitcnt vmcnt(19)
	v_cvt_f32_f16_e32 v92, v74
	v_cvt_f32_f16_sdwa v93, v74 dst_sel:DWORD dst_unused:UNUSED_PAD src0_sel:WORD_1
	s_waitcnt vmcnt(18)
	v_cvt_f32_f16_e32 v106, v78
	v_cvt_f32_f16_sdwa v107, v78 dst_sel:DWORD dst_unused:UNUSED_PAD src0_sel:WORD_1
	v_cvt_pk_f16_f32 v74, v86, v87
	s_waitcnt lgkmcnt(1)
	v_pk_fma_f32 v[86:87], v[98:99], v[92:93], v[88:89]
	v_pk_fma_f32 v[92:93], v[98:99], v[106:107], v[88:89]
	s_waitcnt lgkmcnt(0)
	v_pk_add_f32 v[92:93], v[102:103], v[92:93]
	s_waitcnt vmcnt(17)
	v_cvt_f32_f16_e32 v106, v66
	v_cvt_f32_f16_sdwa v107, v66 dst_sel:DWORD dst_unused:UNUSED_PAD src0_sel:WORD_1
	v_cvt_pk_f16_f32 v85, v92, v93
	s_waitcnt vmcnt(16)
	v_cvt_f32_f16_e32 v92, v62
	v_cvt_f32_f16_sdwa v93, v62 dst_sel:DWORD dst_unused:UNUSED_PAD src0_sel:WORD_1
	v_cvt_f32_f16_e32 v66, v67
	v_cvt_f32_f16_sdwa v67, v67 dst_sel:DWORD dst_unused:UNUSED_PAD src0_sel:WORD_1
	v_cvt_f32_f16_e32 v62, v63
	v_cvt_f32_f16_sdwa v63, v63 dst_sel:DWORD dst_unused:UNUSED_PAD src0_sel:WORD_1
	v_pk_fma_f32 v[106:107], v[98:99], v[106:107], v[88:89]
	v_pk_fma_f32 v[88:89], v[98:99], v[92:93], v[88:89]
	v_cvt_f32_f16_e32 v92, v75
	v_cvt_f32_f16_sdwa v93, v75 dst_sel:DWORD dst_unused:UNUSED_PAD src0_sel:WORD_1
	v_cvt_f32_f16_e32 v98, v79
	v_cvt_f32_f16_sdwa v99, v79 dst_sel:DWORD dst_unused:UNUSED_PAD src0_sel:WORD_1
	v_pk_add_f32 v[88:89], v[102:103], v[88:89]
	v_pk_fma_f32 v[66:67], v[100:101], v[66:67], v[90:91]
	v_pk_fma_f32 v[62:63], v[100:101], v[62:63], v[90:91]
	v_cvt_pk_f16_f32 v75, v88, v89
	v_pk_fma_f32 v[88:89], v[100:101], v[92:93], v[90:91]
	v_pk_fma_f32 v[92:93], v[100:101], v[98:99], v[90:91]
	v_pk_add_f32 v[66:67], v[104:105], v[66:67]
	v_pk_add_f32 v[62:63], v[104:105], v[62:63]
	v_pk_add_f32 v[86:87], v[102:103], v[86:87]
	v_pk_add_f32 v[106:107], v[102:103], v[106:107]
	v_pk_add_f32 v[88:89], v[104:105], v[88:89]
	v_pk_add_f32 v[92:93], v[104:105], v[92:93]
	v_cvt_pk_f16_f32 v79, v66, v67
	ds_read_b128 v[98:101], v108
	ds_read_b128 v[102:105], v109
	v_cvt_f32_f16_e32 v66, v76
	v_cvt_f32_f16_sdwa v67, v76 dst_sel:DWORD dst_unused:UNUSED_PAD src0_sel:WORD_1
	v_cvt_pk_f16_f32 v76, v62, v63
	v_cvt_f32_f16_e32 v62, v80
	v_cvt_f32_f16_sdwa v63, v80 dst_sel:DWORD dst_unused:UNUSED_PAD src0_sel:WORD_1
	s_waitcnt lgkmcnt(1)
	v_pk_fma_f32 v[66:67], v[98:99], v[66:67], v[94:95]
	v_cvt_pk_f16_f32 v87, v86, v87
	s_waitcnt lgkmcnt(0)
	v_pk_add_f32 v[66:67], v[102:103], v[66:67]
	v_pk_fma_f32 v[62:63], v[98:99], v[62:63], v[94:95]
	v_cvt_pk_f16_f32 v88, v88, v89
	v_pk_add_f32 v[62:63], v[102:103], v[62:63]
	v_cvt_pk_f16_f32 v86, v92, v93
	v_cvt_pk_f16_f32 v92, v66, v67
	v_cvt_f32_f16_e32 v66, v68
	v_cvt_f32_f16_sdwa v67, v68 dst_sel:DWORD dst_unused:UNUSED_PAD src0_sel:WORD_1
	v_cvt_pk_f16_f32 v89, v62, v63
	v_cvt_f32_f16_e32 v62, v64
	v_cvt_f32_f16_sdwa v63, v64 dst_sel:DWORD dst_unused:UNUSED_PAD src0_sel:WORD_1
	v_pk_fma_f32 v[66:67], v[98:99], v[66:67], v[94:95]
	v_cvt_pk_f16_f32 v78, v106, v107
	v_pk_add_f32 v[66:67], v[102:103], v[66:67]
	v_pk_fma_f32 v[62:63], v[98:99], v[62:63], v[94:95]
	v_cvt_pk_f16_f32 v80, v66, v67
	v_pk_add_f32 v[62:63], v[102:103], v[62:63]
	v_cvt_f32_f16_e32 v66, v77
	v_cvt_f32_f16_sdwa v67, v77 dst_sel:DWORD dst_unused:UNUSED_PAD src0_sel:WORD_1
	v_cvt_pk_f16_f32 v77, v62, v63
	v_cvt_f32_f16_e32 v62, v81
	v_cvt_f32_f16_sdwa v63, v81 dst_sel:DWORD dst_unused:UNUSED_PAD src0_sel:WORD_1
	v_pk_fma_f32 v[66:67], v[100:101], v[66:67], v[96:97]
	s_waitcnt vmcnt(15)
	v_pk_fma_f16 v59, v83, v59, v88
	v_pk_add_f32 v[66:67], v[104:105], v[66:67]
	v_pk_fma_f32 v[62:63], v[100:101], v[62:63], v[96:97]
	v_cvt_pk_f16_f32 v95, v66, v67
	v_pk_add_f32 v[62:63], v[104:105], v[62:63]
	v_cvt_f32_f16_e32 v66, v69
	v_cvt_pk_f16_f32 v93, v62, v63
	v_cvt_f32_f16_e32 v62, v65
	v_cvt_f32_f16_sdwa v63, v65 dst_sel:DWORD dst_unused:UNUSED_PAD src0_sel:WORD_1
	v_cvt_f32_f16_sdwa v67, v69 dst_sel:DWORD dst_unused:UNUSED_PAD src0_sel:WORD_1
	v_pk_fma_f16 v61, v74, v61, v95
	v_pk_fma_f16 v58, v82, v58, v87
	v_pk_fma_f32 v[62:63], v[100:101], v[62:63], v[96:97]
	v_pk_fma_f32 v[64:65], v[100:101], v[66:67], v[96:97]
	v_pk_add_f32 v[62:63], v[104:105], v[62:63]
	v_pk_add_f32 v[64:65], v[104:105], v[64:65]
	v_cvt_pk_f16_f32 v81, v62, v63
	v_mov_b32_e32 v62, v0
	v_cvt_pk_f16_f32 v91, v64, v65
	v_add_u32_e32 v63, 0xffffff00, v62
	v_lshlrev_b32_e32 v62, 4, v62
	v_ashrrev_i32_e32 v94, 4, v63
	v_and_b32_e32 v90, 0xf0, v62
	v_pk_fma_f16 v60, v84, v60, v92
	s_waitcnt vmcnt(11)
	v_pk_fma_f16 v62, v82, v70, v87
	v_pk_fma_f16 v51, v83, v51, v86
	v_pk_fma_f16 v53, v74, v53, v93
	v_pk_fma_f16 v50, v82, v50, v85
	v_pk_fma_f16 v52, v84, v52, v89
	v_pk_fma_f16 v43, v83, v43, v79
	v_pk_fma_f16 v45, v74, v45, v91
	v_pk_fma_f16 v42, v82, v42, v78
	v_pk_fma_f16 v44, v84, v44, v80
	v_pk_fma_f16 v35, v83, v35, v76
	v_pk_fma_f16 v37, v74, v37, v81
	v_pk_fma_f16 v34, v82, v34, v75
	v_pk_fma_f16 v36, v84, v36, v77
	s_waitcnt vmcnt(8)
	v_pk_fma_f16 v38, v82, v38, v75
	v_pk_fma_f16 v63, v83, v71, v88
	v_pk_fma_f16 v65, v74, v73, v95
	v_pk_fma_f16 v64, v84, v72, v92
	v_pk_max_f16 v60, v60, 0
	v_pk_max_f16 v58, v58, 0
	v_pk_max_f16 v61, v61, 0
	v_pk_max_f16 v59, v59, 0
	v_pk_max_f16 v62, v62, 0
	v_mad_u64_u32 v[96:97], s[24:25], v94, s22, v[90:91]
	v_pk_fma_f16 v55, v83, v55, v86
	v_pk_fma_f16 v57, v74, v57, v93
	v_pk_fma_f16 v54, v82, v54, v85
	v_pk_fma_f16 v56, v84, v56, v89
	v_pk_max_f16 v52, v52, 0
	v_pk_max_f16 v50, v50, 0
	v_pk_max_f16 v53, v53, 0
	v_pk_max_f16 v51, v51, 0
	v_pk_fma_f16 v47, v83, v47, v79
	v_pk_fma_f16 v49, v74, v49, v91
	v_pk_fma_f16 v46, v82, v46, v78
	v_pk_fma_f16 v48, v84, v48, v80
	v_pk_max_f16 v44, v44, 0
	v_pk_max_f16 v42, v42, 0
	v_pk_max_f16 v45, v45, 0
	v_pk_max_f16 v43, v43, 0
	v_pk_fma_f16 v39, v83, v39, v76
	v_pk_fma_f16 v41, v74, v41, v81
	v_pk_fma_f16 v40, v84, v40, v77
	v_pk_max_f16 v36, v36, 0
	v_pk_max_f16 v34, v34, 0
	v_pk_max_f16 v37, v37, 0
	v_pk_max_f16 v35, v35, 0
	v_pk_max_f16 v38, v38, 0
	v_pk_max_f16 v64, v64, 0
	v_pk_max_f16 v65, v65, 0
	v_pk_max_f16 v63, v63, 0
	ds_write_b128 v96, v[58:61]
	ds_write_b128 v96, v[62:65] offset:17408
	v_pk_add_f16 v73, v58, v62
	v_pk_max_f16 v56, v56, 0
	v_pk_max_f16 v54, v54, 0
	v_pk_max_f16 v57, v57, 0
	v_pk_max_f16 v55, v55, 0
	ds_write_b128 v96, v[50:53] offset:4352
	ds_write_b128 v96, v[54:57] offset:21760
	v_pk_max_f16 v48, v48, 0
	v_pk_max_f16 v46, v46, 0
	v_pk_max_f16 v49, v49, 0
	v_pk_max_f16 v47, v47, 0
	ds_write_b128 v96, v[42:45] offset:8704
	ds_write_b128 v96, v[46:49] offset:26112
	v_pk_max_f16 v40, v40, 0
	v_pk_max_f16 v41, v41, 0
	v_pk_max_f16 v39, v39, 0
	ds_write_b128 v96, v[34:37] offset:13056
	ds_write_b128 v96, v[38:41] offset:30464
	v_pk_add_f16 v62, v34, v38
	v_add_u32_e32 v34, s21, v94
	v_lshl_or_b32 v38, v34, 8, v90
	v_pk_add_f16 v71, v60, v64
	v_pk_add_f16 v60, v35, v39
	v_add_u32_e32 v34, 0x1000, v38
	v_add_u32_e32 v39, 0x2000, v38
	v_pk_add_f16 v69, v61, v65
	v_pk_add_f16 v72, v59, v63
	v_pk_add_f16 v65, v53, v57
	v_pk_add_f16 v67, v52, v56
	v_pk_add_f16 v68, v51, v55
	v_pk_add_f16 v70, v50, v54
	v_pk_add_f16 v61, v45, v49
	v_pk_add_f16 v63, v44, v48
	v_pk_add_f16 v64, v43, v47
	v_pk_add_f16 v66, v42, v46
	v_pk_add_f16 v58, v37, v41
	v_pk_add_f16 v59, v36, v40
	buffer_load_dwordx4 v[100:103], v38, s[8:11], 0 offen sc1
	buffer_load_dwordx4 v[50:53], v34, s[8:11], 0 offen sc1
	v_add_u32_e32 v40, 0x3000, v38
	buffer_load_dwordx4 v[42:45], v39, s[8:11], 0 offen sc1
	buffer_load_dwordx4 v[34:37], v40, s[8:11], 0 offen sc1
	v_add_u32_e32 v39, 0x4000, v38
	v_add_u32_e32 v40, 0x5000, v38
	buffer_load_dwordx4 v[104:107], v39, s[8:11], 0 offen sc1
	buffer_load_dwordx4 v[54:57], v40, s[8:11], 0 offen sc1
	v_add_u32_e32 v90, 0x6000, v38
	v_add_u32_e32 v94, 0x7000, v38
	buffer_load_dwordx4 v[46:49], v90, s[8:11], 0 offen sc1
	buffer_load_dwordx4 v[38:41], v94, s[8:11], 0 offen sc1
	v_mov_b32_e32 v90, v0
	s_waitcnt lgkmcnt(0)
	s_barrier
	s_waitcnt vmcnt(15)
	v_pk_fma_f16 v27, v83, v27, v88
	v_add_u32_e32 v94, 0xffffff00, v90
	v_lshlrev_b32_e32 v90, 4, v90
	v_ashrrev_i32_e32 v109, 4, v94
	v_and_b32_e32 v108, 0xf0, v90
	v_pk_fma_f16 v29, v74, v29, v95
	v_pk_fma_f16 v26, v82, v26, v87
	v_pk_fma_f16 v28, v84, v28, v92
	s_waitcnt vmcnt(11)
	v_pk_fma_f16 v30, v82, v30, v87
	v_pk_fma_f16 v19, v83, v19, v86
	v_pk_fma_f16 v21, v74, v21, v93
	v_pk_fma_f16 v18, v82, v18, v85
	v_pk_fma_f16 v20, v84, v20, v89
	v_pk_fma_f16 v11, v83, v11, v79
	v_pk_fma_f16 v13, v74, v13, v91
	v_pk_fma_f16 v10, v82, v10, v78
	v_pk_fma_f16 v12, v84, v12, v80
	v_pk_fma_f16 v3, v83, v3, v76
	v_pk_fma_f16 v5, v74, v5, v81
	v_pk_fma_f16 v2, v82, v2, v75
	v_pk_fma_f16 v4, v84, v4, v77
	s_waitcnt vmcnt(8)
	v_pk_fma_f16 v6, v82, v6, v75
	v_pk_fma_f16 v31, v83, v31, v88
	v_pk_fma_f16 v33, v74, v33, v95
	v_pk_fma_f16 v32, v84, v32, v92
	v_pk_max_f16 v28, v28, 0
	v_pk_max_f16 v26, v26, 0
	v_pk_max_f16 v29, v29, 0
	v_pk_max_f16 v27, v27, 0
	v_pk_max_f16 v30, v30, 0
	v_mad_u64_u32 v[110:111], s[24:25], v109, s22, v[108:109]
	v_pk_fma_f16 v23, v83, v23, v86
	v_pk_fma_f16 v25, v74, v25, v93
	v_pk_fma_f16 v22, v82, v22, v85
	v_pk_fma_f16 v24, v84, v24, v89
	v_pk_max_f16 v20, v20, 0
	v_pk_max_f16 v18, v18, 0
	v_pk_max_f16 v21, v21, 0
	v_pk_max_f16 v19, v19, 0
	v_pk_fma_f16 v15, v83, v15, v79
	v_pk_fma_f16 v17, v74, v17, v91
	v_pk_fma_f16 v14, v82, v14, v78
	v_pk_fma_f16 v16, v84, v16, v80
	v_pk_max_f16 v12, v12, 0
	v_pk_max_f16 v10, v10, 0
	v_pk_max_f16 v13, v13, 0
	v_pk_max_f16 v11, v11, 0
	v_pk_fma_f16 v7, v83, v7, v76
	v_pk_fma_f16 v9, v74, v9, v81
	v_pk_fma_f16 v8, v84, v8, v77
	v_pk_max_f16 v4, v4, 0
	v_pk_max_f16 v2, v2, 0
	v_pk_max_f16 v5, v5, 0
	v_pk_max_f16 v3, v3, 0
	v_pk_max_f16 v6, v6, 0
	v_pk_max_f16 v32, v32, 0
	v_pk_max_f16 v33, v33, 0
	v_pk_max_f16 v31, v31, 0
	ds_write_b128 v110, v[26:29] offset:34816
	ds_write_b128 v110, v[30:33] offset:52224
	v_pk_add_f16 v129, v26, v30
	v_pk_max_f16 v24, v24, 0
	v_pk_max_f16 v22, v22, 0
	v_pk_max_f16 v25, v25, 0
	v_pk_max_f16 v23, v23, 0
	ds_write_b128 v110, v[18:21] offset:39168
	ds_write_b128 v110, v[22:25] offset:56576
	v_pk_max_f16 v16, v16, 0
	v_pk_max_f16 v14, v14, 0
	v_pk_max_f16 v17, v17, 0
	v_pk_max_f16 v15, v15, 0
	ds_write_b128 v110, v[10:13] offset:43520
	ds_write_b128 v110, v[14:17] offset:60928
	v_pk_max_f16 v8, v8, 0
	v_pk_max_f16 v9, v9, 0
	v_pk_max_f16 v7, v7, 0
	ds_write_b128 v110, v[2:5] offset:47872
	ds_write_b128 v110, v[6:9] offset:65280
	v_pk_add_f16 v30, v2, v6
	v_add_u32_e32 v2, s19, v109
	v_lshl_or_b32 v6, v2, 8, v108
	v_pk_add_f16 v99, v28, v32
	v_pk_add_f16 v128, v27, v31
	v_pk_add_f16 v27, v4, v8
	v_pk_add_f16 v28, v3, v7
	v_add_u32_e32 v2, 0x1000, v6
	v_add_u32_e32 v7, 0x2000, v6
	v_add_u32_e32 v8, 0x3000, v6
	v_pk_add_f16 v97, v29, v33
	v_pk_add_f16 v33, v21, v25
	v_pk_add_f16 v94, v20, v24
	v_pk_add_f16 v96, v19, v23
	v_pk_add_f16 v98, v18, v22
	v_pk_add_f16 v29, v13, v17
	v_pk_add_f16 v31, v12, v16
	v_pk_add_f16 v32, v11, v15
	v_pk_add_f16 v90, v10, v14
	v_pk_add_f16 v26, v5, v9
	buffer_load_dwordx4 v[108:111], v6, s[8:11], 0 offen sc1
	buffer_load_dwordx4 v[18:21], v2, s[8:11], 0 offen sc1
	buffer_load_dwordx4 v[10:13], v7, s[8:11], 0 offen sc1
	s_nop 0
	buffer_load_dwordx4 v[2:5], v8, s[8:11], 0 offen sc1
	v_add_u32_e32 v7, 0x4000, v6
	v_add_u32_e32 v8, 0x5000, v6
	v_add_u32_e32 v116, 0x6000, v6
	buffer_load_dwordx4 v[112:115], v7, s[8:11], 0 offen sc1
	buffer_load_dwordx4 v[22:25], v8, s[8:11], 0 offen sc1
	v_add_u32_e32 v117, 0x7000, v6
	buffer_load_dwordx4 v[14:17], v116, s[8:11], 0 offen sc1
	buffer_load_dwordx4 v[6:9], v117, s[8:11], 0 offen sc1
	s_waitcnt lgkmcnt(0)
	s_barrier
	s_lshl_b32 s8, s12, 16
	v_add_u32_e32 v116, 0xffffff00, v130
	v_lshlrev_b32_e32 v117, 3, v130
	v_lshrrev_b32_e32 v131, 4, v116
	v_and_b32_e32 v117, 56, v117
	v_lshrrev_b32_e32 v125, 3, v116
	v_ashrrev_i32_e32 v116, 3, v116
	s_movk_i32 s10, 0xffc0
	s_or_b32 s8, s8, s18
	v_lshl_or_b32 v124, v117, 1, v132
	v_bfi_b32 v121, s10, v116, v125
	s_movk_i32 s11, 0x90
	v_or_b32_e32 v120, s8, v117
	v_mad_u64_u32 v[116:117], s[8:9], v121, s11, v[124:125]
	ds_read_b128 v[116:119], v116
	v_lshlrev_b32_e32 v133, 1, v120
	v_lshrrev_b32_e32 v127, 3, v130
	v_ashrrev_i32_e32 v120, 3, v130
	v_bfi_b32 v134, s10, v120, v127
	v_lshl_add_u32 v126, v121, 8, v133
	v_mad_u64_u32 v[120:121], s[8:9], v134, s11, v[124:125]
	ds_read_b128 v[120:123], v120
	s_waitcnt lgkmcnt(1)
	buffer_store_dwordx4 v[116:119], v126, s[4:7], 0 offen sc1
	v_lshl_add_u32 v134, v134, 8, v133
	s_waitcnt vmcnt(16)
	v_pk_fma_f16 v100, v82, v100, v87
	v_add_u32_e32 v116, 0x100, v130
	v_ashrrev_i32_e32 v116, 3, v116
	v_bfi_b32 v135, s10, v116, v125
	v_mad_u64_u32 v[116:117], s[8:9], v135, s11, v[124:125]
	v_add_u32_e32 v125, 0x200, v130
	v_ashrrev_i32_e32 v125, 3, v125
	v_bfi_b32 v136, s10, v125, v127
	ds_read_b128 v[116:119], v116
	v_mad_u64_u32 v[124:125], s[8:9], v136, s11, v[124:125]
	ds_read_b128 v[124:127], v124
	s_waitcnt lgkmcnt(2)
	buffer_store_dwordx4 v[120:123], v134, s[4:7], 0 offen sc1
	v_pk_fma_f16 v101, v83, v101, v88
	v_pk_fma_f16 v102, v84, v102, v92
	v_lshl_add_u32 v120, v135, 8, v133
	s_waitcnt lgkmcnt(1)
	buffer_store_dwordx4 v[116:119], v120, s[4:7], 0 offen sc1
	v_pk_fma_f16 v103, v74, v103, v95
	s_waitcnt vmcnt(17)
	v_pk_fma_f16 v50, v82, v50, v85
	v_lshl_add_u32 v116, v136, 8, v133
	s_waitcnt lgkmcnt(0)
	buffer_store_dwordx4 v[124:127], v116, s[4:7], 0 offen sc1
	v_lshlrev_b32_e32 v116, 4, v130
	v_and_b32_e32 v116, 0xf0, v116
	v_pk_fma_f16 v51, v83, v51, v86
	v_pk_fma_f16 v52, v84, v52, v89
	v_pk_fma_f16 v53, v74, v53, v93
	s_waitcnt vmcnt(14)
	v_pk_fma_f16 v56, v84, v56, v89
	v_pk_fma_f16 v57, v74, v57, v93
	v_pk_fma_f16 v42, v82, v42, v78
	v_pk_fma_f16 v43, v83, v43, v79
	v_pk_fma_f16 v44, v84, v44, v80
	v_pk_fma_f16 v45, v74, v45, v91
	s_waitcnt vmcnt(13)
	v_pk_fma_f16 v46, v82, v46, v78
	v_pk_fma_f16 v47, v83, v47, v79
	v_pk_fma_f16 v104, v82, v104, v87
	v_pk_fma_f16 v105, v83, v105, v88
	v_pk_fma_f16 v106, v84, v106, v92
	v_pk_fma_f16 v107, v74, v107, v95
	v_pk_max_f16 v103, v103, 0
	v_pk_max_f16 v102, v102, 0
	v_pk_max_f16 v101, v101, 0
	v_pk_max_f16 v100, v100, 0
	v_mad_u64_u32 v[116:117], s[8:9], v131, s22, v[116:117]
	v_pk_fma_f16 v54, v82, v54, v85
	v_pk_fma_f16 v55, v83, v55, v86
	v_pk_max_f16 v53, v53, 0
	v_pk_max_f16 v52, v52, 0
	v_pk_max_f16 v51, v51, 0
	v_pk_max_f16 v50, v50, 0
	v_pk_max_f16 v57, v57, 0
	v_pk_max_f16 v56, v56, 0
	v_pk_fma_f16 v48, v84, v48, v80
	v_pk_fma_f16 v49, v74, v49, v91
	v_pk_max_f16 v45, v45, 0
	v_pk_max_f16 v44, v44, 0
	v_pk_max_f16 v43, v43, 0
	v_pk_max_f16 v42, v42, 0
	v_pk_max_f16 v47, v47, 0
	v_pk_max_f16 v46, v46, 0
	v_pk_max_f16 v107, v107, 0
	v_pk_max_f16 v106, v106, 0
	v_pk_max_f16 v105, v105, 0
	v_pk_max_f16 v104, v104, 0
	ds_write_b128 v116, v[100:103]
	ds_write_b128 v116, v[104:107] offset:17408
	v_pk_max_f16 v55, v55, 0
	v_pk_max_f16 v54, v54, 0
	ds_write_b128 v116, v[50:53] offset:4352
	ds_write_b128 v116, v[54:57] offset:21760
	v_pk_add_f16 v53, v53, v57
	v_pk_add_f16 v52, v52, v56
	v_pk_max_f16 v49, v49, 0
	v_pk_max_f16 v48, v48, 0
	ds_write_b128 v116, v[42:45] offset:8704
	ds_write_b128 v116, v[46:49] offset:26112
	v_pk_add_f16 v56, v43, v47
	v_pk_add_f16 v57, v42, v46
	v_pk_fma_f16 v34, v82, v34, v75
	v_pk_fma_f16 v35, v83, v35, v76
	v_pk_fma_f16 v36, v84, v36, v77
	v_pk_fma_f16 v37, v74, v37, v81
	s_waitcnt vmcnt(12)
	v_pk_fma_f16 v42, v82, v38, v75
	v_pk_fma_f16 v43, v83, v39, v76
	v_pk_add_f16 v100, v100, v104
	v_pk_add_f16 v51, v51, v55
	v_pk_add_f16 v50, v50, v54
	v_pk_add_f16 v54, v45, v49
	v_pk_add_f16 v55, v44, v48
	v_pk_fma_f16 v44, v84, v40, v77
	v_pk_fma_f16 v45, v74, v41, v81
	v_pk_max_f16 v41, v37, 0
	v_pk_max_f16 v40, v36, 0
	v_pk_max_f16 v39, v35, 0
	v_pk_max_f16 v38, v34, 0
	v_pk_max_f16 v43, v43, 0
	v_pk_max_f16 v42, v42, 0
	v_mov_b32_e32 v104, v0
	v_pk_max_f16 v45, v45, 0
	v_pk_max_f16 v44, v44, 0
	ds_write_b128 v116, v[38:41] offset:13056
	ds_write_b128 v116, v[42:45] offset:30464
	v_pk_add_f16 v36, v39, v43
	v_pk_add_f16 v37, v38, v42
	s_waitcnt lgkmcnt(0)
	s_barrier
	v_pk_add_f16 v101, v101, v105
	v_add_u32_e32 v38, 0xffffff00, v104
	v_lshlrev_b32_e32 v39, 3, v104
	v_lshrrev_b32_e32 v105, 4, v38
	v_and_b32_e32 v39, 56, v39
	v_lshrrev_b32_e32 v47, 3, v38
	v_ashrrev_i32_e32 v38, 3, v38
	v_lshl_or_b32 v46, v39, 1, v132
	v_bfi_b32 v43, s10, v38, v47
	v_or_b32_e32 v42, s2, v39
	v_mad_u64_u32 v[38:39], s[8:9], v43, s11, v[46:47]
	v_pk_add_f16 v34, v41, v45
	v_pk_add_f16 v35, v40, v44
	ds_read_b128 v[38:41], v38 offset:18432
	v_pk_add_f16 v102, v102, v106
	v_lshlrev_b32_e32 v106, 1, v42
	v_lshrrev_b32_e32 v49, 3, v104
	v_ashrrev_i32_e32 v42, 3, v104
	v_pk_add_f16 v103, v103, v107
	v_bfi_b32 v107, s10, v42, v49
	v_lshl_add_u32 v48, v43, 8, v106
	v_mad_u64_u32 v[42:43], s[8:9], v107, s11, v[46:47]
	ds_read_b128 v[42:45], v42 offset:18432
	s_waitcnt lgkmcnt(1)
	buffer_store_dwordx4 v[38:41], v48, s[4:7], 0 offen sc1
	v_lshl_add_u32 v107, v107, 8, v106
	s_waitcnt vmcnt(11)
	v_pk_fma_f16 v18, v82, v18, v85
	v_add_u32_e32 v38, 0x100, v104
	v_ashrrev_i32_e32 v38, 3, v38
	v_bfi_b32 v116, s10, v38, v47
	v_mad_u64_u32 v[38:39], s[8:9], v116, s11, v[46:47]
	v_add_u32_e32 v47, 0x200, v104
	v_ashrrev_i32_e32 v47, 3, v47
	v_bfi_b32 v117, s10, v47, v49
	ds_read_b128 v[38:41], v38 offset:18432
	v_mad_u64_u32 v[46:47], s[8:9], v117, s11, v[46:47]
	ds_read_b128 v[46:49], v46 offset:18432
	s_waitcnt lgkmcnt(2)
	buffer_store_dwordx4 v[42:45], v107, s[4:7], 0 offen sc1
	v_pk_fma_f16 v19, v83, v19, v86
	v_pk_fma_f16 v20, v84, v20, v89
	v_lshl_add_u32 v42, v116, 8, v106
	s_waitcnt lgkmcnt(1)
	buffer_store_dwordx4 v[38:41], v42, s[4:7], 0 offen sc1
	v_pk_fma_f16 v21, v74, v21, v93
	s_waitcnt vmcnt(9)
	v_pk_fma_f16 v24, v84, v24, v89
	v_lshl_add_u32 v38, v117, 8, v106
	s_waitcnt lgkmcnt(0)
	buffer_store_dwordx4 v[46:49], v38, s[4:7], 0 offen sc1
	v_lshlrev_b32_e32 v38, 4, v104
	v_pk_fma_f16 v39, v83, v109, v88
	v_and_b32_e32 v46, 0xf0, v38
	v_pk_fma_f16 v38, v82, v108, v87
	v_pk_fma_f16 v40, v84, v110, v92
	v_pk_fma_f16 v41, v74, v111, v95
	v_pk_fma_f16 v25, v74, v25, v93
	v_pk_fma_f16 v10, v82, v10, v78
	v_pk_fma_f16 v11, v83, v11, v79
	v_pk_fma_f16 v12, v84, v12, v80
	v_pk_fma_f16 v13, v74, v13, v91
	v_pk_fma_f16 v2, v82, v2, v75
	v_pk_fma_f16 v3, v83, v3, v76
	v_pk_fma_f16 v4, v84, v4, v77
	v_pk_fma_f16 v5, v74, v5, v81
	s_waitcnt vmcnt(8)
	v_pk_fma_f16 v6, v82, v6, v75
	v_pk_fma_f16 v7, v83, v7, v76
	v_pk_fma_f16 v42, v82, v112, v87
	v_pk_fma_f16 v43, v83, v113, v88
	v_pk_fma_f16 v44, v84, v114, v92
	v_pk_fma_f16 v45, v74, v115, v95
	v_pk_max_f16 v41, v41, 0
	v_pk_max_f16 v40, v40, 0
	v_pk_max_f16 v39, v39, 0
	v_pk_max_f16 v38, v38, 0
	v_mad_u64_u32 v[46:47], s[8:9], v105, s22, v[46:47]
	v_pk_fma_f16 v22, v82, v22, v85
	v_pk_fma_f16 v23, v83, v23, v86
	v_pk_max_f16 v21, v21, 0
	v_pk_max_f16 v20, v20, 0
	v_pk_max_f16 v19, v19, 0
	v_pk_max_f16 v18, v18, 0
	v_pk_max_f16 v25, v25, 0
	v_pk_max_f16 v24, v24, 0
	v_pk_fma_f16 v14, v82, v14, v78
	v_pk_fma_f16 v15, v83, v15, v79
	v_pk_fma_f16 v16, v84, v16, v80
	v_pk_fma_f16 v17, v74, v17, v91
	v_pk_max_f16 v13, v13, 0
	v_pk_max_f16 v12, v12, 0
	v_pk_max_f16 v11, v11, 0
	v_pk_max_f16 v10, v10, 0
	v_pk_fma_f16 v8, v84, v8, v77
	v_pk_fma_f16 v9, v74, v9, v81
	v_pk_max_f16 v5, v5, 0
	v_pk_max_f16 v4, v4, 0
	v_pk_max_f16 v3, v3, 0
	v_pk_max_f16 v2, v2, 0
	v_pk_max_f16 v7, v7, 0
	v_pk_max_f16 v6, v6, 0
	v_pk_max_f16 v45, v45, 0
	v_pk_max_f16 v44, v44, 0
	v_pk_max_f16 v43, v43, 0
	v_pk_max_f16 v42, v42, 0
	ds_write_b128 v46, v[38:41] offset:34816
	ds_write_b128 v46, v[42:45] offset:52224
	v_pk_max_f16 v23, v23, 0
	v_pk_max_f16 v22, v22, 0
	ds_write_b128 v46, v[18:21] offset:39168
	ds_write_b128 v46, v[22:25] offset:56576
	v_pk_add_f16 v21, v21, v25
	v_pk_add_f16 v20, v20, v24
	v_pk_max_f16 v17, v17, 0
	v_pk_max_f16 v16, v16, 0
	v_pk_max_f16 v15, v15, 0
	v_pk_max_f16 v14, v14, 0
	ds_write_b128 v46, v[10:13] offset:43520
	ds_write_b128 v46, v[14:17] offset:60928
	v_pk_max_f16 v9, v9, 0
	v_pk_max_f16 v8, v8, 0
	ds_write_b128 v46, v[2:5] offset:47872
	ds_write_b128 v46, v[6:9] offset:65280
	v_pk_add_f16 v24, v3, v7
	v_pk_add_f16 v25, v2, v6
	v_cvt_f32_f16_e32 v2, v73
	v_cvt_f32_f16_sdwa v3, v73 dst_sel:DWORD dst_unused:UNUSED_PAD src0_sel:WORD_1
	v_pk_add_f16 v19, v19, v23
	v_pk_add_f16 v18, v18, v22
	v_pk_add_f16 v22, v5, v9
	v_pk_add_f16 v23, v4, v8
	v_cvt_f32_f16_e32 v4, v129
	v_cvt_f32_f16_sdwa v5, v129 dst_sel:DWORD dst_unused:UNUSED_PAD src0_sel:WORD_1
	v_pk_add_f16 v38, v38, v42
	v_cvt_f32_f16_e32 v6, v100
	v_cvt_f32_f16_sdwa v7, v100 dst_sel:DWORD dst_unused:UNUSED_PAD src0_sel:WORD_1
	v_cvt_f32_f16_e32 v8, v38
	v_cvt_f32_f16_sdwa v9, v38 dst_sel:DWORD dst_unused:UNUSED_PAD src0_sel:WORD_1
	v_pk_add_f32 v[2:3], v[2:3], 0 op_sel_hi:[1,0]
	v_pk_add_f16 v39, v39, v43
	v_pk_add_f32 v[2:3], v[2:3], v[4:5]
	v_cvt_f32_f16_e32 v4, v72
	v_cvt_f32_f16_sdwa v5, v72 dst_sel:DWORD dst_unused:UNUSED_PAD src0_sel:WORD_1
	v_pk_add_f32 v[2:3], v[2:3], v[6:7]
	v_cvt_f32_f16_e32 v6, v128
	v_cvt_f32_f16_sdwa v7, v128 dst_sel:DWORD dst_unused:UNUSED_PAD src0_sel:WORD_1
	v_pk_add_f32 v[2:3], v[2:3], v[8:9]
	v_cvt_f32_f16_e32 v8, v101
	v_cvt_f32_f16_sdwa v9, v101 dst_sel:DWORD dst_unused:UNUSED_PAD src0_sel:WORD_1
	v_pk_add_f16 v15, v11, v15
	v_pk_add_f16 v14, v10, v14
	v_cvt_f32_f16_e32 v10, v39
	v_cvt_f32_f16_sdwa v11, v39 dst_sel:DWORD dst_unused:UNUSED_PAD src0_sel:WORD_1
	v_pk_add_f32 v[4:5], v[4:5], 0 op_sel_hi:[1,0]
	s_mov_b32 s2, 0x3e000000
	v_pk_add_f32 v[4:5], v[4:5], v[6:7]
	v_pk_mul_f32 v[2:3], v[2:3], s[2:3] op_sel_hi:[1,0]
	v_pk_add_f32 v[4:5], v[4:5], v[8:9]
	v_cvt_pk_f16_f32 v2, v2, v3
	v_pk_add_f32 v[4:5], v[4:5], v[10:11]
	v_cvt_f32_f16_e32 v6, v99
	v_pk_mul_f32 v[4:5], v[4:5], s[2:3] op_sel_hi:[1,0]
	v_cvt_f32_f16_sdwa v7, v99 dst_sel:DWORD dst_unused:UNUSED_PAD src0_sel:WORD_1
	v_cvt_pk_f16_f32 v3, v4, v5
	v_cvt_f32_f16_e32 v4, v71
	v_cvt_f32_f16_sdwa v5, v71 dst_sel:DWORD dst_unused:UNUSED_PAD src0_sel:WORD_1
	v_pk_add_f16 v40, v40, v44
	v_cvt_f32_f16_e32 v8, v102
	v_cvt_f32_f16_sdwa v9, v102 dst_sel:DWORD dst_unused:UNUSED_PAD src0_sel:WORD_1
	v_cvt_f32_f16_e32 v10, v40
	v_cvt_f32_f16_sdwa v11, v40 dst_sel:DWORD dst_unused:UNUSED_PAD src0_sel:WORD_1
	v_pk_add_f32 v[4:5], v[4:5], 0 op_sel_hi:[1,0]
	v_pk_add_f16 v41, v41, v45
	v_pk_add_f32 v[4:5], v[4:5], v[6:7]
	v_cvt_f32_f16_e32 v6, v69
	v_cvt_f32_f16_sdwa v7, v69 dst_sel:DWORD dst_unused:UNUSED_PAD src0_sel:WORD_1
	v_pk_add_f32 v[4:5], v[4:5], v[8:9]
	v_cvt_f32_f16_e32 v8, v97
	v_cvt_f32_f16_sdwa v9, v97 dst_sel:DWORD dst_unused:UNUSED_PAD src0_sel:WORD_1
	v_pk_add_f32 v[4:5], v[4:5], v[10:11]
	v_cvt_f32_f16_e32 v10, v103
	v_cvt_f32_f16_sdwa v11, v103 dst_sel:DWORD dst_unused:UNUSED_PAD src0_sel:WORD_1
	v_pk_add_f16 v17, v13, v17
	v_pk_add_f16 v16, v12, v16
	v_cvt_f32_f16_e32 v12, v41
	v_cvt_f32_f16_sdwa v13, v41 dst_sel:DWORD dst_unused:UNUSED_PAD src0_sel:WORD_1
	v_pk_add_f32 v[6:7], v[6:7], 0 op_sel_hi:[1,0]
	v_pk_mul_f32 v[4:5], v[4:5], s[2:3] op_sel_hi:[1,0]
	v_pk_add_f32 v[6:7], v[6:7], v[8:9]
	v_cvt_pk_f16_f32 v4, v4, v5
	v_pk_add_f32 v[6:7], v[6:7], v[10:11]
	v_add_u32_e32 v38, 0x1a000, v46
	v_pk_add_f32 v[6:7], v[6:7], v[12:13]
	v_cvt_f32_f16_e32 v8, v18
	v_pk_mul_f32 v[6:7], v[6:7], s[2:3] op_sel_hi:[1,0]
	v_cvt_f32_f16_sdwa v9, v18 dst_sel:DWORD dst_unused:UNUSED_PAD src0_sel:WORD_1
	v_cvt_pk_f16_f32 v5, v6, v7
	ds_write_b128 v38, v[2:5]
	v_cvt_f32_f16_e32 v2, v70
	v_cvt_f32_f16_sdwa v3, v70 dst_sel:DWORD dst_unused:UNUSED_PAD src0_sel:WORD_1
	v_cvt_f32_f16_e32 v4, v98
	v_cvt_f32_f16_sdwa v5, v98 dst_sel:DWORD dst_unused:UNUSED_PAD src0_sel:WORD_1
	v_cvt_f32_f16_e32 v6, v50
	v_cvt_f32_f16_sdwa v7, v50 dst_sel:DWORD dst_unused:UNUSED_PAD src0_sel:WORD_1
	v_pk_add_f32 v[2:3], v[2:3], 0 op_sel_hi:[1,0]
	v_cvt_f32_f16_e32 v10, v19
	v_pk_add_f32 v[2:3], v[2:3], v[4:5]
	v_cvt_f32_f16_e32 v4, v68
	v_cvt_f32_f16_sdwa v5, v68 dst_sel:DWORD dst_unused:UNUSED_PAD src0_sel:WORD_1
	v_pk_add_f32 v[2:3], v[2:3], v[6:7]
	v_cvt_f32_f16_e32 v6, v96
	v_cvt_f32_f16_sdwa v7, v96 dst_sel:DWORD dst_unused:UNUSED_PAD src0_sel:WORD_1
	v_pk_add_f32 v[2:3], v[2:3], v[8:9]
	v_cvt_f32_f16_e32 v8, v51
	v_cvt_f32_f16_sdwa v9, v51 dst_sel:DWORD dst_unused:UNUSED_PAD src0_sel:WORD_1
	v_cvt_f32_f16_sdwa v11, v19 dst_sel:DWORD dst_unused:UNUSED_PAD src0_sel:WORD_1
	v_pk_add_f32 v[4:5], v[4:5], 0 op_sel_hi:[1,0]
	v_pk_mul_f32 v[2:3], v[2:3], s[2:3] op_sel_hi:[1,0]
	v_pk_add_f32 v[4:5], v[4:5], v[6:7]
	v_cvt_pk_f16_f32 v2, v2, v3
	v_pk_add_f32 v[4:5], v[4:5], v[8:9]
	v_cvt_f32_f16_e32 v6, v94
	v_pk_add_f32 v[4:5], v[4:5], v[10:11]
	v_cvt_f32_f16_sdwa v7, v94 dst_sel:DWORD dst_unused:UNUSED_PAD src0_sel:WORD_1
	v_pk_mul_f32 v[4:5], v[4:5], s[2:3] op_sel_hi:[1,0]
	v_cvt_f32_f16_e32 v8, v52
	v_cvt_pk_f16_f32 v3, v4, v5
	v_cvt_f32_f16_e32 v4, v67
	v_cvt_f32_f16_sdwa v5, v67 dst_sel:DWORD dst_unused:UNUSED_PAD src0_sel:WORD_1
	v_cvt_f32_f16_sdwa v9, v52 dst_sel:DWORD dst_unused:UNUSED_PAD src0_sel:WORD_1
	v_cvt_f32_f16_e32 v10, v20
	v_cvt_f32_f16_sdwa v11, v20 dst_sel:DWORD dst_unused:UNUSED_PAD src0_sel:WORD_1
	v_pk_add_f32 v[4:5], v[4:5], 0 op_sel_hi:[1,0]
	v_cvt_f32_f16_e32 v12, v21
	v_pk_add_f32 v[4:5], v[4:5], v[6:7]
	v_cvt_f32_f16_e32 v6, v65
	v_cvt_f32_f16_sdwa v7, v65 dst_sel:DWORD dst_unused:UNUSED_PAD src0_sel:WORD_1
	v_pk_add_f32 v[4:5], v[4:5], v[8:9]
	v_cvt_f32_f16_e32 v8, v33
	v_cvt_f32_f16_sdwa v9, v33 dst_sel:DWORD dst_unused:UNUSED_PAD src0_sel:WORD_1
	v_pk_add_f32 v[4:5], v[4:5], v[10:11]
	v_cvt_f32_f16_e32 v10, v53
	v_cvt_f32_f16_sdwa v11, v53 dst_sel:DWORD dst_unused:UNUSED_PAD src0_sel:WORD_1
	v_cvt_f32_f16_sdwa v13, v21 dst_sel:DWORD dst_unused:UNUSED_PAD src0_sel:WORD_1
	v_pk_add_f32 v[6:7], v[6:7], 0 op_sel_hi:[1,0]
	v_pk_mul_f32 v[4:5], v[4:5], s[2:3] op_sel_hi:[1,0]
	v_pk_add_f32 v[6:7], v[6:7], v[8:9]
	v_cvt_pk_f16_f32 v4, v4, v5
	v_pk_add_f32 v[6:7], v[6:7], v[10:11]
	v_cvt_f32_f16_e32 v8, v14
	v_pk_add_f32 v[6:7], v[6:7], v[12:13]
	v_cvt_f32_f16_sdwa v9, v14 dst_sel:DWORD dst_unused:UNUSED_PAD src0_sel:WORD_1
	v_pk_mul_f32 v[6:7], v[6:7], s[2:3] op_sel_hi:[1,0]
	v_cvt_f32_f16_e32 v10, v15
	v_cvt_pk_f16_f32 v5, v6, v7
	ds_write_b128 v38, v[2:5] offset:4352
	v_cvt_f32_f16_e32 v2, v66
	v_cvt_f32_f16_sdwa v3, v66 dst_sel:DWORD dst_unused:UNUSED_PAD src0_sel:WORD_1
	v_cvt_f32_f16_e32 v4, v90
	v_cvt_f32_f16_sdwa v5, v90 dst_sel:DWORD dst_unused:UNUSED_PAD src0_sel:WORD_1
	v_cvt_f32_f16_e32 v6, v57
	v_cvt_f32_f16_sdwa v7, v57 dst_sel:DWORD dst_unused:UNUSED_PAD src0_sel:WORD_1
	v_pk_add_f32 v[2:3], v[2:3], 0 op_sel_hi:[1,0]
	v_cvt_f32_f16_sdwa v11, v15 dst_sel:DWORD dst_unused:UNUSED_PAD src0_sel:WORD_1
	v_pk_add_f32 v[2:3], v[2:3], v[4:5]
	v_cvt_f32_f16_e32 v4, v64
	v_cvt_f32_f16_sdwa v5, v64 dst_sel:DWORD dst_unused:UNUSED_PAD src0_sel:WORD_1
	v_pk_add_f32 v[2:3], v[2:3], v[6:7]
	v_cvt_f32_f16_e32 v6, v32
	v_cvt_f32_f16_sdwa v7, v32 dst_sel:DWORD dst_unused:UNUSED_PAD src0_sel:WORD_1
	v_pk_add_f32 v[2:3], v[2:3], v[8:9]
	v_cvt_f32_f16_e32 v8, v56
	v_cvt_f32_f16_sdwa v9, v56 dst_sel:DWORD dst_unused:UNUSED_PAD src0_sel:WORD_1
	v_pk_add_f32 v[4:5], v[4:5], 0 op_sel_hi:[1,0]
	v_pk_mul_f32 v[2:3], v[2:3], s[2:3] op_sel_hi:[1,0]
	v_pk_add_f32 v[4:5], v[4:5], v[6:7]
	v_cvt_pk_f16_f32 v2, v2, v3
	v_pk_add_f32 v[4:5], v[4:5], v[8:9]
	v_cvt_f32_f16_e32 v6, v31
	v_pk_add_f32 v[4:5], v[4:5], v[10:11]
	v_cvt_f32_f16_sdwa v7, v31 dst_sel:DWORD dst_unused:UNUSED_PAD src0_sel:WORD_1
	v_pk_mul_f32 v[4:5], v[4:5], s[2:3] op_sel_hi:[1,0]
	v_cvt_f32_f16_e32 v8, v55
	v_cvt_pk_f16_f32 v3, v4, v5
	v_cvt_f32_f16_e32 v4, v63
	v_cvt_f32_f16_sdwa v5, v63 dst_sel:DWORD dst_unused:UNUSED_PAD src0_sel:WORD_1
	v_cvt_f32_f16_sdwa v9, v55 dst_sel:DWORD dst_unused:UNUSED_PAD src0_sel:WORD_1
	v_cvt_f32_f16_e32 v10, v16
	v_cvt_f32_f16_sdwa v11, v16 dst_sel:DWORD dst_unused:UNUSED_PAD src0_sel:WORD_1
	v_pk_add_f32 v[4:5], v[4:5], 0 op_sel_hi:[1,0]
	v_cvt_f32_f16_e32 v12, v17
	v_pk_add_f32 v[4:5], v[4:5], v[6:7]
	v_cvt_f32_f16_e32 v6, v61
	v_cvt_f32_f16_sdwa v7, v61 dst_sel:DWORD dst_unused:UNUSED_PAD src0_sel:WORD_1
	v_pk_add_f32 v[4:5], v[4:5], v[8:9]
	v_cvt_f32_f16_e32 v8, v29
	v_cvt_f32_f16_sdwa v9, v29 dst_sel:DWORD dst_unused:UNUSED_PAD src0_sel:WORD_1
	v_pk_add_f32 v[4:5], v[4:5], v[10:11]
	v_cvt_f32_f16_e32 v10, v54
	v_cvt_f32_f16_sdwa v11, v54 dst_sel:DWORD dst_unused:UNUSED_PAD src0_sel:WORD_1
	v_cvt_f32_f16_sdwa v13, v17 dst_sel:DWORD dst_unused:UNUSED_PAD src0_sel:WORD_1
	v_pk_add_f32 v[6:7], v[6:7], 0 op_sel_hi:[1,0]
	v_pk_mul_f32 v[4:5], v[4:5], s[2:3] op_sel_hi:[1,0]
	v_pk_add_f32 v[6:7], v[6:7], v[8:9]
	v_cvt_pk_f16_f32 v4, v4, v5
	v_pk_add_f32 v[6:7], v[6:7], v[10:11]
	v_cvt_f32_f16_e32 v8, v25
	v_pk_add_f32 v[6:7], v[6:7], v[12:13]
	v_cvt_f32_f16_sdwa v9, v25 dst_sel:DWORD dst_unused:UNUSED_PAD src0_sel:WORD_1
	v_pk_mul_f32 v[6:7], v[6:7], s[2:3] op_sel_hi:[1,0]
	v_cvt_f32_f16_e32 v10, v24
	v_cvt_pk_f16_f32 v5, v6, v7
	ds_write_b128 v38, v[2:5] offset:8704
	v_cvt_f32_f16_e32 v2, v62
	v_cvt_f32_f16_sdwa v3, v62 dst_sel:DWORD dst_unused:UNUSED_PAD src0_sel:WORD_1
	v_cvt_f32_f16_e32 v4, v30
	v_cvt_f32_f16_sdwa v5, v30 dst_sel:DWORD dst_unused:UNUSED_PAD src0_sel:WORD_1
	v_cvt_f32_f16_e32 v6, v37
	v_cvt_f32_f16_sdwa v7, v37 dst_sel:DWORD dst_unused:UNUSED_PAD src0_sel:WORD_1
	v_pk_add_f32 v[2:3], v[2:3], 0 op_sel_hi:[1,0]
	v_cvt_f32_f16_sdwa v11, v24 dst_sel:DWORD dst_unused:UNUSED_PAD src0_sel:WORD_1
	v_pk_add_f32 v[2:3], v[2:3], v[4:5]
	v_cvt_f32_f16_e32 v4, v60
	v_cvt_f32_f16_sdwa v5, v60 dst_sel:DWORD dst_unused:UNUSED_PAD src0_sel:WORD_1
	v_pk_add_f32 v[2:3], v[2:3], v[6:7]
	v_cvt_f32_f16_e32 v6, v28
	v_cvt_f32_f16_sdwa v7, v28 dst_sel:DWORD dst_unused:UNUSED_PAD src0_sel:WORD_1
	v_pk_add_f32 v[2:3], v[2:3], v[8:9]
	v_cvt_f32_f16_e32 v8, v36
	v_cvt_f32_f16_sdwa v9, v36 dst_sel:DWORD dst_unused:UNUSED_PAD src0_sel:WORD_1
	v_pk_add_f32 v[4:5], v[4:5], 0 op_sel_hi:[1,0]
	v_pk_mul_f32 v[2:3], v[2:3], s[2:3] op_sel_hi:[1,0]
	v_pk_add_f32 v[4:5], v[4:5], v[6:7]
	v_cvt_pk_f16_f32 v2, v2, v3
	v_pk_add_f32 v[4:5], v[4:5], v[8:9]
	v_cvt_f32_f16_e32 v6, v27
	v_pk_add_f32 v[4:5], v[4:5], v[10:11]
	v_cvt_f32_f16_sdwa v7, v27 dst_sel:DWORD dst_unused:UNUSED_PAD src0_sel:WORD_1
	v_pk_mul_f32 v[4:5], v[4:5], s[2:3] op_sel_hi:[1,0]
	v_cvt_f32_f16_e32 v8, v35
	v_cvt_pk_f16_f32 v3, v4, v5
	v_cvt_f32_f16_e32 v4, v59
	v_cvt_f32_f16_sdwa v5, v59 dst_sel:DWORD dst_unused:UNUSED_PAD src0_sel:WORD_1
	v_cvt_f32_f16_sdwa v9, v35 dst_sel:DWORD dst_unused:UNUSED_PAD src0_sel:WORD_1
	v_cvt_f32_f16_e32 v10, v23
	v_cvt_f32_f16_sdwa v11, v23 dst_sel:DWORD dst_unused:UNUSED_PAD src0_sel:WORD_1
	v_pk_add_f32 v[4:5], v[4:5], 0 op_sel_hi:[1,0]
	v_cvt_f32_f16_e32 v12, v22
	v_pk_add_f32 v[4:5], v[4:5], v[6:7]
	v_cvt_f32_f16_e32 v6, v58
	v_cvt_f32_f16_sdwa v7, v58 dst_sel:DWORD dst_unused:UNUSED_PAD src0_sel:WORD_1
	v_pk_add_f32 v[4:5], v[4:5], v[8:9]
	v_cvt_f32_f16_e32 v8, v26
	v_cvt_f32_f16_sdwa v9, v26 dst_sel:DWORD dst_unused:UNUSED_PAD src0_sel:WORD_1
	v_pk_add_f32 v[4:5], v[4:5], v[10:11]
	v_cvt_f32_f16_e32 v10, v34
	v_cvt_f32_f16_sdwa v11, v34 dst_sel:DWORD dst_unused:UNUSED_PAD src0_sel:WORD_1
	v_cvt_f32_f16_sdwa v13, v22 dst_sel:DWORD dst_unused:UNUSED_PAD src0_sel:WORD_1
	v_pk_add_f32 v[6:7], v[6:7], 0 op_sel_hi:[1,0]
	v_pk_mul_f32 v[4:5], v[4:5], s[2:3] op_sel_hi:[1,0]
	v_pk_add_f32 v[6:7], v[6:7], v[8:9]
	s_cmpk_lt_u32 s15, 0x180
	v_pk_add_f32 v[6:7], v[6:7], v[10:11]
	v_cvt_pk_f16_f32 v4, v4, v5
	v_pk_add_f32 v[6:7], v[6:7], v[12:13]
	s_cselect_b64 s[8:9], -1, 0
	v_pk_mul_f32 v[6:7], v[6:7], s[2:3] op_sel_hi:[1,0]
	s_cmpk_gt_u32 s15, 0x17f
	v_cvt_pk_f16_f32 v5, v6, v7
	ds_write_b128 v38, v[2:5] offset:13056
	s_cbranch_scc1 .LBB3_3
	s_load_dwordx2 s[10:11], s[0:1], 0x78
	s_load_dwordx4 s[24:27], s[0:1], 0x50
	v_mov_b32_e32 v2, v0
	s_lshl_b64 s[22:23], s[12:13], 12
	s_waitcnt lgkmcnt(0)
	s_add_u32 s10, s10, s22
	v_lshlrev_b32_e32 v2, 3, v2
	s_addc_u32 s11, s11, s23
	v_and_b32_e32 v2, 0x1f8, v2
	global_load_dwordx2 v[136:137], v2, s[10:11]
	global_load_dwordx2 v[132:133], v2, s[10:11] offset:512
	global_load_dwordx2 v[128:129], v2, s[10:11] offset:1024
	global_load_dwordx2 v[124:125], v2, s[10:11] offset:1536
	global_load_dwordx2 v[134:135], v2, s[10:11] offset:2048
	global_load_dwordx2 v[130:131], v2, s[10:11] offset:2560
	global_load_dwordx2 v[126:127], v2, s[10:11] offset:3072
	global_load_dwordx2 v[122:123], v2, s[10:11] offset:3584
	s_lshl_b32 s2, s14, 4
	s_lshl_b32 s10, s17, 3
	s_add_i32 s10, s10, s2
	s_sub_i32 s2, s10, 32
	s_lshl_b64 s[2:3], s[2:3], 10
	v_lshl_or_b32 v2, v2, 1, s2
	v_mov_b32_e32 v3, s3
	v_lshl_add_u64 v[4:5], s[24:25], 0, v[2:3]
	global_load_dwordx4 v[18:21], v[4:5], off
	global_load_dwordx4 v[102:105], v[4:5], off offset:1024
	global_load_dwordx4 v[94:97], v[4:5], off offset:2048
	global_load_dwordx4 v[86:89], v[4:5], off offset:3072
	v_add_co_u32_e32 v4, vcc, s20, v4
	v_lshl_add_u64 v[6:7], s[26:27], 0, v[2:3]
	s_nop 0
	v_addc_co_u32_e32 v5, vcc, 0, v5, vcc
	global_load_dwordx4 v[78:81], v[4:5], off
	global_load_dwordx4 v[74:77], v[4:5], off offset:1024
	global_load_dwordx4 v[70:73], v[4:5], off offset:2048
	global_load_dwordx4 v[66:69], v[4:5], off offset:3072
	s_nop 0
	global_load_dwordx4 v[2:5], v[6:7], off
	global_load_dwordx4 v[118:121], v[6:7], off offset:1024
	global_load_dwordx4 v[114:117], v[6:7], off offset:2048
	global_load_dwordx4 v[110:113], v[6:7], off offset:3072
	v_add_co_u32_e32 v6, vcc, s20, v6
	s_nop 1
	v_addc_co_u32_e32 v7, vcc, 0, v7, vcc
	global_load_dwordx4 v[106:109], v[6:7], off
	global_load_dwordx4 v[98:101], v[6:7], off offset:1024
	global_load_dwordx4 v[90:93], v[6:7], off offset:2048
	global_load_dwordx4 v[82:85], v[6:7], off offset:3072
	s_branch .LBB3_4

.LBB3_6:
	s_load_dwordx2 s[2:3], s[0:1], 0x90
	s_andn2_b64 vcc, exec, s[8:9]
	s_cbranch_vccnz .LBB3_10
	v_mov_b32_e32 v154, v0
	s_mov_b32 s8, 0x1a000
	v_and_b32_e32 v155, 31, v154
	v_bfe_u32 v156, v154, 5, 1
	v_mul_u32_u24_e32 v6, 0x110, v155
	v_lshlrev_b32_e32 v7, 4, v156
	v_add3_u32 v157, v6, v7, s8
	ds_read_b128 v[6:9], v157
	ds_read_b128 v[22:25], v157 offset:8704
	ds_read_b128 v[138:141], v157 offset:32
	ds_read_b128 v[142:145], v157 offset:8736
	s_mov_b32 s13, 0xc060c00
	s_waitcnt vmcnt(7) lgkmcnt(0)
	v_mfma_f32_32x32x16_f16 v[50:65], v[6:9], v[2:5], 0
	s_load_dwordx2 s[10:11], s[0:1], 0x68
	s_mov_b32 s20, 0xe400
	s_lshl_b32 s17, s17, 5
	s_add_i32 s17, s17, s18
	s_addk_i32 s17, 0xff80
	s_load_dwordx2 s[8:9], s[0:1], 0x88
	s_waitcnt lgkmcnt(0)
	s_and_b32 s9, s9, 0xffff
	v_mfma_f32_32x32x16_f16 v[34:49], v[22:25], v[2:5], 0
	v_mfma_f32_32x32x16_f16 v[2:17], v[6:9], v[18:21], 0
	v_mfma_f32_32x32x16_f16 v[18:33], v[22:25], v[18:21], 0
	ds_read_b128 v[146:149], v157 offset:64
	ds_read_b128 v[150:153], v157 offset:8768
	s_waitcnt vmcnt(6)
	v_mfma_f32_32x32x16_f16 v[50:65], v[138:141], v[118:121], v[50:65]
	v_mfma_f32_32x32x16_f16 v[34:49], v[142:145], v[118:121], v[34:49]
	v_mfma_f32_32x32x16_f16 v[2:17], v[138:141], v[102:105], v[2:17]
	v_mfma_f32_32x32x16_f16 v[18:33], v[142:145], v[102:105], v[18:33]
	ds_read_b128 v[102:105], v157 offset:96
	ds_read_b128 v[118:121], v157 offset:8800
	s_waitcnt vmcnt(5) lgkmcnt(3)
	v_mfma_f32_32x32x16_f16 v[50:65], v[146:149], v[114:117], v[50:65]
	s_waitcnt lgkmcnt(2)
	v_mfma_f32_32x32x16_f16 v[34:49], v[150:153], v[114:117], v[34:49]
	v_mfma_f32_32x32x16_f16 v[2:17], v[146:149], v[94:97], v[2:17]
	v_mfma_f32_32x32x16_f16 v[18:33], v[150:153], v[94:97], v[18:33]
	ds_read_b128 v[94:97], v157 offset:128
	ds_read_b128 v[114:117], v157 offset:8832
	s_waitcnt vmcnt(4) lgkmcnt(3)
	v_mfma_f32_32x32x16_f16 v[50:65], v[102:105], v[110:113], v[50:65]
	s_waitcnt lgkmcnt(2)
	v_mfma_f32_32x32x16_f16 v[34:49], v[118:121], v[110:113], v[34:49]
	v_mfma_f32_32x32x16_f16 v[2:17], v[102:105], v[86:89], v[2:17]
	v_mfma_f32_32x32x16_f16 v[18:33], v[118:121], v[86:89], v[18:33]
	ds_read_b128 v[86:89], v157 offset:160
	ds_read_b128 v[102:105], v157 offset:8864
	s_waitcnt vmcnt(3) lgkmcnt(3)
	v_mfma_f32_32x32x16_f16 v[50:65], v[94:97], v[106:109], v[50:65]
	s_waitcnt lgkmcnt(2)
	v_mfma_f32_32x32x16_f16 v[34:49], v[114:117], v[106:109], v[34:49]
	v_mfma_f32_32x32x16_f16 v[2:17], v[94:97], v[78:81], v[2:17]
	v_mfma_f32_32x32x16_f16 v[18:33], v[114:117], v[78:81], v[18:33]
	ds_read_b128 v[78:81], v157 offset:192
	ds_read_b128 v[94:97], v157 offset:8896
	s_waitcnt vmcnt(2) lgkmcnt(3)
	v_mfma_f32_32x32x16_f16 v[50:65], v[86:89], v[98:101], v[50:65]
	s_waitcnt lgkmcnt(2)
	v_mfma_f32_32x32x16_f16 v[34:49], v[102:105], v[98:101], v[34:49]
	v_mfma_f32_32x32x16_f16 v[2:17], v[86:89], v[74:77], v[2:17]
	v_mfma_f32_32x32x16_f16 v[18:33], v[102:105], v[74:77], v[18:33]
	ds_read_b128 v[74:77], v157 offset:224
	ds_read_b128 v[86:89], v157 offset:8928
	s_waitcnt vmcnt(1) lgkmcnt(3)
	v_mfma_f32_32x32x16_f16 v[50:65], v[78:81], v[90:93], v[50:65]
	s_waitcnt lgkmcnt(2)
	v_mfma_f32_32x32x16_f16 v[34:49], v[94:97], v[90:93], v[34:49]
	v_mfma_f32_32x32x16_f16 v[2:17], v[78:81], v[70:73], v[2:17]
	v_lshrrev_b32_e32 v81, 16, v127
	v_mfma_f32_32x32x16_f16 v[18:33], v[94:97], v[70:73], v[18:33]
	v_perm_b32 v73, v240, v130, s43
	s_waitcnt vmcnt(0) lgkmcnt(1)
	v_mfma_f32_32x32x16_f16 v[50:65], v[74:77], v[82:85], v[50:65]
	v_pk_add_f16 v73, v73, s20 op_sel_hi:[1,0]
	v_and_b32_e32 v70, 63, v154
	v_cmp_gt_u32_e32 vcc, 32, v70
	s_waitcnt lgkmcnt(0)
	v_mfma_f32_32x32x16_f16 v[34:49], v[86:89], v[82:85], v[34:49]
	s_nop 6
	v_cvt_pk_f16_f32 v65, v64, v65
	v_cvt_pk_f16_f32 v64, v62, v63
	v_cvt_pk_f16_f32 v63, v60, v61
	v_cvt_pk_f16_f32 v57, v56, v57
	v_cvt_pk_f16_f32 v56, v54, v55
	v_cvt_pk_f16_f32 v55, v52, v53
	v_mfma_f32_32x32x16_f16 v[2:17], v[74:77], v[66:69], v[2:17]
	v_perm_b32 v74, v240, v131, s42
	v_cvt_pk_f16_f32 v41, v40, v41
	v_cvt_pk_f16_f32 v40, v38, v39
	v_cvt_pk_f16_f32 v38, v34, v35
	v_mfma_f32_32x32x16_f16 v[18:33], v[86:89], v[66:69], v[18:33]
	v_perm_b32 v71, v240, v130, s42
	v_perm_b32 v75, v240, v131, s43
	v_pk_add_f16 v72, v71, s20 op_sel_hi:[1,0]
	v_perm_b32 v71, v240, v128, s42
	v_perm_b32 v77, v240, v128, s43
	v_or_b32_e32 v34, s17, v155
	v_mov_b32_e32 v35, 0
	v_cvt_pk_f16_f32 v39, v36, v37
	v_lshl_add_u64 v[36:37], v[34:35], 2, s[10:11]
	global_load_dword v80, v[36:37], off
	v_cvt_pk_f16_f32 v54, v50, v51
	v_perm_b32 v50, v240, v136, s42
	v_perm_b32 v51, v240, v136, s43
	v_perm_b32 v52, v240, v137, s42
	v_perm_b32 v53, v240, v137, s43
	v_perm_b32 v66, v240, v134, s42
	v_perm_b32 v67, v240, v134, s43
	v_perm_b32 v68, v240, v135, s42
	v_perm_b32 v69, v240, v135, s43
	v_pk_add_f16 v50, v50, s20 op_sel_hi:[1,0]
	v_pk_add_f16 v51, v51, s20 op_sel_hi:[1,0]
	v_pk_add_f16 v52, v52, s20 op_sel_hi:[1,0]
	v_pk_add_f16 v53, v53, s20 op_sel_hi:[1,0]
	v_pk_add_f16 v66, v66, s20 op_sel_hi:[1,0]
	v_pk_add_f16 v67, v67, s20 op_sel_hi:[1,0]
	v_pk_add_f16 v68, v68, s20 op_sel_hi:[1,0]
	v_pk_add_f16 v69, v69, s20 op_sel_hi:[1,0]
	v_cvt_pk_f16_f32 v62, v58, v59
	v_mfma_f32_32x32x16_f16 v[2:17], v[50:53], v[54:57], v[2:17]
	v_perm_b32 v58, v240, v132, s42
	v_perm_b32 v59, v240, v132, s43
	v_perm_b32 v60, v240, v133, s42
	v_perm_b32 v61, v240, v133, s43
	v_pk_add_f16 v58, v58, s20 op_sel_hi:[1,0]
	v_mfma_f32_32x32x16_f16 v[18:33], v[66:69], v[54:57], v[18:33]
	v_pk_add_f16 v59, v59, s20 op_sel_hi:[1,0]
	v_pk_add_f16 v60, v60, s20 op_sel_hi:[1,0]
	v_pk_add_f16 v61, v61, s20 op_sel_hi:[1,0]
	v_pk_add_f16 v74, v74, s20 op_sel_hi:[1,0]
	v_pk_add_f16 v75, v75, s20 op_sel_hi:[1,0]
	v_perm_b32 v36, v240, v129, s42
	v_perm_b32 v37, v240, v129, s43
	v_pk_add_f16 v76, v71, s20 op_sel_hi:[1,0]
	v_pk_add_f16 v79, v37, s20 op_sel_hi:[1,0]
	v_pk_add_f16 v78, v36, s20 op_sel_hi:[1,0]
	v_lshrrev_b32_e32 v82, 8, v127
	v_mfma_f32_32x32x16_f16 v[2:17], v[58:61], v[62:65], v[2:17]
	v_perm_b32 v81, v82, v81, s13
	v_perm_b32 v36, v240, v126, s42
	v_perm_b32 v37, v240, v126, s43
	v_perm_b32 v71, v240, v127, s42
	v_or_b32_e32 v81, 0x64006400, v81
	v_mfma_f32_32x32x16_f16 v[18:33], v[72:75], v[62:65], v[18:33]
	v_pk_add_f16 v77, v77, s20 op_sel_hi:[1,0]
	v_pk_add_f16 v50, v36, s20 op_sel_hi:[1,0]
	v_pk_add_f16 v51, v37, s20 op_sel_hi:[1,0]
	v_pk_add_f16 v52, v71, s20 op_sel_hi:[1,0]
	v_pk_add_f16 v53, v81, s20 op_sel_hi:[1,0]
	v_cvt_pk_f16_f32 v49, v48, v49
	v_cvt_pk_f16_f32 v48, v46, v47
	v_cvt_pk_f16_f32 v46, v42, v43
	v_cvt_pk_f16_f32 v47, v44, v45
	v_perm_b32 v37, v240, v124, s43
	v_perm_b32 v44, v240, v125, s42
	v_perm_b32 v36, v240, v124, s42
	v_pk_add_f16 v43, v37, s20 op_sel_hi:[1,0]
	v_lshrrev_b32_e32 v37, 16, v122
	v_lshrrev_b32_e32 v54, 8, v122
	v_perm_b32 v45, v240, v125, s43
	v_pk_add_f16 v42, v36, s20 op_sel_hi:[1,0]
	v_mfma_f32_32x32x16_f16 v[2:17], v[76:79], v[38:41], v[2:17]
	v_perm_b32 v37, v54, v37, s13
	v_lshlrev_b32_e32 v54, 8, v123
	v_perm_b32 v54, v54, v123, s13
	v_perm_b32 v36, v240, v122, s42
	v_or_b32_e32 v37, 0x64006400, v37
	v_pk_add_f16 v36, v36, s20 op_sel_hi:[1,0]
	v_mfma_f32_32x32x16_f16 v[18:33], v[50:53], v[38:41], v[18:33]
	v_or_b32_e32 v38, 0x64006400, v54
	v_perm_b32 v39, v240, v123, s43
	v_pk_add_f16 v37, v37, s20 op_sel_hi:[1,0]
	v_pk_add_f16 v38, v38, s20 op_sel_hi:[1,0]
	v_pk_add_f16 v39, v39, s20 op_sel_hi:[1,0]
	v_pk_add_f16 v44, v44, s20 op_sel_hi:[1,0]
	v_pk_add_f16 v45, v45, s20 op_sel_hi:[1,0]
	v_mfma_f32_32x32x16_f16 v[18:33], v[36:39], v[46:49], v[18:33]
	s_lshl_b32 s13, s12, 14
	v_lshlrev_b32_e32 v40, 1, v34
	v_lshl_or_b32 v38, v156, 10, s13
	s_mov_b32 s11, 0x20000
	s_mov_b32 s10, 0x200000
	v_add_u32_e32 v39, v38, v40
	s_waitcnt vmcnt(0)
	s_nop 4
	v_add_f32_e32 v18, v80, v18
	v_mfma_f32_32x32x16_f16 v[2:17], v[42:45], v[46:49], v[2:17]
	v_mul_f32_e32 v37, v18, v18
	s_nop 10
	v_add_f32_e32 v2, v80, v2
	v_add_f32_e32 v36, v2, v18
	v_fmac_f32_e32 v37, v2, v2
	v_cvt_f16_f32_e32 v2, v2
	v_cvt_f16_f32_e32 v18, v18
	v_add_f32_e32 v36, 0, v36
	buffer_store_short v2, v39, s[8:11], 0 offen sc1
	v_add_u32_e32 v39, 0x2000, v40
	v_add_u32_e32 v2, v38, v39
	buffer_store_short v18, v2, s[8:11], 0 offen sc1
	v_add_f32_e32 v2, v80, v3
	v_add_f32_e32 v3, v80, v19
	v_mul_f32_e32 v19, v3, v3
	v_add_f32_e32 v18, v2, v3
	v_fmac_f32_e32 v19, v2, v2
	v_cvt_f16_f32_e32 v2, v2
	v_cvt_f16_f32_e32 v3, v3
	v_add_f32_e32 v18, v36, v18
	v_or_b32_e32 v36, 0x100, v38
	v_add_f32_e32 v19, v37, v19
	v_add_u32_e32 v37, v36, v40
	buffer_store_short v2, v37, s[8:11], 0 offen sc1
	v_add_u32_e32 v2, v36, v39
	buffer_store_short v3, v2, s[8:11], 0 offen sc1
	v_add_f32_e32 v2, v80, v4
	v_add_f32_e32 v3, v80, v20
	v_add_f32_e32 v4, v2, v3
	v_add_f32_e32 v4, v18, v4
	v_mul_f32_e32 v18, v3, v3
	v_fmac_f32_e32 v18, v2, v2
	v_cvt_f16_f32_e32 v2, v2
	v_cvt_f16_f32_e32 v3, v3
	v_add_f32_e32 v18, v19, v18
	v_or_b32_e32 v19, 0x200, v38
	v_add_u32_e32 v20, v19, v40
	buffer_store_short v2, v20, s[8:11], 0 offen sc1
	v_add_u32_e32 v2, v19, v39
	buffer_store_short v3, v2, s[8:11], 0 offen sc1
	v_add_f32_e32 v2, v80, v5
	v_add_f32_e32 v3, v80, v21
	v_add_f32_e32 v5, v2, v3
	v_add_f32_e32 v4, v4, v5
	v_mul_f32_e32 v5, v3, v3
	v_fmac_f32_e32 v5, v2, v2
	v_cvt_f16_f32_e32 v2, v2
	v_cvt_f16_f32_e32 v3, v3
	v_add_f32_e32 v5, v18, v5
	v_or_b32_e32 v18, 0x300, v38
	v_add_u32_e32 v19, v18, v40
	buffer_store_short v2, v19, s[8:11], 0 offen sc1
	v_add_u32_e32 v2, v18, v39
	buffer_store_short v3, v2, s[8:11], 0 offen sc1
	v_add_f32_e32 v2, v80, v6
	v_add_f32_e32 v3, v80, v22
	v_add_f32_e32 v6, v2, v3
	v_add_f32_e32 v4, v4, v6
	v_mul_f32_e32 v6, v3, v3
	v_fmac_f32_e32 v6, v2, v2
	v_cvt_f16_f32_e32 v2, v2
	v_cvt_f16_f32_e32 v3, v3
	v_add_f32_e32 v5, v5, v6
	v_or_b32_e32 v6, 0x800, v38
	v_add_u32_e32 v18, v6, v40
	buffer_store_short v2, v18, s[8:11], 0 offen sc1
	v_add_u32_e32 v2, v6, v39
	buffer_store_short v3, v2, s[8:11], 0 offen sc1
	v_add_f32_e32 v2, v80, v7
	v_add_f32_e32 v3, v80, v23
	v_add_f32_e32 v6, v2, v3
	v_add_f32_e32 v4, v4, v6
	v_mul_f32_e32 v6, v3, v3
	v_fmac_f32_e32 v6, v2, v2
	v_cvt_f16_f32_e32 v2, v2
	v_cvt_f16_f32_e32 v3, v3
	v_add_f32_e32 v5, v5, v6
	v_or_b32_e32 v6, 0x900, v38
	v_add_u32_e32 v7, v6, v40
	buffer_store_short v2, v7, s[8:11], 0 offen sc1
	v_add_u32_e32 v2, v6, v39
	buffer_store_short v3, v2, s[8:11], 0 offen sc1
	v_add_f32_e32 v2, v80, v8
	v_add_f32_e32 v3, v80, v24
	v_add_f32_e32 v6, v2, v3
	v_add_f32_e32 v4, v4, v6
	v_mul_f32_e32 v6, v3, v3
	v_fmac_f32_e32 v6, v2, v2
	v_cvt_f16_f32_e32 v2, v2
	v_cvt_f16_f32_e32 v3, v3
	v_add_f32_e32 v5, v5, v6
	v_or_b32_e32 v6, 0xa00, v38
	v_add_u32_e32 v7, v6, v40
	buffer_store_short v2, v7, s[8:11], 0 offen sc1
	v_add_u32_e32 v2, v6, v39
	buffer_store_short v3, v2, s[8:11], 0 offen sc1
	v_add_f32_e32 v2, v80, v9
	v_add_f32_e32 v3, v80, v25
	v_add_f32_e32 v6, v2, v3
	v_add_f32_e32 v4, v4, v6
	v_mul_f32_e32 v6, v3, v3
	v_fmac_f32_e32 v6, v2, v2
	v_cvt_f16_f32_e32 v2, v2
	v_cvt_f16_f32_e32 v3, v3
	v_add_f32_e32 v5, v5, v6
	v_or_b32_e32 v6, 0xb00, v38
	v_add_u32_e32 v7, v6, v40
	buffer_store_short v2, v7, s[8:11], 0 offen sc1
	v_add_u32_e32 v2, v6, v39
	buffer_store_short v3, v2, s[8:11], 0 offen sc1
	v_add_f32_e32 v2, v80, v10
	v_add_f32_e32 v3, v80, v26
	v_add_f32_e32 v6, v2, v3
	v_add_f32_e32 v4, v4, v6
	v_mul_f32_e32 v6, v3, v3
	v_fmac_f32_e32 v6, v2, v2
	v_cvt_f16_f32_e32 v2, v2
	v_cvt_f16_f32_e32 v3, v3
	v_add_f32_e32 v5, v5, v6
	v_or_b32_e32 v6, 0x1000, v38
	v_add_u32_e32 v7, v6, v40
	buffer_store_short v2, v7, s[8:11], 0 offen sc1
	v_add_u32_e32 v2, v6, v39
	buffer_store_short v3, v2, s[8:11], 0 offen sc1
	v_add_f32_e32 v2, v80, v11
	v_add_f32_e32 v3, v80, v27
	v_add_f32_e32 v6, v2, v3
	v_add_f32_e32 v4, v4, v6
	v_mul_f32_e32 v6, v3, v3
	v_fmac_f32_e32 v6, v2, v2
	v_cvt_f16_f32_e32 v2, v2
	v_cvt_f16_f32_e32 v3, v3
	v_add_f32_e32 v5, v5, v6
	v_or_b32_e32 v6, 0x1100, v38
	v_add_u32_e32 v7, v6, v40
	buffer_store_short v2, v7, s[8:11], 0 offen sc1
	v_add_u32_e32 v2, v6, v39
	buffer_store_short v3, v2, s[8:11], 0 offen sc1
	v_add_f32_e32 v2, v80, v12
	v_add_f32_e32 v3, v80, v28
	v_add_f32_e32 v6, v2, v3
	v_add_f32_e32 v4, v4, v6
	v_mul_f32_e32 v6, v3, v3
	v_fmac_f32_e32 v6, v2, v2
	v_cvt_f16_f32_e32 v2, v2
	v_cvt_f16_f32_e32 v3, v3
	v_add_f32_e32 v5, v5, v6
	v_or_b32_e32 v6, 0x1200, v38
	v_add_u32_e32 v7, v6, v40
	buffer_store_short v2, v7, s[8:11], 0 offen sc1
	v_add_u32_e32 v2, v6, v39
	buffer_store_short v3, v2, s[8:11], 0 offen sc1
	v_add_f32_e32 v2, v80, v13
	v_add_f32_e32 v3, v80, v29
	v_add_f32_e32 v6, v2, v3
	v_add_f32_e32 v4, v4, v6
	v_mul_f32_e32 v6, v3, v3
	v_fmac_f32_e32 v6, v2, v2
	v_cvt_f16_f32_e32 v2, v2
	v_cvt_f16_f32_e32 v3, v3
	v_add_f32_e32 v5, v5, v6
	v_or_b32_e32 v6, 0x1300, v38
	v_add_u32_e32 v7, v6, v40
	buffer_store_short v2, v7, s[8:11], 0 offen sc1
	v_add_u32_e32 v2, v6, v39
	buffer_store_short v3, v2, s[8:11], 0 offen sc1
	v_add_f32_e32 v2, v80, v14
	v_add_f32_e32 v3, v80, v30
	v_add_f32_e32 v6, v2, v3
	v_add_f32_e32 v4, v4, v6
	v_mul_f32_e32 v6, v3, v3
	v_fmac_f32_e32 v6, v2, v2
	v_cvt_f16_f32_e32 v2, v2
	v_cvt_f16_f32_e32 v3, v3
	v_add_f32_e32 v5, v5, v6
	v_or_b32_e32 v6, 0x1800, v38
	v_add_u32_e32 v7, v6, v40
	buffer_store_short v2, v7, s[8:11], 0 offen sc1
	v_add_u32_e32 v2, v6, v39
	buffer_store_short v3, v2, s[8:11], 0 offen sc1
	v_add_f32_e32 v2, v80, v15
	v_add_f32_e32 v3, v80, v31
	v_add_f32_e32 v6, v2, v3
	v_add_f32_e32 v4, v4, v6
	v_mul_f32_e32 v6, v3, v3
	v_fmac_f32_e32 v6, v2, v2
	v_cvt_f16_f32_e32 v2, v2
	v_cvt_f16_f32_e32 v3, v3
	v_add_f32_e32 v5, v5, v6
	v_or_b32_e32 v6, 0x1900, v38
	v_add_u32_e32 v7, v6, v40
	buffer_store_short v2, v7, s[8:11], 0 offen sc1
	v_add_u32_e32 v2, v6, v39
	buffer_store_short v3, v2, s[8:11], 0 offen sc1
	v_add_f32_e32 v2, v80, v16
	v_add_f32_e32 v3, v80, v32
	v_add_f32_e32 v6, v2, v3
	v_add_f32_e32 v4, v4, v6
	v_mul_f32_e32 v6, v3, v3
	v_fmac_f32_e32 v6, v2, v2
	v_cvt_f16_f32_e32 v2, v2
	v_cvt_f16_f32_e32 v3, v3
	v_add_f32_e32 v5, v5, v6
	v_or_b32_e32 v6, 0x1a00, v38
	v_add_u32_e32 v7, v6, v40
	buffer_store_short v2, v7, s[8:11], 0 offen sc1
	v_add_u32_e32 v2, v6, v39
	v_add_f32_e32 v6, v80, v17
	v_add_f32_e32 v7, v80, v33
	buffer_store_short v3, v2, s[8:11], 0 offen sc1
	v_add_f32_e32 v2, v6, v7
	v_mul_f32_e32 v3, v7, v7
	v_add_f32_e32 v2, v4, v2
	v_fmac_f32_e32 v3, v6, v6
	v_lshlrev_b32_e32 v4, 2, v70
	v_add_f32_e32 v3, v5, v3
	v_xor_b32_e32 v5, 0x80, v4
	v_cvt_f16_f32_e32 v6, v6
	ds_bpermute_b32 v4, v5, v2
	ds_bpermute_b32 v5, v5, v3
	v_cvt_f16_f32_e32 v7, v7
	v_or_b32_e32 v8, 0x1b00, v38
	v_add_u32_e32 v9, v8, v40
	buffer_store_short v6, v9, s[8:11], 0 offen sc1
	v_add_u32_e32 v6, v8, v39
	buffer_store_short v7, v6, s[8:11], 0 offen sc1
	s_and_saveexec_b64 s[8:9], vcc
	s_cbranch_execz .LBB3_9
	s_load_dwordx2 s[10:11], s[0:1], 0x98
	v_lshl_add_u32 v34, s16, 8, v34
	s_waitcnt lgkmcnt(0)
	v_add_f32_e32 v5, v3, v5
	v_add_f32_e32 v4, v2, v4
	v_lshl_add_u64 v[2:3], v[34:35], 2, s[10:11]
	global_atomic_add_f32 v[2:3], v4, off
	global_atomic_add_f32 v[2:3], v5, off offset:512

.LBB3_17:
	s_and_b64 vcc, exec, s[2:3]
	s_cbranch_vccz .LBB3_27
	v_mov_b32_e32 v240, 0x64646464
	s_mov_b32 s42, 0x4010400
	s_mov_b32 s43, 0x4030402
	s_load_dwordx2 s[8:9], s[0:1], 0x70
	s_load_dwordx4 s[4:7], s[0:1], 0x40
	s_load_dwordx4 s[20:23], s[0:1], 0x10
	s_load_dwordx4 s[28:31], s[0:1], 0x20
	s_load_dwordx4 s[32:35], s[0:1], 0x30
	s_load_dwordx2 s[36:37], s[0:1], 0x60
	v_mov_b32_e32 v3, 0
	v_lshlrev_b32_e32 v2, 2, v0
	s_movk_i32 s2, 0xfe00
	s_mov_b32 s3, -1
	s_waitcnt lgkmcnt(0)
	v_lshl_add_u64 v[6:7], s[22:23], 0, v[2:3]
	s_lshr_b32 s16, s15, 7
	s_movk_i32 s10, 0x80
	v_lshl_add_u64 v[6:7], v[6:7], 0, s[2:3]
	s_lshl_b32 s2, s12, 3
	v_cmp_gt_u32_e32 vcc, s10, v0
	s_or_b32 s10, s16, s2
	v_lshl_add_u64 v[4:5], s[20:21], 0, v[2:3]
	s_ashr_i32 s11, s10, 31
	v_cndmask_b32_e32 v6, v6, v4, vcc
	s_movk_i32 s17, 0x1000
	s_bfe_u32 s13, s15, 0x10006
	s_lshl_b64 s[2:3], s[10:11], 12
	v_and_b32_e32 v156, 63, v0
	v_cndmask_b32_e32 v7, v7, v5, vcc
	v_add_co_u32_e32 v20, vcc, s17, v6
	s_add_u32 s2, s8, s2
	s_nop 0
	v_addc_co_u32_e32 v21, vcc, 0, v7, vcc
	s_addc_u32 s3, s9, s3
	v_lshlrev_b32_e32 v1, 3, v156
	global_load_dword v17, v[6:7], off
	global_load_dword v16, v[6:7], off offset:512
	global_load_dword v13, v[6:7], off offset:1024
	global_load_dword v12, v[6:7], off offset:1536
	global_load_dword v9, v[6:7], off offset:2048
	global_load_dword v8, v[6:7], off offset:2560
	global_load_dword v5, v[6:7], off offset:3072
	global_load_dword v4, v[6:7], off offset:3584
	global_load_dword v19, v[20:21], off
	global_load_dword v18, v[20:21], off offset:512
	global_load_dword v15, v[20:21], off offset:1024
	global_load_dword v14, v[20:21], off offset:1536
	global_load_dword v11, v[20:21], off offset:2048
	global_load_dword v10, v[20:21], off offset:2560
	global_load_dword v7, v[20:21], off offset:3072
	global_load_dword v6, v[20:21], off offset:3584
	s_cmpk_lt_u32 s15, 0x80
	s_cselect_b32 s38, s28, s32
	s_cselect_b32 s39, s29, s33
	s_cselect_b32 s40, s30, s34
	s_cselect_b32 s41, s31, s35
	v_and_b32_e32 v24, 0x1fc, v2
	v_and_b32_e32 v28, 0xfc, v2
	v_lshl_or_b32 v28, s14, 8, v28
	global_load_dword v25, v24, s[38:39]
	global_load_dword v26, v24, s[40:41]
	global_load_dword v27, v28, s[36:37]
	global_load_dwordx2 v[154:155], v1, s[2:3]
	global_load_dwordx2 v[150:151], v1, s[2:3] offset:512
	global_load_dwordx2 v[146:147], v1, s[2:3] offset:1024
	global_load_dwordx2 v[142:143], v1, s[2:3] offset:1536
	global_load_dwordx2 v[152:153], v1, s[2:3] offset:2048
	global_load_dwordx2 v[148:149], v1, s[2:3] offset:2560
	global_load_dwordx2 v[144:145], v1, s[2:3] offset:3072
	global_load_dwordx2 v[140:141], v1, s[2:3] offset:3584
	s_lshl_b32 s2, s14, 10
	s_lshl_b32 s3, s13, 9
	s_or_b32 s2, s3, s2
	v_or_b32_e32 v1, s2, v156
	v_lshlrev_b32_e32 v20, 4, v1
	v_mov_b32_e32 v21, v3
	v_lshl_add_u64 v[22:23], s[4:5], 0, v[20:21]
	v_add_co_u32_e32 v22, vcc, s17, v22
	s_movk_i32 s2, 0x7f
	s_nop 0
	v_addc_co_u32_e32 v23, vcc, 0, v23, vcc
	global_load_dwordx4 v[86:89], v[22:23], off
	global_load_dwordx4 v[78:81], v[22:23], off offset:1024
	global_load_dwordx4 v[70:73], v[22:23], off offset:2048
	global_load_dwordx4 v[66:69], v[22:23], off offset:3072
	global_load_dwordx4 v[122:125], v20, s[4:5]
	global_load_dwordx4 v[126:129], v20, s[6:7]
	global_load_dwordx4 v[114:117], v20, s[4:5] offset:1024
	global_load_dwordx4 v[118:121], v20, s[6:7] offset:1024
	global_load_dwordx4 v[106:109], v20, s[4:5] offset:2048
	global_load_dwordx4 v[110:113], v20, s[6:7] offset:2048
	global_load_dwordx4 v[98:101], v20, s[4:5] offset:3072
	global_load_dwordx4 v[102:105], v20, s[6:7] offset:3072
	v_lshl_add_u64 v[22:23], s[6:7], 0, v[20:21]
	v_add_co_u32_e32 v20, vcc, 0x1000, v22
	s_nop 1
	v_addc_co_u32_e32 v21, vcc, 0, v23, vcc
	global_load_dwordx4 v[94:97], v[20:21], off
	global_load_dwordx4 v[90:93], v[20:21], off offset:1024
	global_load_dwordx4 v[82:85], v[20:21], off offset:2048
	global_load_dwordx4 v[74:77], v[20:21], off offset:3072
	v_cmp_lt_u32_e32 vcc, s2, v0
	v_cmp_gt_u32_e64 s[2:3], 64, v0
	s_and_saveexec_b64 s[4:5], s[2:3]
	s_cbranch_execz .LBB3_20
	v_add_u32_e32 v20, 0x1ee00, v2
	s_waitcnt vmcnt(24)
	ds_write_b32 v20, v27

.LBB3_24:
	s_or_b64 exec, exec, s[2:3]
	v_and_b32_e32 v1, 31, v0
	v_lshlrev_b32_e32 v2, 2, v1
	v_lshl_or_b32 v2, s13, 7, v2
	v_or_b32_e32 v2, 0x1ee00, v2
	v_lshrrev_b32_e32 v158, 5, v156
	s_waitcnt lgkmcnt(0)
	s_barrier
	s_barrier
	ds_read_b32 v157, v2
	v_mul_u32_u24_e32 v2, 0x88, v1
	s_mul_i32 s0, s16, 0x4400
	v_lshlrev_b32_e32 v2, 1, v2
	v_lshlrev_b32_e32 v3, 4, v158
	v_mov_b32_e32 v138, v0
	v_add3_u32 v159, s0, v2, v3
	ds_read_b128 v[2:5], v159
	ds_read_b128 v[18:21], v159 offset:8704
	ds_read_b128 v[130:133], v159 offset:32
	s_waitcnt vmcnt(10) lgkmcnt(2)
	v_mfma_f32_32x32x16_f16 v[50:65], v[2:5], v[126:129], 0
	s_mov_b32 s2, 0xc060c00
	s_mov_b32 s3, 0xe400
	s_mulk_i32 s16, 0x2400
	s_lshl_b32 s0, s13, 6
	s_or_b32 s0, s16, s0
	s_add_i32 s0, s0, 0x11000
	v_lshl_or_b32 v1, v1, 1, s0
	s_waitcnt lgkmcnt(1)
	v_mfma_f32_32x32x16_f16 v[34:49], v[18:21], v[126:129], 0
	s_or_b32 s0, s10, 2
	s_ashr_i32 s1, s0, 31
	s_lshl_b64 s[0:1], s[0:1], 12
	s_add_u32 s0, s8, s0
	s_addc_u32 s1, s9, s1
	v_cmp_gt_u32_e32 vcc, 32, v156
	v_mfma_f32_32x32x16_f16 v[2:17], v[2:5], v[122:125], 0
	v_mfma_f32_32x32x16_f16 v[18:33], v[18:21], v[122:125], 0
	ds_read_b128 v[134:137], v159 offset:8736
	ds_read_b128 v[160:163], v159 offset:64
	s_waitcnt vmcnt(8) lgkmcnt(2)
	v_mfma_f32_32x32x16_f16 v[50:65], v[130:133], v[118:121], v[50:65]
	s_waitcnt lgkmcnt(1)
	v_mfma_f32_32x32x16_f16 v[34:49], v[134:137], v[118:121], v[34:49]
	v_mfma_f32_32x32x16_f16 v[2:17], v[130:133], v[114:117], v[2:17]
	v_mfma_f32_32x32x16_f16 v[18:33], v[134:137], v[114:117], v[18:33]
	ds_read_b128 v[130:133], v159 offset:8768
	ds_read_b128 v[134:137], v159 offset:96
	s_waitcnt vmcnt(6) lgkmcnt(2)
	v_mfma_f32_32x32x16_f16 v[50:65], v[160:163], v[110:113], v[50:65]
	s_waitcnt lgkmcnt(1)
	v_mfma_f32_32x32x16_f16 v[34:49], v[130:133], v[110:113], v[34:49]
	v_mfma_f32_32x32x16_f16 v[2:17], v[160:163], v[106:109], v[2:17]
	v_mfma_f32_32x32x16_f16 v[18:33], v[130:133], v[106:109], v[18:33]
	ds_read_b128 v[130:133], v159 offset:8800
	ds_read_b128 v[160:163], v159 offset:128
	s_waitcnt vmcnt(4) lgkmcnt(2)
	v_mfma_f32_32x32x16_f16 v[50:65], v[134:137], v[102:105], v[50:65]
	s_waitcnt lgkmcnt(1)
	v_mfma_f32_32x32x16_f16 v[34:49], v[130:133], v[102:105], v[34:49]
	v_mfma_f32_32x32x16_f16 v[2:17], v[134:137], v[98:101], v[2:17]
	v_mfma_f32_32x32x16_f16 v[18:33], v[130:133], v[98:101], v[18:33]
	ds_read_b128 v[130:133], v159 offset:8832
	ds_read_b128 v[134:137], v159 offset:160
	s_waitcnt vmcnt(3) lgkmcnt(2)
	v_mfma_f32_32x32x16_f16 v[50:65], v[160:163], v[94:97], v[50:65]
	s_waitcnt lgkmcnt(1)
	v_mfma_f32_32x32x16_f16 v[34:49], v[130:133], v[94:97], v[34:49]
	v_mfma_f32_32x32x16_f16 v[2:17], v[160:163], v[86:89], v[2:17]
	v_mfma_f32_32x32x16_f16 v[18:33], v[130:133], v[86:89], v[18:33]
	ds_read_b128 v[130:133], v159 offset:8864
	ds_read_b128 v[160:163], v159 offset:192
	s_waitcnt vmcnt(2) lgkmcnt(2)
	v_mfma_f32_32x32x16_f16 v[50:65], v[134:137], v[90:93], v[50:65]
	s_waitcnt lgkmcnt(1)
	v_mfma_f32_32x32x16_f16 v[34:49], v[130:133], v[90:93], v[34:49]
	v_mfma_f32_32x32x16_f16 v[2:17], v[134:137], v[78:81], v[2:17]
	v_mfma_f32_32x32x16_f16 v[18:33], v[130:133], v[78:81], v[18:33]
	ds_read_b128 v[130:133], v159 offset:8896
	ds_read_b128 v[164:167], v159 offset:224
	s_waitcnt vmcnt(1) lgkmcnt(2)
	v_mfma_f32_32x32x16_f16 v[50:65], v[160:163], v[82:85], v[50:65]
	s_waitcnt lgkmcnt(1)
	v_mfma_f32_32x32x16_f16 v[34:49], v[130:133], v[82:85], v[34:49]
	v_mfma_f32_32x32x16_f16 v[2:17], v[160:163], v[70:73], v[2:17]
	v_mfma_f32_32x32x16_f16 v[18:33], v[130:133], v[70:73], v[18:33]
	v_lshlrev_b32_e32 v130, 3, v138
	v_and_b32_e32 v168, 0x1f8, v130
	global_load_dwordx2 v[138:139], v168, s[0:1]
	global_load_dwordx2 v[134:135], v168, s[0:1] offset:512
	global_load_dwordx2 v[132:133], v168, s[0:1] offset:1024
	global_load_dwordx2 v[130:131], v168, s[0:1] offset:1536
	global_load_dwordx2 v[136:137], v168, s[0:1] offset:2048
	s_waitcnt vmcnt(5) lgkmcnt(0)
	v_mfma_f32_32x32x16_f16 v[50:65], v[164:167], v[74:77], v[50:65]
	v_mfma_f32_32x32x16_f16 v[2:17], v[164:167], v[66:69], v[2:17]
	s_nop 10
	v_cvt_pk_f16_f32 v57, v56, v57
	v_cvt_pk_f16_f32 v56, v54, v55
	v_cvt_pk_f16_f32 v55, v52, v53
	v_cvt_pk_f16_f32 v54, v50, v51
	v_perm_b32 v50, v240, v154, s42
	v_perm_b32 v51, v240, v154, s43
	v_perm_b32 v52, v240, v155, s42
	v_perm_b32 v53, v240, v155, s43
	v_pk_add_f16 v50, v50, s3 op_sel_hi:[1,0]
	v_pk_add_f16 v51, v51, s3 op_sel_hi:[1,0]
	v_pk_add_f16 v52, v52, s3 op_sel_hi:[1,0]
	v_pk_add_f16 v53, v53, s3 op_sel_hi:[1,0]
	v_cvt_pk_f16_f32 v65, v64, v65
	v_cvt_pk_f16_f32 v64, v62, v63
	v_cvt_pk_f16_f32 v63, v60, v61
	v_cvt_pk_f16_f32 v62, v58, v59
	v_mfma_f32_32x32x16_f16 v[2:17], v[50:53], v[54:57], v[2:17]
	v_perm_b32 v58, v240, v150, s42
	v_perm_b32 v59, v240, v150, s43
	v_perm_b32 v60, v240, v151, s42
	v_perm_b32 v61, v240, v151, s43
	v_pk_add_f16 v58, v58, s3 op_sel_hi:[1,0]
	v_pk_add_f16 v59, v59, s3 op_sel_hi:[1,0]
	v_pk_add_f16 v60, v60, s3 op_sel_hi:[1,0]
	v_pk_add_f16 v61, v61, s3 op_sel_hi:[1,0]
	s_nop 1
	v_mfma_f32_32x32x16_f16 v[2:17], v[58:61], v[62:65], v[2:17]
	ds_read_b128 v[160:163], v159 offset:8928
	v_perm_b32 v155, v240, v152, s43
	v_perm_b32 v164, v240, v153, s42
	s_waitcnt lgkmcnt(0)
	v_mfma_f32_32x32x16_f16 v[18:33], v[160:163], v[66:69], v[18:33]
	v_perm_b32 v154, v240, v152, s42
	v_perm_b32 v165, v240, v153, s43
	v_pk_add_f16 v152, v154, s3 op_sel_hi:[1,0]
	v_pk_add_f16 v153, v155, s3 op_sel_hi:[1,0]
	v_pk_add_f16 v154, v164, s3 op_sel_hi:[1,0]
	v_pk_add_f16 v155, v165, s3 op_sel_hi:[1,0]
	v_mfma_f32_32x32x16_f16 v[34:49], v[160:163], v[74:77], v[34:49]
	v_perm_b32 v151, v240, v148, s43
	v_perm_b32 v164, v240, v149, s42
	v_mfma_f32_32x32x16_f16 v[18:33], v[152:155], v[54:57], v[18:33]
	v_perm_b32 v150, v240, v148, s42
	v_perm_b32 v165, v240, v149, s43
	v_pk_add_f16 v148, v150, s3 op_sel_hi:[1,0]
	v_pk_add_f16 v149, v151, s3 op_sel_hi:[1,0]
	v_pk_add_f16 v150, v164, s3 op_sel_hi:[1,0]
	v_pk_add_f16 v151, v165, s3 op_sel_hi:[1,0]
	s_nop 2
	v_cvt_pk_f16_f32 v41, v40, v41
	v_cvt_pk_f16_f32 v40, v38, v39
	v_cvt_pk_f16_f32 v38, v34, v35
	v_cvt_pk_f16_f32 v39, v36, v37
	v_mfma_f32_32x32x16_f16 v[18:33], v[148:151], v[62:65], v[18:33]
	v_perm_b32 v34, v240, v146, s42
	v_perm_b32 v35, v240, v146, s43
	v_perm_b32 v36, v240, v147, s42
	v_perm_b32 v37, v240, v147, s43
	v_pk_add_f16 v34, v34, s3 op_sel_hi:[1,0]
	v_pk_add_f16 v35, v35, s3 op_sel_hi:[1,0]
	v_pk_add_f16 v36, v36, s3 op_sel_hi:[1,0]
	v_pk_add_f16 v37, v37, s3 op_sel_hi:[1,0]
	v_perm_b32 v146, v240, v144, s42
	v_perm_b32 v144, v240, v144, s43
	v_perm_b32 v147, v240, v145, s42
	v_perm_b32 v53, v240, v145, s43
	v_pk_add_f16 v50, v146, s3 op_sel_hi:[1,0]
	v_pk_add_f16 v51, v144, s3 op_sel_hi:[1,0]
	v_pk_add_f16 v52, v147, s3 op_sel_hi:[1,0]
	v_pk_add_f16 v53, v53, s3 op_sel_hi:[1,0]
	v_cvt_pk_f16_f32 v49, v48, v49
	v_cvt_pk_f16_f32 v48, v46, v47
	v_cvt_pk_f16_f32 v47, v44, v45
	v_mfma_f32_32x32x16_f16 v[2:17], v[34:37], v[38:41], v[2:17]
	v_cvt_pk_f16_f32 v46, v42, v43
	v_lshlrev_b32_e32 v54, 8, v140
	v_mfma_f32_32x32x16_f16 v[18:33], v[50:53], v[38:41], v[18:33]
	v_lshrrev_b32_e32 v37, 16, v141
	v_lshrrev_b32_e32 v38, 8, v141
	v_perm_b32 v34, v54, v140, s2
	v_perm_b32 v37, v38, v37, s2
	v_or_b32_e32 v34, 0x64006400, v34
	v_perm_b32 v35, v240, v140, s43
	v_perm_b32 v36, v240, v141, s42
	v_or_b32_e32 v37, 0x64006400, v37
	v_perm_b32 v42, v240, v142, s42
	v_perm_b32 v43, v240, v142, s43
	v_perm_b32 v44, v240, v143, s42
	v_perm_b32 v45, v240, v143, s43
	v_pk_add_f16 v34, v34, s3 op_sel_hi:[1,0]
	v_pk_add_f16 v35, v35, s3 op_sel_hi:[1,0]
	v_pk_add_f16 v36, v36, s3 op_sel_hi:[1,0]
	v_pk_add_f16 v37, v37, s3 op_sel_hi:[1,0]
	v_pk_add_f16 v42, v42, s3 op_sel_hi:[1,0]
	v_pk_add_f16 v43, v43, s3 op_sel_hi:[1,0]
	v_pk_add_f16 v44, v44, s3 op_sel_hi:[1,0]
	v_pk_add_f16 v45, v45, s3 op_sel_hi:[1,0]
	v_mfma_f32_32x32x16_f16 v[18:33], v[34:37], v[46:49], v[18:33]
	global_load_dwordx2 v[154:155], v168, s[0:1] offset:2560
	global_load_dwordx2 v[152:153], v168, s[0:1] offset:3072
	global_load_dwordx2 v[150:151], v168, s[0:1] offset:3584
	v_mov_b32_e32 v148, v0
	s_or_b32 s0, s10, 4
	s_ashr_i32 s1, s0, 31
	s_lshl_b64 s[0:1], s[0:1], 12
	v_mfma_f32_32x32x16_f16 v[2:17], v[42:45], v[46:49], v[2:17]
	s_nop 3
	v_add_f32_e32 v196, v157, v18
	v_mul_u32_u24_e32 v18, 0x120, v158
	v_lshl_add_u32 v158, v18, 1, v1
	v_cvt_f16_f32_e32 v1, v196
	v_add_f32_e32 v204, v157, v20
	v_add_f32_e32 v160, v157, v21
	v_add_f32_e32 v162, v157, v22
	s_nop 0
	v_add_f32_e32 v193, v157, v2
	v_add_f32_e32 v198, v157, v3
	v_cvt_f16_f32_e32 v2, v193
	v_cvt_f16_f32_e32 v3, v198
	ds_write_b16 v158, v1 offset:4608
	v_add_f32_e32 v203, v157, v4
	v_add_f32_e32 v1, v157, v5
	ds_write_b16 v158, v2
	ds_write_b16 v158, v3 offset:144
	v_cvt_f16_f32_e32 v2, v203
	v_cvt_f16_f32_e32 v3, v204
	v_cvt_f16_f32_e32 v4, v1
	v_cvt_f16_f32_e32 v5, v160
	v_add_f32_e32 v161, v157, v6
	v_add_f32_e32 v163, v157, v7
	v_add_f32_e32 v164, v157, v23
	ds_write_b16 v158, v2 offset:288
	ds_write_b16 v158, v3 offset:4896
	ds_write_b16 v158, v4 offset:432
	ds_write_b16 v158, v5 offset:5040
	v_cvt_f16_f32_e32 v2, v161
	v_cvt_f16_f32_e32 v3, v162
	v_cvt_f16_f32_e32 v4, v163
	v_cvt_f16_f32_e32 v5, v164
	v_add_f32_e32 v165, v157, v8
	v_add_f32_e32 v166, v157, v24
	v_add_f32_e32 v167, v157, v9
	v_add_f32_e32 v168, v157, v25
	ds_write_b16 v158, v2 offset:1152
	ds_write_b16 v158, v3 offset:5760
	ds_write_b16 v158, v4 offset:1296
	ds_write_b16 v158, v5 offset:5904
	v_cvt_f16_f32_e32 v2, v165
	v_cvt_f16_f32_e32 v3, v166
	v_cvt_f16_f32_e32 v4, v167
	v_cvt_f16_f32_e32 v5, v168
	v_add_f32_e32 v169, v157, v10
	v_add_f32_e32 v170, v157, v26
	v_add_f32_e32 v171, v157, v11
	v_add_f32_e32 v172, v157, v27
	ds_write_b16 v158, v2 offset:1440
	ds_write_b16 v158, v3 offset:6048
	ds_write_b16 v158, v4 offset:1584
	ds_write_b16 v158, v5 offset:6192
	v_cvt_f16_f32_e32 v2, v169
	v_cvt_f16_f32_e32 v3, v170
	v_cvt_f16_f32_e32 v4, v171
	v_cvt_f16_f32_e32 v5, v172
	v_add_f32_e32 v173, v157, v12
	v_add_f32_e32 v174, v157, v28
	v_add_f32_e32 v175, v157, v13
	v_add_f32_e32 v176, v157, v29
	ds_write_b16 v158, v2 offset:2304
	ds_write_b16 v158, v3 offset:6912
	ds_write_b16 v158, v4 offset:2448
	ds_write_b16 v158, v5 offset:7056
	v_cvt_f16_f32_e32 v2, v173
	v_cvt_f16_f32_e32 v3, v174
	v_cvt_f16_f32_e32 v4, v175
	v_cvt_f16_f32_e32 v5, v176
	v_add_f32_e32 v177, v157, v14
	v_add_f32_e32 v178, v157, v30
	v_add_f32_e32 v179, v157, v15
	v_add_f32_e32 v180, v157, v31
	ds_write_b16 v158, v2 offset:2592
	ds_write_b16 v158, v3 offset:7200
	ds_write_b16 v158, v4 offset:2736
	ds_write_b16 v158, v5 offset:7344
	v_cvt_f16_f32_e32 v2, v177
	v_cvt_f16_f32_e32 v3, v178
	v_cvt_f16_f32_e32 v4, v179
	v_cvt_f16_f32_e32 v5, v180
	v_add_f32_e32 v200, v157, v19
	v_add_f32_e32 v181, v157, v16
	v_add_f32_e32 v183, v157, v32
	v_add_f32_e32 v182, v157, v17
	v_add_f32_e32 v184, v157, v33
	v_cvt_f16_f32_e32 v18, v200
	ds_write_b16 v158, v2 offset:3456
	ds_write_b16 v158, v3 offset:8064
	ds_write_b16 v158, v4 offset:3600
	ds_write_b16 v158, v5 offset:8208
	v_cvt_f16_f32_e32 v2, v181
	v_cvt_f16_f32_e32 v3, v183
	v_cvt_f16_f32_e32 v4, v182
	v_cvt_f16_f32_e32 v5, v184
	ds_write_b16 v158, v18 offset:4752
	ds_write_b16 v158, v2 offset:3744
	ds_write_b16 v158, v3 offset:8352
	ds_write_b16 v158, v4 offset:3888
	ds_write_b16 v158, v5 offset:8496
	s_waitcnt lgkmcnt(0)
	s_barrier
	ds_read_b128 v[2:5], v159 offset:34816
	ds_read_b128 v[18:21], v159 offset:43520
	s_waitcnt lgkmcnt(1)
	v_mfma_f32_32x32x16_f16 v[50:65], v[2:5], v[126:129], 0
	s_add_u32 s0, s8, s0
	s_addc_u32 s1, s9, s1
	s_waitcnt lgkmcnt(0)
	v_mfma_f32_32x32x16_f16 v[34:49], v[18:21], v[126:129], 0
	v_mfma_f32_32x32x16_f16 v[2:17], v[2:5], v[122:125], 0
	v_mfma_f32_32x32x16_f16 v[18:33], v[18:21], v[122:125], 0
	ds_read_b128 v[140:143], v159 offset:34848
	ds_read_b128 v[144:147], v159 offset:43552
	s_waitcnt lgkmcnt(1)
	v_mfma_f32_32x32x16_f16 v[50:65], v[140:143], v[118:121], v[50:65]
	s_waitcnt lgkmcnt(0)
	v_mfma_f32_32x32x16_f16 v[34:49], v[144:147], v[118:121], v[34:49]
	v_mfma_f32_32x32x16_f16 v[2:17], v[140:143], v[114:117], v[2:17]
	v_mfma_f32_32x32x16_f16 v[18:33], v[144:147], v[114:117], v[18:33]
	ds_read_b128 v[140:143], v159 offset:34880
	ds_read_b128 v[144:147], v159 offset:43584
	s_waitcnt lgkmcnt(1)
	v_mfma_f32_32x32x16_f16 v[50:65], v[140:143], v[110:113], v[50:65]
	s_waitcnt lgkmcnt(0)
	v_mfma_f32_32x32x16_f16 v[34:49], v[144:147], v[110:113], v[34:49]
	v_mfma_f32_32x32x16_f16 v[2:17], v[140:143], v[106:109], v[2:17]
	v_mfma_f32_32x32x16_f16 v[18:33], v[144:147], v[106:109], v[18:33]
	ds_read_b128 v[140:143], v159 offset:34912
	ds_read_b128 v[144:147], v159 offset:43616
	s_waitcnt lgkmcnt(1)
	v_mfma_f32_32x32x16_f16 v[50:65], v[140:143], v[102:105], v[50:65]
	s_waitcnt lgkmcnt(0)
	v_mfma_f32_32x32x16_f16 v[34:49], v[144:147], v[102:105], v[34:49]
	v_mfma_f32_32x32x16_f16 v[2:17], v[140:143], v[98:101], v[2:17]
	v_mfma_f32_32x32x16_f16 v[18:33], v[144:147], v[98:101], v[18:33]
	ds_read_b128 v[140:143], v159 offset:34944
	ds_read_b128 v[144:147], v159 offset:43648
	s_waitcnt lgkmcnt(1)
	v_mfma_f32_32x32x16_f16 v[50:65], v[140:143], v[94:97], v[50:65]
	s_waitcnt lgkmcnt(0)
	v_mfma_f32_32x32x16_f16 v[34:49], v[144:147], v[94:97], v[34:49]
	v_mfma_f32_32x32x16_f16 v[2:17], v[140:143], v[86:89], v[2:17]
	v_mfma_f32_32x32x16_f16 v[18:33], v[144:147], v[86:89], v[18:33]
	ds_read_b128 v[186:189], v159 offset:34976
	ds_read_b128 v[206:209], v159 offset:43680
	ds_read_b128 v[140:143], v159 offset:35008
	ds_read_b128 v[144:147], v159 offset:43712
	s_waitcnt lgkmcnt(3)
	v_mfma_f32_32x32x16_f16 v[50:65], v[186:189], v[90:93], v[50:65]
	s_waitcnt lgkmcnt(2)
	v_mfma_f32_32x32x16_f16 v[34:49], v[206:209], v[90:93], v[34:49]
	v_mfma_f32_32x32x16_f16 v[2:17], v[186:189], v[78:81], v[2:17]
	v_mfma_f32_32x32x16_f16 v[18:33], v[206:209], v[78:81], v[18:33]
	ds_read_b128 v[186:189], v159 offset:35040
	ds_read_b128 v[206:209], v159 offset:43744
	s_waitcnt lgkmcnt(3)
	v_mfma_f32_32x32x16_f16 v[50:65], v[140:143], v[82:85], v[50:65]
	s_waitcnt lgkmcnt(2)
	v_mfma_f32_32x32x16_f16 v[34:49], v[144:147], v[82:85], v[34:49]
	v_mfma_f32_32x32x16_f16 v[2:17], v[140:143], v[70:73], v[2:17]
	v_lshlrev_b32_e32 v140, 3, v148
	v_and_b32_e32 v185, 0x1f8, v140
	global_load_dwordx2 v[148:149], v185, s[0:1]
	global_load_dwordx2 v[142:143], v185, s[0:1] offset:1024
	global_load_dwordx2 v[140:141], v185, s[0:1] offset:1536
	v_mfma_f32_32x32x16_f16 v[18:33], v[144:147], v[70:73], v[18:33]
	global_load_dwordx2 v[144:145], v185, s[0:1] offset:512
	global_load_dwordx2 v[146:147], v185, s[0:1] offset:2048
	s_waitcnt lgkmcnt(1)
	v_mfma_f32_32x32x16_f16 v[50:65], v[186:189], v[74:77], v[50:65]
	v_mfma_f32_32x32x16_f16 v[2:17], v[186:189], v[66:69], v[2:17]
	s_nop 10
	v_cvt_pk_f16_f32 v57, v56, v57
	v_cvt_pk_f16_f32 v56, v54, v55
	v_cvt_pk_f16_f32 v54, v50, v51
	s_waitcnt vmcnt(12)
	v_cvt_pk_f16_f32 v55, v52, v53
	s_waitcnt vmcnt(8)
	v_perm_b32 v50, v240, v138, s42
	v_perm_b32 v51, v240, v138, s43
	v_perm_b32 v52, v240, v139, s42
	v_perm_b32 v53, v240, v139, s43
	v_perm_b32 v139, v240, v136, s43
	v_pk_add_f16 v50, v50, s3 op_sel_hi:[1,0]
	v_pk_add_f16 v51, v51, s3 op_sel_hi:[1,0]
	v_pk_add_f16 v52, v52, s3 op_sel_hi:[1,0]
	v_pk_add_f16 v53, v53, s3 op_sel_hi:[1,0]
	v_perm_b32 v190, v240, v137, s42
	s_waitcnt lgkmcnt(0)
	v_mfma_f32_32x32x16_f16 v[18:33], v[206:209], v[66:69], v[18:33]
	v_perm_b32 v138, v240, v136, s42
	v_perm_b32 v191, v240, v137, s43
	v_pk_add_f16 v136, v138, s3 op_sel_hi:[1,0]
	v_pk_add_f16 v137, v139, s3 op_sel_hi:[1,0]
	v_pk_add_f16 v138, v190, s3 op_sel_hi:[1,0]
	v_pk_add_f16 v139, v191, s3 op_sel_hi:[1,0]
	v_cvt_pk_f16_f32 v65, v64, v65
	v_cvt_pk_f16_f32 v64, v62, v63
	v_cvt_pk_f16_f32 v63, v60, v61
	v_cvt_pk_f16_f32 v62, v58, v59
	v_mfma_f32_32x32x16_f16 v[34:49], v[206:209], v[74:77], v[34:49]
	v_mfma_f32_32x32x16_f16 v[2:17], v[50:53], v[54:57], v[2:17]
	s_waitcnt vmcnt(7)
	v_perm_b32 v58, v240, v134, s42
	v_perm_b32 v59, v240, v134, s43
	v_perm_b32 v60, v240, v135, s42
	v_perm_b32 v61, v240, v135, s43
	v_pk_add_f16 v58, v58, s3 op_sel_hi:[1,0]
	v_pk_add_f16 v59, v59, s3 op_sel_hi:[1,0]
	v_pk_add_f16 v60, v60, s3 op_sel_hi:[1,0]
	v_pk_add_f16 v61, v61, s3 op_sel_hi:[1,0]
	v_mfma_f32_32x32x16_f16 v[18:33], v[136:139], v[54:57], v[18:33]
	v_perm_b32 v134, v240, v154, s42
	v_perm_b32 v135, v240, v154, s43
	v_perm_b32 v154, v240, v155, s42
	v_perm_b32 v155, v240, v155, s43
	v_pk_add_f16 v210, v134, s3 op_sel_hi:[1,0]
	v_pk_add_f16 v211, v135, s3 op_sel_hi:[1,0]
	v_pk_add_f16 v212, v154, s3 op_sel_hi:[1,0]
	v_pk_add_f16 v213, v155, s3 op_sel_hi:[1,0]
	v_cvt_pk_f16_f32 v41, v40, v41
	v_cvt_pk_f16_f32 v40, v38, v39
	v_cvt_pk_f16_f32 v39, v36, v37
	v_cvt_pk_f16_f32 v38, v34, v35
	v_mfma_f32_32x32x16_f16 v[2:17], v[58:61], v[62:65], v[2:17]
	v_perm_b32 v34, v240, v132, s42
	v_perm_b32 v35, v240, v132, s43
	v_perm_b32 v36, v240, v133, s42
	v_perm_b32 v37, v240, v133, s43
	v_pk_add_f16 v34, v34, s3 op_sel_hi:[1,0]
	v_pk_add_f16 v35, v35, s3 op_sel_hi:[1,0]
	v_pk_add_f16 v36, v36, s3 op_sel_hi:[1,0]
	v_pk_add_f16 v37, v37, s3 op_sel_hi:[1,0]
	s_waitcnt vmcnt(6)
	v_mfma_f32_32x32x16_f16 v[18:33], v[210:213], v[62:65], v[18:33]
	v_perm_b32 v132, v240, v152, s42
	v_perm_b32 v133, v240, v152, s43
	v_perm_b32 v134, v240, v153, s42
	v_perm_b32 v53, v240, v153, s43
	v_pk_add_f16 v50, v132, s3 op_sel_hi:[1,0]
	v_pk_add_f16 v51, v133, s3 op_sel_hi:[1,0]
	v_pk_add_f16 v52, v134, s3 op_sel_hi:[1,0]
	v_pk_add_f16 v53, v53, s3 op_sel_hi:[1,0]
	v_cvt_pk_f16_f32 v49, v48, v49
	v_cvt_pk_f16_f32 v48, v46, v47
	v_cvt_pk_f16_f32 v47, v44, v45
	v_cvt_pk_f16_f32 v46, v42, v43
	v_mfma_f32_32x32x16_f16 v[2:17], v[34:37], v[38:41], v[2:17]
	v_perm_b32 v42, v240, v130, s42
	v_perm_b32 v43, v240, v130, s43
	v_perm_b32 v44, v240, v131, s42
	v_perm_b32 v45, v240, v131, s43
	v_pk_add_f16 v42, v42, s3 op_sel_hi:[1,0]
	v_pk_add_f16 v43, v43, s3 op_sel_hi:[1,0]
	v_pk_add_f16 v44, v44, s3 op_sel_hi:[1,0]
	v_pk_add_f16 v45, v45, s3 op_sel_hi:[1,0]
	s_waitcnt vmcnt(5)
	v_lshlrev_b32_e32 v54, 8, v150
	v_mfma_f32_32x32x16_f16 v[18:33], v[50:53], v[38:41], v[18:33]
	v_lshrrev_b32_e32 v37, 16, v151
	v_lshrrev_b32_e32 v38, 8, v151
	v_perm_b32 v34, v54, v150, s2
	v_perm_b32 v37, v38, v37, s2
	v_or_b32_e32 v34, 0x64006400, v34
	v_perm_b32 v35, v240, v150, s43
	v_perm_b32 v36, v240, v151, s42
	v_or_b32_e32 v37, 0x64006400, v37
	v_pk_add_f16 v34, v34, s3 op_sel_hi:[1,0]
	v_pk_add_f16 v35, v35, s3 op_sel_hi:[1,0]
	v_pk_add_f16 v36, v36, s3 op_sel_hi:[1,0]
	v_pk_add_f16 v37, v37, s3 op_sel_hi:[1,0]
	v_mfma_f32_32x32x16_f16 v[2:17], v[42:45], v[46:49], v[2:17]
	global_load_dwordx2 v[154:155], v185, s[0:1] offset:2560
	global_load_dwordx2 v[152:153], v185, s[0:1] offset:3072
	global_load_dwordx2 v[150:151], v185, s[0:1] offset:3584
	s_or_b32 s0, s10, 6
	s_ashr_i32 s1, s0, 31
	s_lshl_b64 s[0:1], s[0:1], 12
	s_add_u32 s0, s8, s0
	v_mfma_f32_32x32x16_f16 v[18:33], v[34:37], v[46:49], v[18:33]
	s_nop 3
	v_add_f32_e32 v185, v157, v2
	v_add_f32_e32 v187, v157, v3
	v_cvt_f16_f32_e32 v2, v185
	v_cvt_f16_f32_e32 v3, v187
	v_add_f32_e32 v189, v157, v4
	v_add_f32_e32 v191, v157, v5
	ds_write_b16 v158, v2 offset:18432
	s_nop 0
	v_add_f32_e32 v190, v157, v20
	v_add_f32_e32 v192, v157, v21
	ds_write_b16 v158, v3 offset:18576
	v_cvt_f16_f32_e32 v2, v189
	v_cvt_f16_f32_e32 v3, v190
	v_cvt_f16_f32_e32 v4, v191
	v_cvt_f16_f32_e32 v5, v192
	v_add_f32_e32 v194, v157, v6
	v_add_f32_e32 v195, v157, v22
	v_add_f32_e32 v197, v157, v7
	v_add_f32_e32 v199, v157, v23
	ds_write_b16 v158, v2 offset:18720
	ds_write_b16 v158, v3 offset:23328
	ds_write_b16 v158, v4 offset:18864
	ds_write_b16 v158, v5 offset:23472
	v_cvt_f16_f32_e32 v2, v194
	v_cvt_f16_f32_e32 v3, v195
	v_cvt_f16_f32_e32 v4, v197
	v_cvt_f16_f32_e32 v5, v199
	v_add_f32_e32 v201, v157, v8
	v_add_f32_e32 v202, v157, v24
	v_add_f32_e32 v205, v157, v9
	v_add_f32_e32 v206, v157, v25
	ds_write_b16 v158, v2 offset:19584
	ds_write_b16 v158, v3 offset:24192
	ds_write_b16 v158, v4 offset:19728
	ds_write_b16 v158, v5 offset:24336
	v_cvt_f16_f32_e32 v2, v201
	v_cvt_f16_f32_e32 v3, v202
	v_cvt_f16_f32_e32 v4, v205
	v_cvt_f16_f32_e32 v5, v206
	v_add_f32_e32 v207, v157, v10
	v_add_f32_e32 v209, v157, v26
	v_add_f32_e32 v208, v157, v11
	v_add_f32_e32 v210, v157, v27
	ds_write_b16 v158, v2 offset:19872
	ds_write_b16 v158, v3 offset:24480
	ds_write_b16 v158, v4 offset:20016
	ds_write_b16 v158, v5 offset:24624
	v_cvt_f16_f32_e32 v2, v207
	v_cvt_f16_f32_e32 v3, v209
	v_cvt_f16_f32_e32 v4, v208
	v_cvt_f16_f32_e32 v5, v210
	v_add_f32_e32 v211, v157, v12
	v_add_f32_e32 v212, v157, v28
	v_add_f32_e32 v213, v157, v13
	v_add_f32_e32 v214, v157, v29
	ds_write_b16 v158, v2 offset:20736
	ds_write_b16 v158, v3 offset:25344
	ds_write_b16 v158, v4 offset:20880
	ds_write_b16 v158, v5 offset:25488
	v_cvt_f16_f32_e32 v2, v211
	v_cvt_f16_f32_e32 v3, v212
	v_cvt_f16_f32_e32 v4, v213
	v_cvt_f16_f32_e32 v5, v214
	v_add_f32_e32 v215, v157, v14
	v_add_f32_e32 v216, v157, v30
	v_add_f32_e32 v217, v157, v15
	v_add_f32_e32 v218, v157, v31
	ds_write_b16 v158, v2 offset:21024
	ds_write_b16 v158, v3 offset:25632
	ds_write_b16 v158, v4 offset:21168
	ds_write_b16 v158, v5 offset:25776
	v_cvt_f16_f32_e32 v2, v215
	v_cvt_f16_f32_e32 v3, v216
	v_cvt_f16_f32_e32 v4, v217
	v_cvt_f16_f32_e32 v5, v218
	v_add_f32_e32 v186, v157, v18
	v_add_f32_e32 v188, v157, v19
	v_add_f32_e32 v219, v157, v16
	v_add_f32_e32 v221, v157, v32
	v_add_f32_e32 v220, v157, v17
	v_add_f32_e32 v222, v157, v33
	v_cvt_f16_f32_e32 v18, v186
	v_cvt_f16_f32_e32 v19, v188
	ds_write_b16 v158, v2 offset:21888
	ds_write_b16 v158, v3 offset:26496
	ds_write_b16 v158, v4 offset:22032
	ds_write_b16 v158, v5 offset:26640
	v_cvt_f16_f32_e32 v2, v219
	v_cvt_f16_f32_e32 v3, v221
	v_cvt_f16_f32_e32 v4, v220
	v_cvt_f16_f32_e32 v5, v222
	ds_write_b16 v158, v18 offset:23040
	ds_write_b16 v158, v19 offset:23184
	ds_write_b16 v158, v2 offset:22176
	ds_write_b16 v158, v3 offset:26784
	ds_write_b16 v158, v4 offset:22320
	ds_write_b16 v158, v5 offset:26928
	s_waitcnt lgkmcnt(0)
	s_barrier
	ds_read_b128 v[2:5], v159
	ds_read_b128 v[18:21], v159 offset:8704
	s_waitcnt lgkmcnt(1)
	v_mfma_f32_32x32x16_f16 v[50:65], v[2:5], v[126:129], 0
	v_lshlrev_b32_e32 v0, 3, v0
	s_addc_u32 s1, s9, s1
	v_and_b32_e32 v0, 0x1f8, v0
	global_load_dwordx2 v[138:139], v0, s[0:1]
	s_waitcnt lgkmcnt(0)
	v_mfma_f32_32x32x16_f16 v[34:49], v[18:21], v[126:129], 0
	v_mfma_f32_32x32x16_f16 v[2:17], v[2:5], v[122:125], 0
	v_mfma_f32_32x32x16_f16 v[18:33], v[18:21], v[122:125], 0
	ds_read_b128 v[130:133], v159 offset:32
	ds_read_b128 v[134:137], v159 offset:8736
	s_waitcnt lgkmcnt(1)
	v_mfma_f32_32x32x16_f16 v[50:65], v[130:133], v[118:121], v[50:65]
	s_waitcnt lgkmcnt(0)
	v_mfma_f32_32x32x16_f16 v[34:49], v[134:137], v[118:121], v[34:49]
	v_mfma_f32_32x32x16_f16 v[2:17], v[130:133], v[114:117], v[2:17]
	v_mfma_f32_32x32x16_f16 v[18:33], v[134:137], v[114:117], v[18:33]
	ds_read_b128 v[224:227], v159 offset:64
	ds_read_b128 v[228:231], v159 offset:8768
	ds_read_b128 v[130:133], v159 offset:96
	ds_read_b128 v[134:137], v159 offset:8800
	s_waitcnt lgkmcnt(3)
	v_mfma_f32_32x32x16_f16 v[50:65], v[224:227], v[110:113], v[50:65]
	s_waitcnt lgkmcnt(2)
	v_mfma_f32_32x32x16_f16 v[34:49], v[228:231], v[110:113], v[34:49]
	v_mfma_f32_32x32x16_f16 v[2:17], v[224:227], v[106:109], v[2:17]
	v_mfma_f32_32x32x16_f16 v[18:33], v[228:231], v[106:109], v[18:33]
	ds_read_b128 v[224:227], v159 offset:128
	ds_read_b128 v[228:231], v159 offset:8832
	s_waitcnt lgkmcnt(3)
	v_mfma_f32_32x32x16_f16 v[50:65], v[130:133], v[102:105], v[50:65]
	s_waitcnt lgkmcnt(2)
	v_mfma_f32_32x32x16_f16 v[34:49], v[134:137], v[102:105], v[34:49]
	v_mfma_f32_32x32x16_f16 v[2:17], v[130:133], v[98:101], v[2:17]
	v_mfma_f32_32x32x16_f16 v[18:33], v[134:137], v[98:101], v[18:33]
	ds_read_b128 v[130:133], v159 offset:160
	ds_read_b128 v[134:137], v159 offset:8864
	s_waitcnt lgkmcnt(3)
	v_mfma_f32_32x32x16_f16 v[50:65], v[224:227], v[94:97], v[50:65]
	s_waitcnt lgkmcnt(2)
	v_mfma_f32_32x32x16_f16 v[34:49], v[228:231], v[94:97], v[34:49]
	v_mfma_f32_32x32x16_f16 v[2:17], v[224:227], v[86:89], v[2:17]
	v_mfma_f32_32x32x16_f16 v[18:33], v[228:231], v[86:89], v[18:33]
	ds_read_b128 v[224:227], v159 offset:192
	ds_read_b128 v[228:231], v159 offset:8896
	s_waitcnt lgkmcnt(3)
	v_mfma_f32_32x32x16_f16 v[50:65], v[130:133], v[90:93], v[50:65]
	s_waitcnt lgkmcnt(2)
	v_mfma_f32_32x32x16_f16 v[34:49], v[134:137], v[90:93], v[34:49]
	v_mfma_f32_32x32x16_f16 v[2:17], v[130:133], v[78:81], v[2:17]
	v_add_f32_e32 v130, v193, v196
	v_add_f32_e32 v130, 0, v130
	v_add_f32_e32 v132, v198, v200
	v_add_f32_e32 v130, v132, v130
	v_mul_f32_e32 v132, v200, v200
	v_fmac_f32_e32 v132, v198, v198
	v_mul_f32_e32 v131, v196, v196
	v_mfma_f32_32x32x16_f16 v[18:33], v[134:137], v[78:81], v[18:33]
	ds_read_b128 v[232:235], v159 offset:224
	ds_read_b128 v[236:239], v159 offset:8928
	v_fmac_f32_e32 v131, v193, v193
	v_add_f32_e32 v131, v131, v132
	v_add_f32_e32 v132, v203, v204
	v_add_f32_e32 v130, v132, v130
	v_mul_f32_e32 v132, v204, v204
	s_waitcnt lgkmcnt(3)
	v_mfma_f32_32x32x16_f16 v[50:65], v[224:227], v[82:85], v[50:65]
	v_fmac_f32_e32 v132, v203, v203
	v_add_f32_e32 v193, v132, v131
	v_add_f32_e32 v131, v1, v160
	v_add_f32_e32 v196, v131, v130
	global_load_dwordx2 v[134:135], v0, s[0:1] offset:512
	global_load_dwordx2 v[132:133], v0, s[0:1] offset:1024
	global_load_dwordx2 v[130:131], v0, s[0:1] offset:1536
	s_waitcnt lgkmcnt(2)
	v_mfma_f32_32x32x16_f16 v[34:49], v[228:231], v[82:85], v[34:49]
	global_load_dwordx2 v[136:137], v0, s[0:1] offset:2048
	v_mfma_f32_32x32x16_f16 v[2:17], v[224:227], v[70:73], v[2:17]
	v_mfma_f32_32x32x16_f16 v[18:33], v[228:231], v[70:73], v[18:33]
	s_waitcnt lgkmcnt(1)
	v_mfma_f32_32x32x16_f16 v[50:65], v[232:235], v[74:77], v[50:65]
	v_mfma_f32_32x32x16_f16 v[2:17], v[232:235], v[66:69], v[2:17]
	s_nop 10
	v_cvt_pk_f16_f32 v57, v56, v57
	v_cvt_pk_f16_f32 v56, v54, v55
	v_cvt_pk_f16_f32 v54, v50, v51
	s_waitcnt vmcnt(12)
	v_lshlrev_b32_e32 v50, 8, v148
	v_cvt_pk_f16_f32 v55, v52, v53
	v_perm_b32 v50, v50, v148, s2
	v_lshrrev_b32_e32 v51, 16, v148
	v_lshrrev_b32_e32 v52, 8, v148
	v_lshrrev_b32_e32 v53, 16, v149
	v_lshrrev_b32_e32 v148, 8, v149
	v_perm_b32 v51, v52, v51, s2
	v_lshlrev_b32_e32 v52, 8, v149
	v_perm_b32 v53, v148, v53, s2
	s_waitcnt vmcnt(8)
	v_perm_b32 v52, v52, v149, s2
	v_perm_b32 v149, v240, v146, s43
	v_perm_b32 v198, v240, v147, s42
	s_waitcnt lgkmcnt(0)
	v_mfma_f32_32x32x16_f16 v[18:33], v[236:239], v[66:69], v[18:33]
	v_or_b32_e32 v50, 0x64006400, v50
	v_or_b32_e32 v51, 0x64006400, v51
	v_or_b32_e32 v52, 0x64006400, v52
	v_or_b32_e32 v53, 0x64006400, v53
	v_pk_add_f16 v50, v50, s3 op_sel_hi:[1,0]
	v_pk_add_f16 v51, v51, s3 op_sel_hi:[1,0]
	v_pk_add_f16 v52, v52, s3 op_sel_hi:[1,0]
	v_pk_add_f16 v53, v53, s3 op_sel_hi:[1,0]
	v_perm_b32 v148, v240, v146, s42
	v_perm_b32 v200, v240, v147, s43
	v_pk_add_f16 v146, v148, s3 op_sel_hi:[1,0]
	v_pk_add_f16 v147, v149, s3 op_sel_hi:[1,0]
	v_pk_add_f16 v148, v198, s3 op_sel_hi:[1,0]
	v_pk_add_f16 v149, v200, s3 op_sel_hi:[1,0]
	v_cvt_pk_f16_f32 v65, v64, v65
	v_cvt_pk_f16_f32 v64, v62, v63
	v_cvt_pk_f16_f32 v62, v58, v59
	v_cvt_pk_f16_f32 v63, v60, v61
	s_waitcnt vmcnt(7)
	v_mfma_f32_32x32x16_f16 v[34:49], v[236:239], v[74:77], v[34:49]
	v_mfma_f32_32x32x16_f16 v[2:17], v[50:53], v[54:57], v[2:17]
	v_perm_b32 v58, v240, v144, s42
	v_perm_b32 v59, v240, v144, s43
	v_perm_b32 v60, v240, v145, s42
	v_perm_b32 v61, v240, v145, s43
	v_mfma_f32_32x32x16_f16 v[18:33], v[146:149], v[54:57], v[18:33]
	v_pk_add_f16 v58, v58, s3 op_sel_hi:[1,0]
	v_pk_add_f16 v59, v59, s3 op_sel_hi:[1,0]
	v_pk_add_f16 v60, v60, s3 op_sel_hi:[1,0]
	v_pk_add_f16 v61, v61, s3 op_sel_hi:[1,0]
	v_perm_b32 v144, v240, v154, s42
	v_perm_b32 v145, v240, v154, s43
	v_perm_b32 v154, v240, v155, s42
	v_perm_b32 v155, v240, v155, s43
	v_pk_add_f16 v224, v144, s3 op_sel_hi:[1,0]
	v_pk_add_f16 v225, v145, s3 op_sel_hi:[1,0]
	v_pk_add_f16 v226, v154, s3 op_sel_hi:[1,0]
	v_pk_add_f16 v227, v155, s3 op_sel_hi:[1,0]
	v_cvt_pk_f16_f32 v41, v40, v41
	v_cvt_pk_f16_f32 v40, v38, v39
	v_cvt_pk_f16_f32 v39, v36, v37
	v_cvt_pk_f16_f32 v38, v34, v35
	s_waitcnt vmcnt(6)
	v_mfma_f32_32x32x16_f16 v[2:17], v[58:61], v[62:65], v[2:17]
	v_perm_b32 v34, v240, v142, s42
	v_perm_b32 v35, v240, v142, s43
	v_mfma_f32_32x32x16_f16 v[18:33], v[224:227], v[62:65], v[18:33]
	v_perm_b32 v36, v240, v143, s42
	v_perm_b32 v37, v240, v143, s43
	v_pk_add_f16 v34, v34, s3 op_sel_hi:[1,0]
	v_pk_add_f16 v35, v35, s3 op_sel_hi:[1,0]
	v_pk_add_f16 v36, v36, s3 op_sel_hi:[1,0]
	v_pk_add_f16 v37, v37, s3 op_sel_hi:[1,0]
	v_perm_b32 v142, v240, v152, s42
	v_perm_b32 v143, v240, v152, s43
	v_perm_b32 v144, v240, v153, s42
	v_perm_b32 v53, v240, v153, s43
	v_pk_add_f16 v50, v142, s3 op_sel_hi:[1,0]
	v_pk_add_f16 v51, v143, s3 op_sel_hi:[1,0]
	v_pk_add_f16 v52, v144, s3 op_sel_hi:[1,0]
	v_pk_add_f16 v53, v53, s3 op_sel_hi:[1,0]
	v_cvt_pk_f16_f32 v49, v48, v49
	v_cvt_pk_f16_f32 v48, v46, v47
	v_cvt_pk_f16_f32 v47, v44, v45
	v_cvt_pk_f16_f32 v46, v42, v43
	v_mfma_f32_32x32x16_f16 v[2:17], v[34:37], v[38:41], v[2:17]
	s_waitcnt vmcnt(5)
	v_lshlrev_b32_e32 v54, 8, v150
	v_mfma_f32_32x32x16_f16 v[18:33], v[50:53], v[38:41], v[18:33]
	v_lshrrev_b32_e32 v37, 16, v151
	v_lshrrev_b32_e32 v38, 8, v151
	v_perm_b32 v34, v54, v150, s2
	v_perm_b32 v37, v38, v37, s2
	v_perm_b32 v42, v240, v140, s42
	v_perm_b32 v43, v240, v140, s43
	v_perm_b32 v44, v240, v141, s42
	v_perm_b32 v45, v240, v141, s43
	v_or_b32_e32 v34, 0x64006400, v34
	v_perm_b32 v35, v240, v150, s43
	v_perm_b32 v36, v240, v151, s42
	v_or_b32_e32 v37, 0x64006400, v37
	v_pk_add_f16 v42, v42, s3 op_sel_hi:[1,0]
	v_pk_add_f16 v43, v43, s3 op_sel_hi:[1,0]
	v_pk_add_f16 v44, v44, s3 op_sel_hi:[1,0]
	v_pk_add_f16 v45, v45, s3 op_sel_hi:[1,0]
	v_pk_add_f16 v34, v34, s3 op_sel_hi:[1,0]
	v_pk_add_f16 v35, v35, s3 op_sel_hi:[1,0]
	v_pk_add_f16 v36, v36, s3 op_sel_hi:[1,0]
	v_pk_add_f16 v37, v37, s3 op_sel_hi:[1,0]
	v_mfma_f32_32x32x16_f16 v[2:17], v[42:45], v[46:49], v[2:17]
	global_load_dwordx2 v[142:143], v0, s[0:1] offset:2560
	global_load_dwordx2 v[140:141], v0, s[0:1] offset:3072
	global_load_dwordx2 v[64:65], v0, s[0:1] offset:3584
	v_mfma_f32_32x32x16_f16 v[18:33], v[34:37], v[46:49], v[18:33]
	s_nop 7
	v_add_f32_e32 v146, v157, v2
	v_add_f32_e32 v148, v157, v3
	v_cvt_f16_f32_e32 v0, v146
	v_cvt_f16_f32_e32 v3, v148
	v_add_f32_e32 v150, v157, v4
	v_add_f32_e32 v152, v157, v5
	ds_write_b16 v158, v0
	v_add_f32_e32 v147, v157, v18
	v_cvt_f16_f32_e32 v2, v147
	v_add_f32_e32 v151, v157, v20
	v_add_f32_e32 v153, v157, v21
	ds_write_b16 v158, v3 offset:144
	ds_write_b16 v158, v2 offset:4608
	v_cvt_f16_f32_e32 v0, v150
	v_cvt_f16_f32_e32 v2, v151
	v_cvt_f16_f32_e32 v3, v152
	v_cvt_f16_f32_e32 v4, v153
	v_add_f32_e32 v154, v157, v6
	v_add_f32_e32 v155, v157, v22
	v_add_f32_e32 v198, v157, v7
	v_add_f32_e32 v200, v157, v23
	ds_write_b16 v158, v0 offset:288
	ds_write_b16 v158, v2 offset:4896
	ds_write_b16 v158, v3 offset:432
	ds_write_b16 v158, v4 offset:5040
	v_cvt_f16_f32_e32 v0, v154
	v_cvt_f16_f32_e32 v2, v155
	v_cvt_f16_f32_e32 v3, v198
	v_cvt_f16_f32_e32 v4, v200
	v_add_f32_e32 v203, v157, v8
	v_add_f32_e32 v204, v157, v24
	v_add_f32_e32 v223, v157, v9
	v_add_f32_e32 v224, v157, v25
	ds_write_b16 v158, v0 offset:1152
	ds_write_b16 v158, v2 offset:5760
	ds_write_b16 v158, v3 offset:1296
	ds_write_b16 v158, v4 offset:5904
	v_cvt_f16_f32_e32 v0, v203
	v_cvt_f16_f32_e32 v2, v204
	v_cvt_f16_f32_e32 v3, v223
	v_cvt_f16_f32_e32 v4, v224
	v_add_f32_e32 v225, v157, v10
	v_add_f32_e32 v226, v157, v26
	v_add_f32_e32 v227, v157, v11
	v_add_f32_e32 v228, v157, v27
	ds_write_b16 v158, v0 offset:1440
	ds_write_b16 v158, v2 offset:6048
	ds_write_b16 v158, v3 offset:1584
	ds_write_b16 v158, v4 offset:6192
	v_cvt_f16_f32_e32 v0, v225
	v_cvt_f16_f32_e32 v2, v226
	v_cvt_f16_f32_e32 v3, v227
	v_cvt_f16_f32_e32 v4, v228
	v_add_f32_e32 v229, v157, v12
	v_add_f32_e32 v230, v157, v28
	v_add_f32_e32 v231, v157, v13
	v_add_f32_e32 v232, v157, v29
	ds_write_b16 v158, v0 offset:2304
	ds_write_b16 v158, v2 offset:6912
	ds_write_b16 v158, v3 offset:2448
	ds_write_b16 v158, v4 offset:7056
	v_cvt_f16_f32_e32 v0, v229
	v_cvt_f16_f32_e32 v2, v230
	v_cvt_f16_f32_e32 v3, v231
	v_cvt_f16_f32_e32 v4, v232
	v_add_f32_e32 v233, v157, v14
	v_add_f32_e32 v234, v157, v30
	v_add_f32_e32 v235, v157, v15
	v_add_f32_e32 v236, v157, v31
	ds_write_b16 v158, v0 offset:2592
	ds_write_b16 v158, v2 offset:7200
	ds_write_b16 v158, v3 offset:2736
	ds_write_b16 v158, v4 offset:7344
	v_cvt_f16_f32_e32 v0, v233
	v_cvt_f16_f32_e32 v2, v234
	v_cvt_f16_f32_e32 v3, v235
	v_cvt_f16_f32_e32 v4, v236
	v_add_f32_e32 v149, v157, v19
	v_add_f32_e32 v237, v157, v16
	v_add_f32_e32 v238, v157, v32
	v_add_f32_e32 v144, v157, v17
	v_add_f32_e32 v145, v157, v33
	v_cvt_f16_f32_e32 v18, v149
	ds_write_b16 v158, v0 offset:3456
	ds_write_b16 v158, v2 offset:8064
	ds_write_b16 v158, v3 offset:3600
	ds_write_b16 v158, v4 offset:8208
	v_cvt_f16_f32_e32 v0, v237
	v_cvt_f16_f32_e32 v2, v238
	v_cvt_f16_f32_e32 v3, v144
	v_cvt_f16_f32_e32 v4, v145
	ds_write_b16 v158, v18 offset:4752
	ds_write_b16 v158, v0 offset:3744
	ds_write_b16 v158, v2 offset:8352
	ds_write_b16 v158, v3 offset:3888
	ds_write_b16 v158, v4 offset:8496
	s_waitcnt lgkmcnt(0)
	s_barrier
	ds_read_b128 v[16:19], v159 offset:43520
	s_waitcnt lgkmcnt(0)
	v_mfma_f32_32x32x16_f16 v[32:47], v[16:19], v[126:129], 0
	ds_read_b128 v[2:5], v159 offset:34816
	v_mul_f32_e32 v0, v160, v160
	v_fmac_f32_e32 v0, v1, v1
	v_mul_f32_e32 v6, v162, v162
	v_add_f32_e32 v0, v0, v193
	v_add_f32_e32 v1, v161, v162
	v_fmac_f32_e32 v6, v161, v161
	s_waitcnt lgkmcnt(0)
	v_mfma_f32_32x32x16_f16 v[48:63], v[2:5], v[126:129], 0
	ds_read_b128 v[126:129], v159 offset:34848
	v_add_f32_e32 v1, v1, v196
	v_add_f32_e32 v0, v6, v0
	v_add_f32_e32 v6, v163, v164
	v_add_f32_e32 v1, v6, v1
	v_mul_f32_e32 v6, v164, v164
	v_fmac_f32_e32 v6, v163, v163
	v_add_f32_e32 v0, v6, v0
	v_add_f32_e32 v6, v165, v166
	v_add_f32_e32 v1, v6, v1
	v_mul_f32_e32 v6, v166, v166
	v_fmac_f32_e32 v6, v165, v165
	v_add_f32_e32 v20, v6, v0
	v_add_f32_e32 v0, v167, v168
	v_add_f32_e32 v21, v0, v1
	s_waitcnt lgkmcnt(0)
	v_mfma_f32_32x32x16_f16 v[48:63], v[126:129], v[118:121], v[48:63]
	v_mul_f32_e32 v22, v168, v168
	v_fmac_f32_e32 v22, v167, v167
	v_add_f32_e32 v160, v22, v20
	v_add_f32_e32 v20, v169, v170
	v_mul_f32_e32 v162, v170, v170
	v_add_f32_e32 v161, v20, v21
	v_fmac_f32_e32 v162, v169, v169
	v_mfma_f32_32x32x16_f16 v[0:15], v[2:5], v[122:125], 0
	v_mfma_f32_32x32x16_f16 v[0:15], v[126:129], v[114:117], v[0:15]
	v_mfma_f32_32x32x16_f16 v[16:31], v[16:19], v[122:125], 0
	v_add_f32_e32 v123, v171, v172
	v_add_f32_e32 v122, v162, v160
	v_add_f32_e32 v160, v123, v161
	v_mul_f32_e32 v123, v172, v172
	v_fmac_f32_e32 v123, v171, v171
	v_add_f32_e32 v161, v123, v122
	ds_read_b128 v[122:125], v159 offset:43552
	v_add_f32_e32 v162, v173, v174
	v_add_f32_e32 v160, v162, v160
	v_mul_f32_e32 v162, v174, v174
	v_fmac_f32_e32 v162, v173, v173
	s_waitcnt lgkmcnt(0)
	v_mfma_f32_32x32x16_f16 v[32:47], v[122:125], v[118:121], v[32:47]
	v_mul_f32_e32 v118, v176, v176
	v_add_f32_e32 v161, v162, v161
	v_add_f32_e32 v162, v175, v176
	v_fmac_f32_e32 v118, v175, v175
	v_mul_f32_e32 v120, v178, v178
	v_add_f32_e32 v160, v162, v160
	v_add_f32_e32 v118, v118, v161
	v_add_f32_e32 v119, v177, v178
	v_fmac_f32_e32 v120, v177, v177
	v_add_f32_e32 v119, v119, v160
	v_add_f32_e32 v118, v120, v118
	v_add_f32_e32 v120, v179, v180
	v_add_f32_e32 v126, v120, v119
	v_mul_f32_e32 v119, v180, v180
	v_mfma_f32_32x32x16_f16 v[16:31], v[122:125], v[114:117], v[16:31]
	v_add_f32_e32 v114, v181, v183
	v_fmac_f32_e32 v119, v179, v179
	v_add_f32_e32 v122, v114, v126
	v_mul_f32_e32 v114, v183, v183
	v_add_f32_e32 v127, v119, v118
	v_fmac_f32_e32 v114, v181, v181
	ds_read_b128 v[118:121], v159 offset:34880
	v_add_f32_e32 v123, v114, v127
	ds_read_b128 v[114:117], v159 offset:43584
	v_add_f32_e32 v124, v182, v184
	v_add_f32_e32 v122, v124, v122
	v_mul_f32_e32 v124, v184, v184
	v_fmac_f32_e32 v124, v182, v182
	s_waitcnt lgkmcnt(1)
	v_mfma_f32_32x32x16_f16 v[48:63], v[118:121], v[110:113], v[48:63]
	v_add_f32_e32 v123, v124, v123
	v_add_f32_e32 v124, v185, v186
	v_add_f32_e32 v124, 0, v124
	v_add_f32_e32 v122, 0, v122
	s_waitcnt lgkmcnt(0)
	v_mfma_f32_32x32x16_f16 v[32:47], v[114:117], v[110:113], v[32:47]
	v_mul_f32_e32 v110, v186, v186
	v_mul_f32_e32 v112, v188, v188
	v_fmac_f32_e32 v110, v185, v185
	v_add_f32_e32 v111, v187, v188
	v_fmac_f32_e32 v112, v187, v187
	v_add_f32_e32 v111, v111, v124
	v_add_f32_e32 v110, v110, v112
	v_add_f32_e32 v112, v189, v190
	v_mfma_f32_32x32x16_f16 v[0:15], v[118:121], v[106:109], v[0:15]
	v_add_f32_e32 v118, v112, v111
	v_mul_f32_e32 v111, v190, v190
	v_fmac_f32_e32 v111, v189, v189
	v_add_f32_e32 v119, v111, v110
	v_add_f32_e32 v120, v191, v192
	ds_read_b128 v[110:113], v159 offset:34912
	v_mfma_f32_32x32x16_f16 v[16:31], v[114:117], v[106:109], v[16:31]
	v_mul_f32_e32 v107, v192, v192
	v_fmac_f32_e32 v107, v191, v191
	v_add_f32_e32 v106, v120, v118
	v_add_f32_e32 v114, v107, v119
	v_add_f32_e32 v107, v194, v195
	v_add_f32_e32 v115, v107, v106
	ds_read_b128 v[106:109], v159 offset:43616
	v_mul_f32_e32 v116, v195, v195
	v_fmac_f32_e32 v116, v194, v194
	v_add_f32_e32 v114, v116, v114
	v_add_f32_e32 v116, v197, v199
	v_add_f32_e32 v115, v116, v115
	v_mul_f32_e32 v116, v199, v199
	s_waitcnt lgkmcnt(1)
	v_mfma_f32_32x32x16_f16 v[48:63], v[110:113], v[102:105], v[48:63]
	v_fmac_f32_e32 v116, v197, v197
	s_waitcnt lgkmcnt(0)
	v_mfma_f32_32x32x16_f16 v[32:47], v[106:109], v[102:105], v[32:47]
	v_mul_f32_e32 v104, v202, v202
	v_add_f32_e32 v102, v116, v114
	v_add_f32_e32 v103, v201, v202
	v_fmac_f32_e32 v104, v201, v201
	v_add_f32_e32 v103, v103, v115
	v_add_f32_e32 v102, v104, v102
	v_add_f32_e32 v104, v205, v206
	v_add_f32_e32 v103, v104, v103
	v_mul_f32_e32 v104, v206, v206
	v_mfma_f32_32x32x16_f16 v[0:15], v[110:113], v[98:101], v[0:15]
	v_fmac_f32_e32 v104, v205, v205
	v_add_f32_e32 v110, v104, v102
	v_add_f32_e32 v102, v207, v209
	v_add_f32_e32 v111, v102, v103
	ds_read_b128 v[102:105], v159 offset:34944
	v_mfma_f32_32x32x16_f16 v[16:31], v[106:109], v[98:101], v[16:31]
	v_mul_f32_e32 v98, v209, v209
	v_fmac_f32_e32 v98, v207, v207
	v_add_f32_e32 v106, v98, v110
	v_add_f32_e32 v98, v208, v210
	v_add_f32_e32 v107, v98, v111
	ds_read_b128 v[98:101], v159 offset:43648
	v_mul_f32_e32 v108, v210, v210
	v_fmac_f32_e32 v108, v208, v208
	v_add_f32_e32 v106, v108, v106
	v_add_f32_e32 v108, v211, v212
	s_waitcnt lgkmcnt(1)
	v_mfma_f32_32x32x16_f16 v[48:63], v[102:105], v[94:97], v[48:63]
	v_add_f32_e32 v107, v108, v107
	v_mul_f32_e32 v108, v212, v212
	v_fmac_f32_e32 v108, v211, v211
	v_add_f32_e32 v106, v108, v106
	s_waitcnt lgkmcnt(0)
	v_mfma_f32_32x32x16_f16 v[32:47], v[98:101], v[94:97], v[32:47]
	v_add_f32_e32 v94, v213, v214
	v_add_f32_e32 v94, v94, v107
	v_mul_f32_e32 v95, v214, v214
	v_add_f32_e32 v96, v215, v216
	v_fmac_f32_e32 v95, v213, v213
	v_add_f32_e32 v94, v96, v94
	v_mul_f32_e32 v96, v216, v216
	v_add_f32_e32 v95, v95, v106
	v_fmac_f32_e32 v96, v215, v215
	v_mfma_f32_32x32x16_f16 v[0:15], v[102:105], v[86:89], v[0:15]
	v_add_f32_e32 v102, v96, v95
	v_add_f32_e32 v95, v217, v218
	v_add_f32_e32 v103, v95, v94
	ds_read_b128 v[94:97], v159 offset:34976
	v_mul_f32_e32 v104, v218, v218
	v_fmac_f32_e32 v104, v217, v217
	v_mfma_f32_32x32x16_f16 v[16:31], v[98:101], v[86:89], v[16:31]
	v_add_f32_e32 v86, v219, v221
	v_add_f32_e32 v99, v86, v103
	ds_read_b128 v[86:89], v159 offset:43680
	v_mul_f32_e32 v100, v221, v221
	v_add_f32_e32 v98, v104, v102
	v_fmac_f32_e32 v100, v219, v219
	v_add_f32_e32 v98, v100, v98
	s_waitcnt lgkmcnt(1)
	v_mfma_f32_32x32x16_f16 v[48:63], v[94:97], v[90:93], v[48:63]
	v_add_f32_e32 v100, v220, v222
	v_add_f32_e32 v99, v100, v99
	v_mul_f32_e32 v100, v222, v222
	v_fmac_f32_e32 v100, v220, v220
	v_add_f32_e32 v98, v100, v98
	v_add_f32_e32 v98, v123, v98
	v_add_f32_e32 v99, v122, v99
	s_waitcnt lgkmcnt(0)
	v_mfma_f32_32x32x16_f16 v[32:47], v[86:89], v[90:93], v[32:47]
	v_add_f32_e32 v90, v146, v147
	v_add_f32_e32 v90, 0, v90
	v_add_f32_e32 v92, v148, v149
	v_mul_f32_e32 v91, v147, v147
	v_add_f32_e32 v90, v92, v90
	v_mul_f32_e32 v92, v149, v149
	v_fmac_f32_e32 v91, v146, v146
	v_fmac_f32_e32 v92, v148, v148
	v_mfma_f32_32x32x16_f16 v[0:15], v[94:97], v[78:81], v[0:15]
	v_add_f32_e32 v94, v91, v92
	v_add_f32_e32 v91, v150, v151
	v_add_f32_e32 v95, v91, v90
	ds_read_b128 v[90:93], v159 offset:35008
	v_mul_f32_e32 v96, v151, v151
	v_fmac_f32_e32 v96, v150, v150
	v_mfma_f32_32x32x16_f16 v[16:31], v[86:89], v[78:81], v[16:31]
	v_add_f32_e32 v78, v152, v153
	v_add_f32_e32 v87, v78, v95
	ds_read_b128 v[78:81], v159 offset:43712
	v_mul_f32_e32 v88, v153, v153
	v_add_f32_e32 v86, v96, v94
	v_fmac_f32_e32 v88, v152, v152
	v_add_f32_e32 v86, v88, v86
	v_add_f32_e32 v88, v154, v155
	v_add_f32_e32 v87, v88, v87
	v_mul_f32_e32 v88, v155, v155
	v_fmac_f32_e32 v88, v154, v154
	v_add_f32_e32 v86, v88, v86
	v_add_f32_e32 v88, v198, v200
	s_waitcnt lgkmcnt(1)
	v_mfma_f32_32x32x16_f16 v[48:63], v[90:93], v[82:85], v[48:63]
	s_waitcnt lgkmcnt(0)
	v_mfma_f32_32x32x16_f16 v[32:47], v[78:81], v[82:85], v[32:47]
	v_add_f32_e32 v82, v88, v87
	v_mul_f32_e32 v83, v200, v200
	v_add_f32_e32 v84, v203, v204
	v_fmac_f32_e32 v83, v198, v198
	v_add_f32_e32 v82, v84, v82
	v_mul_f32_e32 v84, v204, v204
	v_add_f32_e32 v83, v83, v86
	v_fmac_f32_e32 v84, v203, v203
	v_add_f32_e32 v86, v84, v83
	v_add_f32_e32 v83, v223, v224
	v_mfma_f32_32x32x16_f16 v[0:15], v[90:93], v[70:73], v[0:15]
	v_add_f32_e32 v87, v83, v82
	v_mul_f32_e32 v88, v224, v224
	v_fmac_f32_e32 v88, v223, v223
	ds_read_b128 v[82:85], v159 offset:35040
	v_mfma_f32_32x32x16_f16 v[16:31], v[78:81], v[70:73], v[16:31]
	v_add_f32_e32 v71, v225, v226
	v_add_f32_e32 v78, v71, v87
	v_mul_f32_e32 v71, v226, v226
	v_add_f32_e32 v70, v88, v86
	v_fmac_f32_e32 v71, v225, v225
	v_add_f32_e32 v79, v71, v70
	ds_read_b128 v[70:73], v159 offset:43744
	s_waitcnt lgkmcnt(1)
	v_mfma_f32_32x32x16_f16 v[48:63], v[82:85], v[74:77], v[48:63]
	v_add_f32_e32 v80, v227, v228
	v_add_f32_e32 v78, v80, v78
	v_mul_f32_e32 v80, v228, v228
	v_fmac_f32_e32 v80, v227, v227
	v_add_f32_e32 v79, v80, v79
	v_add_f32_e32 v80, v229, v230
	v_add_f32_e32 v78, v80, v78
	v_mfma_f32_32x32x16_f16 v[0:15], v[82:85], v[66:69], v[0:15]
	s_nop 3
	v_cvt_pk_f16_f32 v55, v54, v55
	v_cvt_pk_f16_f32 v54, v52, v53
	v_cvt_pk_f16_f32 v53, v50, v51
	v_cvt_pk_f16_f32 v52, v48, v49
	s_waitcnt vmcnt(3)
	s_waitcnt lgkmcnt(0)
	v_mfma_f32_32x32x16_f16 v[16:31], v[70:73], v[66:69], v[16:31]
	v_lshrrev_b32_e32 v69, 16, v139
	v_mfma_f32_32x32x16_f16 v[32:47], v[70:73], v[74:77], v[32:47]
	v_lshrrev_b32_e32 v70, 8, v139
	v_perm_b32 v69, v70, v69, s2
	v_perm_b32 v66, v240, v138, s42
	v_perm_b32 v67, v240, v138, s43
	v_perm_b32 v68, v240, v139, s42
	v_or_b32_e32 v69, 0x64006400, v69
	v_pk_add_f16 v66, v66, s3 op_sel_hi:[1,0]
	v_pk_add_f16 v67, v67, s3 op_sel_hi:[1,0]
	v_pk_add_f16 v68, v68, s3 op_sel_hi:[1,0]
	v_pk_add_f16 v69, v69, s3 op_sel_hi:[1,0]
	s_nop 1
	v_mfma_f32_32x32x16_f16 v[0:15], v[66:69], v[52:55], v[0:15]
	v_perm_b32 v48, v240, v136, s42
	v_perm_b32 v49, v240, v136, s43
	v_perm_b32 v50, v240, v137, s42
	v_perm_b32 v51, v240, v137, s43
	v_pk_add_f16 v48, v48, s3 op_sel_hi:[1,0]
	v_pk_add_f16 v49, v49, s3 op_sel_hi:[1,0]
	v_pk_add_f16 v50, v50, s3 op_sel_hi:[1,0]
	v_pk_add_f16 v51, v51, s3 op_sel_hi:[1,0]
	v_cvt_pk_f16_f32 v39, v38, v39
	v_cvt_pk_f16_f32 v38, v36, v37
	v_mfma_f32_32x32x16_f16 v[16:31], v[48:51], v[52:55], v[16:31]
	v_perm_b32 v48, v240, v134, s42
	v_perm_b32 v49, v240, v134, s43
	v_perm_b32 v50, v240, v135, s42
	v_perm_b32 v51, v240, v135, s43
	v_pk_add_f16 v48, v48, s3 op_sel_hi:[1,0]
	v_pk_add_f16 v49, v49, s3 op_sel_hi:[1,0]
	v_pk_add_f16 v50, v50, s3 op_sel_hi:[1,0]
	v_pk_add_f16 v51, v51, s3 op_sel_hi:[1,0]
	v_cvt_pk_f16_f32 v55, v62, v63
	v_cvt_pk_f16_f32 v54, v60, v61
	v_cvt_pk_f16_f32 v53, v58, v59
	v_cvt_pk_f16_f32 v52, v56, v57
	s_waitcnt vmcnt(2)
	v_cvt_pk_f16_f32 v37, v34, v35
	v_mfma_f32_32x32x16_f16 v[0:15], v[48:51], v[52:55], v[0:15]
	v_perm_b32 v48, v240, v142, s42
	v_perm_b32 v49, v240, v142, s43
	v_perm_b32 v50, v240, v143, s42
	v_perm_b32 v51, v240, v143, s43
	v_pk_add_f16 v48, v48, s3 op_sel_hi:[1,0]
	v_pk_add_f16 v49, v49, s3 op_sel_hi:[1,0]
	v_pk_add_f16 v50, v50, s3 op_sel_hi:[1,0]
	v_pk_add_f16 v51, v51, s3 op_sel_hi:[1,0]
	v_cvt_pk_f16_f32 v36, v32, v33
	s_waitcnt vmcnt(1)
	v_mfma_f32_32x32x16_f16 v[16:31], v[48:51], v[52:55], v[16:31]
	v_lshrrev_b32_e32 v51, 16, v133
	v_lshrrev_b32_e32 v52, 8, v133
	v_perm_b32 v51, v52, v51, s2
	v_perm_b32 v48, v240, v132, s42
	v_perm_b32 v49, v240, v132, s43
	v_perm_b32 v50, v240, v133, s42
	v_or_b32_e32 v51, 0x64006400, v51
	v_pk_add_f16 v48, v48, s3 op_sel_hi:[1,0]
	v_pk_add_f16 v49, v49, s3 op_sel_hi:[1,0]
	v_pk_add_f16 v50, v50, s3 op_sel_hi:[1,0]
	v_pk_add_f16 v51, v51, s3 op_sel_hi:[1,0]
	s_nop 1
	v_mfma_f32_32x32x16_f16 v[0:15], v[48:51], v[36:39], v[0:15]
	v_perm_b32 v32, v240, v140, s42
	v_perm_b32 v33, v240, v140, s43
	v_perm_b32 v34, v240, v141, s42
	v_perm_b32 v35, v240, v141, s43
	v_pk_add_f16 v32, v32, s3 op_sel_hi:[1,0]
	v_pk_add_f16 v33, v33, s3 op_sel_hi:[1,0]
	v_pk_add_f16 v34, v34, s3 op_sel_hi:[1,0]
	v_pk_add_f16 v35, v35, s3 op_sel_hi:[1,0]
	v_mul_f32_e32 v74, v230, v230
	v_fmac_f32_e32 v74, v229, v229
	v_mfma_f32_32x32x16_f16 v[16:31], v[32:35], v[36:39], v[16:31]
	v_perm_b32 v32, v240, v130, s42
	v_perm_b32 v33, v240, v130, s43
	v_perm_b32 v34, v240, v131, s42
	v_perm_b32 v35, v240, v131, s43
	v_pk_add_f16 v32, v32, s3 op_sel_hi:[1,0]
	v_pk_add_f16 v33, v33, s3 op_sel_hi:[1,0]
	v_pk_add_f16 v34, v34, s3 op_sel_hi:[1,0]
	v_pk_add_f16 v35, v35, s3 op_sel_hi:[1,0]
	v_cvt_pk_f16_f32 v39, v46, v47
	v_cvt_pk_f16_f32 v38, v44, v45
	v_cvt_pk_f16_f32 v37, v42, v43
	v_cvt_pk_f16_f32 v36, v40, v41
	s_waitcnt vmcnt(0)
	v_mul_f32_e32 v76, v232, v232
	v_mfma_f32_32x32x16_f16 v[0:15], v[32:35], v[36:39], v[0:15]
	v_perm_b32 v32, v240, v64, s42
	v_perm_b32 v33, v240, v64, s43
	v_perm_b32 v34, v240, v65, s42
	v_perm_b32 v35, v240, v65, s43
	v_pk_add_f16 v32, v32, s3 op_sel_hi:[1,0]
	v_pk_add_f16 v33, v33, s3 op_sel_hi:[1,0]
	v_pk_add_f16 v34, v34, s3 op_sel_hi:[1,0]
	v_pk_add_f16 v35, v35, s3 op_sel_hi:[1,0]
	s_nop 3
	v_add_f32_e32 v0, v157, v0
	v_add_f32_e32 v74, v74, v79
	v_mfma_f32_32x32x16_f16 v[16:31], v[32:35], v[36:39], v[16:31]
	v_cvt_f16_f32_e32 v33, v0
	v_add_f32_e32 v75, v231, v232
	v_fmac_f32_e32 v76, v231, v231
	v_add_f32_e32 v75, v75, v78
	ds_write_b16 v158, v33 offset:18432
	v_add_f32_e32 v74, v76, v74
	v_add_f32_e32 v76, v233, v234
	s_nop 4
	v_add_f32_e32 v16, v157, v16
	v_add_f32_e32 v32, v0, v16
	v_cvt_f16_f32_e32 v34, v16
	v_mul_f32_e32 v16, v16, v16
	v_fmac_f32_e32 v16, v0, v0
	v_add_f32_e32 v0, v157, v1
	v_add_f32_e32 v1, v157, v17
	v_add_f32_e32 v32, 0, v32
	v_add_f32_e32 v17, v0, v1
	v_add_f32_e32 v17, v17, v32
	v_mul_f32_e32 v32, v1, v1
	v_cvt_f16_f32_e32 v1, v1
	v_fmac_f32_e32 v32, v0, v0
	v_cvt_f16_f32_e32 v33, v0
	v_add_f32_e32 v0, v16, v32
	ds_write_b16 v158, v1 offset:23184
	v_add_f32_e32 v1, v157, v2
	v_add_f32_e32 v2, v157, v18
	v_add_f32_e32 v16, v1, v2
	v_add_f32_e32 v16, v16, v17
	v_mul_f32_e32 v17, v2, v2
	v_cvt_f16_f32_e32 v2, v2
	v_cvt_f16_f32_e32 v18, v1
	v_fmac_f32_e32 v17, v1, v1
	v_add_f32_e32 v1, v157, v3
	ds_write_b16 v158, v2 offset:23328
	v_add_f32_e32 v2, v157, v19
	v_add_f32_e32 v3, v1, v2
	v_add_f32_e32 v3, v3, v16
	v_mul_f32_e32 v16, v2, v2
	v_cvt_f16_f32_e32 v2, v2
	v_add_f32_e32 v0, v17, v0
	v_cvt_f16_f32_e32 v17, v1
	v_fmac_f32_e32 v16, v1, v1
	ds_write_b16 v158, v2 offset:23472
	v_add_f32_e32 v1, v157, v4
	v_add_f32_e32 v2, v157, v20
	v_add_f32_e32 v4, v1, v2
	v_add_f32_e32 v3, v4, v3
	v_mul_f32_e32 v4, v2, v2
	v_cvt_f16_f32_e32 v2, v2
	v_add_f32_e32 v0, v16, v0
	v_cvt_f16_f32_e32 v16, v1
	v_fmac_f32_e32 v4, v1, v1
	ds_write_b16 v158, v2 offset:24192
	v_add_f32_e32 v1, v157, v5
	v_add_f32_e32 v2, v157, v21
	v_add_f32_e32 v0, v4, v0
	v_add_f32_e32 v4, v1, v2
	v_add_f32_e32 v3, v4, v3
	v_mul_f32_e32 v4, v2, v2
	v_cvt_f16_f32_e32 v2, v2
	v_cvt_f16_f32_e32 v5, v1
	v_fmac_f32_e32 v4, v1, v1
	v_add_f32_e32 v1, v157, v6
	ds_write_b16 v158, v2 offset:24336
	v_add_f32_e32 v2, v157, v22
	v_add_f32_e32 v0, v4, v0
	v_add_f32_e32 v4, v1, v2
	v_add_f32_e32 v3, v4, v3
	v_mul_f32_e32 v4, v2, v2
	v_cvt_f16_f32_e32 v2, v2
	ds_write_b16 v158, v5 offset:19728
	v_cvt_f16_f32_e32 v5, v1
	v_fmac_f32_e32 v4, v1, v1
	ds_write_b16 v158, v2 offset:24480
	v_add_f32_e32 v1, v157, v7
	v_add_f32_e32 v2, v157, v23
	v_add_f32_e32 v0, v4, v0
	v_add_f32_e32 v4, v1, v2
	v_add_f32_e32 v3, v4, v3
	v_mul_f32_e32 v4, v2, v2
	v_cvt_f16_f32_e32 v2, v2
	ds_write_b16 v158, v5 offset:19872
	v_cvt_f16_f32_e32 v5, v1
	v_fmac_f32_e32 v4, v1, v1
	ds_write_b16 v158, v2 offset:24624
	v_add_f32_e32 v1, v157, v8
	v_add_f32_e32 v2, v157, v24
	v_add_f32_e32 v0, v4, v0
	v_add_f32_e32 v4, v1, v2
	v_add_f32_e32 v3, v4, v3
	v_mul_f32_e32 v4, v2, v2
	v_cvt_f16_f32_e32 v2, v2
	ds_write_b16 v158, v5 offset:20016
	v_cvt_f16_f32_e32 v5, v1
	v_fmac_f32_e32 v4, v1, v1
	ds_write_b16 v158, v2 offset:25344
	v_add_f32_e32 v1, v157, v9
	v_add_f32_e32 v2, v157, v25
	v_add_f32_e32 v0, v4, v0
	v_add_f32_e32 v4, v1, v2
	v_add_f32_e32 v3, v4, v3
	v_mul_f32_e32 v4, v2, v2
	v_cvt_f16_f32_e32 v2, v2
	ds_write_b16 v158, v5 offset:20736
	v_cvt_f16_f32_e32 v5, v1
	v_fmac_f32_e32 v4, v1, v1
	ds_write_b16 v158, v2 offset:25488
	v_add_f32_e32 v1, v157, v10
	v_add_f32_e32 v2, v157, v26
	v_add_f32_e32 v0, v4, v0
	v_add_f32_e32 v4, v1, v2
	v_add_f32_e32 v3, v4, v3
	v_mul_f32_e32 v4, v2, v2
	v_cvt_f16_f32_e32 v2, v2
	ds_write_b16 v158, v5 offset:20880
	v_cvt_f16_f32_e32 v5, v1
	v_fmac_f32_e32 v4, v1, v1
	ds_write_b16 v158, v2 offset:25632
	v_add_f32_e32 v1, v157, v11
	v_add_f32_e32 v2, v157, v27
	v_add_f32_e32 v0, v4, v0
	v_add_f32_e32 v4, v1, v2
	v_add_f32_e32 v3, v4, v3
	v_mul_f32_e32 v4, v2, v2
	v_cvt_f16_f32_e32 v2, v2
	ds_write_b16 v158, v5 offset:21024
	v_cvt_f16_f32_e32 v5, v1
	v_fmac_f32_e32 v4, v1, v1
	ds_write_b16 v158, v2 offset:25776
	v_add_f32_e32 v1, v157, v12
	v_add_f32_e32 v2, v157, v28
	v_add_f32_e32 v0, v4, v0
	v_add_f32_e32 v4, v1, v2
	v_add_f32_e32 v3, v4, v3
	v_mul_f32_e32 v4, v2, v2
	v_cvt_f16_f32_e32 v2, v2
	ds_write_b16 v158, v5 offset:21168
	v_cvt_f16_f32_e32 v5, v1
	v_fmac_f32_e32 v4, v1, v1
	ds_write_b16 v158, v2 offset:26496
	v_add_f32_e32 v1, v157, v13
	v_add_f32_e32 v2, v157, v29
	v_add_f32_e32 v0, v4, v0
	v_add_f32_e32 v4, v1, v2
	v_add_f32_e32 v3, v4, v3
	v_mul_f32_e32 v4, v2, v2
	v_cvt_f16_f32_e32 v2, v2
	ds_write_b16 v158, v5 offset:21888
	v_cvt_f16_f32_e32 v5, v1
	v_fmac_f32_e32 v4, v1, v1
	ds_write_b16 v158, v2 offset:26640
	v_add_f32_e32 v1, v157, v14
	v_add_f32_e32 v2, v157, v30
	v_add_f32_e32 v0, v4, v0
	v_add_f32_e32 v4, v1, v2
	v_add_f32_e32 v3, v4, v3
	v_cvt_f16_f32_e32 v4, v1
	v_add_f32_e32 v75, v76, v75
	v_mul_f32_e32 v76, v234, v234
	ds_write_b16 v158, v5 offset:22032
	v_mul_f32_e32 v5, v2, v2
	v_fmac_f32_e32 v76, v233, v233
	v_mul_f32_e32 v67, v236, v236
	v_fmac_f32_e32 v5, v1, v1
	v_add_f32_e32 v74, v76, v74
	v_fmac_f32_e32 v67, v235, v235
	v_mul_f32_e32 v57, v238, v238
	v_add_f32_e32 v0, v5, v0
	v_cvt_f16_f32_e32 v5, v2
	v_add_f32_e32 v1, v157, v15
	v_add_f32_e32 v2, v157, v31
	v_add_f32_e32 v76, v235, v236
	v_add_f32_e32 v67, v67, v74
	v_fmac_f32_e32 v57, v237, v237
	v_mul_f32_e32 v50, v145, v145
	ds_write_b16 v158, v4 offset:22176
	v_add_f32_e32 v4, v1, v2
	v_add_f32_e32 v66, v76, v75
	v_add_f32_e32 v56, v237, v238
	v_add_f32_e32 v48, v57, v67
	v_fmac_f32_e32 v50, v144, v144
	v_add_f32_e32 v3, v4, v3
	v_mul_f32_e32 v4, v2, v2
	v_add_f32_e32 v56, v56, v66
	v_add_f32_e32 v49, v144, v145
	v_add_f32_e32 v40, v50, v48
	v_fmac_f32_e32 v4, v1, v1
	v_add_f32_e32 v49, v49, v56
	v_add_f32_e32 v40, v98, v40
	v_add_f32_e32 v4, v4, v0
	v_add_f32_e32 v41, v99, v49
	v_cvt_f16_f32_e32 v6, v1
	v_add_f32_e32 v1, v40, v4
	v_lshlrev_b32_e32 v4, 2, v156
	v_add_f32_e32 v0, v41, v3
	v_xor_b32_e32 v3, 0x80, v4
	v_cvt_f16_f32_e32 v7, v2
	ds_bpermute_b32 v2, v3, v0
	ds_bpermute_b32 v3, v3, v1
	ds_write_b16 v158, v34 offset:23040
	ds_write_b16 v158, v33 offset:18576
	ds_write_b16 v158, v18 offset:18720
	ds_write_b16 v158, v17 offset:18864
	ds_write_b16 v158, v16 offset:19584
	ds_write_b16 v158, v5 offset:26784
	ds_write_b16 v158, v6 offset:22320
	ds_write_b16 v158, v7 offset:26928
	s_and_saveexec_b64 s[0:1], vcc
	s_cbranch_execz .LBB3_26
	s_lshl_b32 s2, s13, 5
	v_lshl_add_u32 v4, s2, 2, v4
	v_or_b32_e32 v5, 0x1e400, v4
	s_waitcnt lgkmcnt(9)
	v_add_f32_e32 v0, v0, v2
	v_add_u32_e32 v4, 0x1e500, v4
	s_waitcnt lgkmcnt(8)
	v_add_f32_e32 v1, v1, v3
	ds_add_f32 v5, v0
	ds_add_f32 v4, v1

	.amdhsa_kernel _Z7k_layerILi0EEvPKDF16_S1_PKfS3_S3_S3_S3_S3_S1_S1_S1_S1_S3_S3_PKhS5_PDF16_S6_PfS7_
		.amdhsa_group_segment_fixed_size 126720
		.amdhsa_private_segment_fixed_size 0
		.amdhsa_kernarg_size 160
		.amdhsa_user_sgpr_count 2
		.amdhsa_user_sgpr_dispatch_ptr 0
		.amdhsa_user_sgpr_queue_ptr 0
		.amdhsa_user_sgpr_kernarg_segment_ptr 1
		.amdhsa_user_sgpr_dispatch_id 0
		.amdhsa_user_sgpr_kernarg_preload_length 0
		.amdhsa_user_sgpr_kernarg_preload_offset 0
		.amdhsa_user_sgpr_private_segment_size 0
		.amdhsa_uses_dynamic_stack 0
		.amdhsa_enable_private_segment 0
		.amdhsa_system_sgpr_workgroup_id_x 1
		.amdhsa_system_sgpr_workgroup_id_y 0
		.amdhsa_system_sgpr_workgroup_id_z 0
		.amdhsa_system_sgpr_workgroup_info 0
		.amdhsa_system_vgpr_workitem_id 0
		.amdhsa_next_free_vgpr 248
		.amdhsa_next_free_sgpr 96
		.amdhsa_accum_offset 248
		.amdhsa_reserve_vcc 1
		.amdhsa_float_round_mode_32 0
		.amdhsa_float_round_mode_16_64 0
		.amdhsa_float_denorm_mode_32 3
		.amdhsa_float_denorm_mode_16_64 3
		.amdhsa_dx10_clamp 1
		.amdhsa_ieee_mode 1
		.amdhsa_fp16_overflow 0
		.amdhsa_tg_split 0
		.amdhsa_exception_fp_ieee_invalid_op 0
		.amdhsa_exception_fp_denorm_src 0
		.amdhsa_exception_fp_ieee_div_zero 0
		.amdhsa_exception_fp_ieee_overflow 0
		.amdhsa_exception_fp_ieee_underflow 0
		.amdhsa_exception_fp_ieee_inexact 0
		.amdhsa_exception_int_div_zero 0
	.end_amdhsa_kernel

amdhsa.kernels:
  - .agpr_count:     32
    .args:
      - .actual_access:  read_only
        .address_space:  global
        .offset:         0
        .size:           8
        .value_kind:     global_buffer
      - .actual_access:  read_only
        .address_space:  global
        .offset:         8
        .size:           8
        .value_kind:     global_buffer
      - .actual_access:  read_only
        .address_space:  global
        .offset:         16
        .size:           8
        .value_kind:     global_buffer
      - .actual_access:  write_only
        .address_space:  global
        .offset:         24
        .size:           8
        .value_kind:     global_buffer
      - .actual_access:  read_only
        .address_space:  global
        .offset:         32
        .size:           8
        .value_kind:     global_buffer
      - .actual_access:  read_only
        .address_space:  global
        .offset:         40
        .size:           8
        .value_kind:     global_buffer
      - .actual_access:  read_only
        .address_space:  global
        .offset:         48
        .size:           8
        .value_kind:     global_buffer
      - .actual_access:  read_only
        .address_space:  global
        .offset:         56
        .size:           8
        .value_kind:     global_buffer
      - .actual_access:  read_only
        .address_space:  global
        .offset:         64
        .size:           8
        .value_kind:     global_buffer
      - .actual_access:  read_only
        .address_space:  global
        .offset:         72
        .size:           8
        .value_kind:     global_buffer
      - .actual_access:  read_only
        .address_space:  global
        .offset:         80
        .size:           8
        .value_kind:     global_buffer
      - .actual_access:  write_only
        .address_space:  global
        .offset:         88
        .size:           8
        .value_kind:     global_buffer
      - .actual_access:  write_only
        .address_space:  global
        .offset:         96
        .size:           8
        .value_kind:     global_buffer
      - .actual_access:  write_only
        .address_space:  global
        .offset:         104
        .size:           8
        .value_kind:     global_buffer
      - .actual_access:  write_only
        .address_space:  global
        .offset:         112
        .size:           8
        .value_kind:     global_buffer
      - .actual_access:  write_only
        .address_space:  global
        .offset:         120
        .size:           8
        .value_kind:     global_buffer
    .group_segment_fixed_size: 17408
    .kernarg_segment_align: 8
    .kernarg_segment_size: 128
    .language:       OpenCL C
    .language_version:
      - 2
      - 0
    .max_flat_workgroup_size: 256
    .name:           _Z9k_encprepPKfS0_S0_PDF16_PKiS3_S0_S0_S0_S0_S0_PhS4_S1_S1_Pf
    .private_segment_fixed_size: 0
    .sgpr_count:     22
    .sgpr_spill_count: 0
    .symbol:         _Z9k_encprepPKfS0_S0_PDF16_PKiS3_S0_S0_S0_S0_S0_PhS4_S1_S1_Pf.kd
    .uniform_work_group_size: 1
    .uses_dynamic_stack: false
    .vgpr_count:     128
    .vgpr_spill_count: 0
    .wavefront_size: 64
  - .agpr_count:     0
    .args:
      - .actual_access:  read_only
        .address_space:  global
        .offset:         0
        .size:           8
        .value_kind:     global_buffer
      - .actual_access:  read_only
        .address_space:  global
        .offset:         8
        .size:           8
        .value_kind:     global_buffer
      - .actual_access:  read_only
        .address_space:  global
        .offset:         16
        .size:           8
        .value_kind:     global_buffer
      - .actual_access:  read_only
        .address_space:  global
        .offset:         24
        .size:           8
        .value_kind:     global_buffer
      - .actual_access:  read_only
        .address_space:  global
        .offset:         32
        .size:           8
        .value_kind:     global_buffer
      - .actual_access:  read_only
        .address_space:  global
        .offset:         40
        .size:           8
        .value_kind:     global_buffer
      - .actual_access:  read_only
        .address_space:  global
        .offset:         48
        .size:           8
        .value_kind:     global_buffer
      - .actual_access:  read_only
        .address_space:  global
        .offset:         56
        .size:           8
        .value_kind:     global_buffer
      - .actual_access:  read_only
        .address_space:  global
        .offset:         64
        .size:           8
        .value_kind:     global_buffer
      - .actual_access:  read_only
        .address_space:  global
        .offset:         72
        .size:           8
        .value_kind:     global_buffer
      - .actual_access:  read_only
        .address_space:  global
        .offset:         80
        .size:           8
        .value_kind:     global_buffer
      - .actual_access:  read_only
        .address_space:  global
        .offset:         88
        .size:           8
        .value_kind:     global_buffer
      - .actual_access:  write_only
        .address_space:  global
        .offset:         96
        .size:           8
        .value_kind:     global_buffer
    .group_segment_fixed_size: 40448
    .kernarg_segment_align: 8
    .kernarg_segment_size: 104
    .language:       OpenCL C
    .language_version:
      - 2
      - 0
    .max_flat_workgroup_size: 1024
    .name:           _Z7k_finalPKDF16_S0_PKfS2_S2_S2_S2_S2_S0_S2_S2_S2_Pf
    .private_segment_fixed_size: 0
    .sgpr_count:     24
    .sgpr_spill_count: 0
    .symbol:         _Z7k_finalPKDF16_S0_PKfS2_S2_S2_S2_S2_S0_S2_S2_S2_Pf.kd
    .uniform_work_group_size: 1
    .uses_dynamic_stack: false
    .vgpr_count:     99
    .vgpr_spill_count: 0
    .wavefront_size: 64
  - .agpr_count:     0
    .args:
      - .actual_access:  read_only
        .address_space:  global
        .offset:         0
        .size:           8
        .value_kind:     global_buffer
      - .actual_access:  read_only
        .address_space:  global
        .offset:         8
        .size:           8
        .value_kind:     global_buffer
      - .actual_access:  read_only
        .address_space:  global
        .offset:         16
        .size:           8
        .value_kind:     global_buffer
      - .actual_access:  read_only
        .address_space:  global
        .offset:         24
        .size:           8
        .value_kind:     global_buffer
      - .actual_access:  read_only
        .address_space:  global
        .offset:         32
        .size:           8
        .value_kind:     global_buffer
      - .actual_access:  read_only
        .address_space:  global
        .offset:         40
        .size:           8
        .value_kind:     global_buffer
      - .actual_access:  read_only
        .address_space:  global
        .offset:         48
        .size:           8
        .value_kind:     global_buffer
      - .actual_access:  read_only
        .address_space:  global
        .offset:         56
        .size:           8
        .value_kind:     global_buffer
      - .actual_access:  read_only
        .address_space:  global
        .offset:         64
        .size:           8
        .value_kind:     global_buffer
      - .actual_access:  read_only
        .address_space:  global
        .offset:         72
        .size:           8
        .value_kind:     global_buffer
      - .actual_access:  read_only
        .address_space:  global
        .offset:         80
        .size:           8
        .value_kind:     global_buffer
      - .actual_access:  read_only
        .address_space:  global
        .offset:         88
        .size:           8
        .value_kind:     global_buffer
      - .actual_access:  read_only
        .address_space:  global
        .offset:         96
        .size:           8
        .value_kind:     global_buffer
      - .actual_access:  read_only
        .address_space:  global
        .offset:         104
        .size:           8
        .value_kind:     global_buffer
      - .actual_access:  read_only
        .address_space:  global
        .offset:         112
        .size:           8
        .value_kind:     global_buffer
      - .actual_access:  read_only
        .address_space:  global
        .offset:         120
        .size:           8
        .value_kind:     global_buffer
      - .actual_access:  write_only
        .address_space:  global
        .offset:         128
        .size:           8
        .value_kind:     global_buffer
      - .actual_access:  write_only
        .address_space:  global
        .offset:         136
        .size:           8
        .value_kind:     global_buffer
      - .address_space:  global
        .offset:         144
        .size:           8
        .value_kind:     global_buffer
      - .address_space:  global
        .offset:         152
        .size:           8
        .value_kind:     global_buffer
    .group_segment_fixed_size: 126720
    .kernarg_segment_align: 8
    .kernarg_segment_size: 160
    .language:       OpenCL C
    .language_version:
      - 2
      - 0
    .max_flat_workgroup_size: 512
    .name:           _Z7k_layerILi1EEvPKDF16_S1_PKfS3_S3_S3_S3_S3_S1_S1_S1_S1_S3_S3_PKhS5_PDF16_S6_PfS7_
    .private_segment_fixed_size: 0
    .sgpr_count:     50
    .sgpr_spill_count: 0
    .symbol:         _Z7k_layerILi1EEvPKDF16_S1_PKfS3_S3_S3_S3_S3_S1_S1_S1_S1_S3_S3_PKhS5_PDF16_S6_PfS7_.kd
    .uniform_work_group_size: 1
    .uses_dynamic_stack: false
    .vgpr_count:     248
    .vgpr_spill_count: 0
    .wavefront_size: 64
  - .agpr_count:     0
    .args:
      - .actual_access:  read_only
        .address_space:  global
        .offset:         0
        .size:           8
        .value_kind:     global_buffer
      - .actual_access:  read_only
        .address_space:  global
        .offset:         8
        .size:           8
        .value_kind:     global_buffer
      - .actual_access:  read_only
        .address_space:  global
        .offset:         16
        .size:           8
        .value_kind:     global_buffer
      - .actual_access:  read_only
        .address_space:  global
        .offset:         24
        .size:           8
        .value_kind:     global_buffer
      - .actual_access:  read_only
        .address_space:  global
        .offset:         32
        .size:           8
        .value_kind:     global_buffer
      - .actual_access:  read_only
        .address_space:  global
        .offset:         40
        .size:           8
        .value_kind:     global_buffer
      - .actual_access:  read_only
        .address_space:  global
        .offset:         48
        .size:           8
        .value_kind:     global_buffer
      - .actual_access:  read_only
        .address_space:  global
        .offset:         56
        .size:           8
        .value_kind:     global_buffer
      - .actual_access:  read_only
        .address_space:  global
        .offset:         64
        .size:           8
        .value_kind:     global_buffer
      - .actual_access:  read_only
        .address_space:  global
        .offset:         72
        .size:           8
        .value_kind:     global_buffer
      - .actual_access:  read_only
        .address_space:  global
        .offset:         80
        .size:           8
        .value_kind:     global_buffer
      - .actual_access:  read_only
        .address_space:  global
        .offset:         88
        .size:           8
        .value_kind:     global_buffer
      - .actual_access:  read_only
        .address_space:  global
        .offset:         96
        .size:           8
        .value_kind:     global_buffer
      - .actual_access:  read_only
        .address_space:  global
        .offset:         104
        .size:           8
        .value_kind:     global_buffer
      - .actual_access:  read_only
        .address_space:  global
        .offset:         112
        .size:           8
        .value_kind:     global_buffer
      - .actual_access:  read_only
        .address_space:  global
        .offset:         120
        .size:           8
        .value_kind:     global_buffer
      - .actual_access:  write_only
        .address_space:  global
        .offset:         128
        .size:           8
        .value_kind:     global_buffer
      - .actual_access:  write_only
        .address_space:  global
        .offset:         136
        .size:           8
        .value_kind:     global_buffer
      - .address_space:  global
        .offset:         144
        .size:           8
        .value_kind:     global_buffer
      - .address_space:  global
        .offset:         152
        .size:           8
        .value_kind:     global_buffer
    .group_segment_fixed_size: 126720
    .kernarg_segment_align: 8
    .kernarg_segment_size: 160
    .language:       OpenCL C
    .language_version:
      - 2
      - 0
    .max_flat_workgroup_size: 512
    .name:           _Z7k_layerILi0EEvPKDF16_S1_PKfS3_S3_S3_S3_S3_S1_S1_S1_S1_S3_S3_PKhS5_PDF16_S6_PfS7_
    .private_segment_fixed_size: 0
    .sgpr_count:     50
    .sgpr_spill_count: 0
    .symbol:         _Z7k_layerILi0EEvPKDF16_S1_PKfS3_S3_S3_S3_S3_S1_S1_S1_S1_S3_S3_PKhS5_PDF16_S6_PfS7_.kd
    .uniform_work_group_size: 1
    .uses_dynamic_stack: false
    .vgpr_count:     248
    .vgpr_spill_count: 0
    .wavefront_size: 64
